# v47 with the converted fp8 expert weights stored with the default cache policy instead of nt
# baseline (speedup 1.0000x reference)
; #define LAS __attribute__((address_space(3)))
; __device__ __forceinline__ float clamp8(float x) { return __builtin_amdgcn_fmed3f(x, -448.f, 448.f); }
; #define LDS_WAIT() asm volatile("s_waitcnt lgkmcnt(0)" ::: "memory")
; __device__ __forceinline__ void cvt_load(const CvtDesc& d, float (&t)[64], int lane) {
;     const float* p = d.src + (size_t)(lane >> 4) * d.N + 4 * (lane & 15);
; #pragma unroll
;     for (int i = 0; i < 16; ++i) { const f32x4 v = __builtin_nontemporal_load((const f32x4*)(p + (size_t)(4 * i) * d.N));
;         t[4 * i] = v.x; t[4 * i + 1] = v.y; t[4 * i + 2] = v.z; t[4 * i + 3] = v.w; }
; }
; __device__ __forceinline__ void cvt_finish(const CvtDesc& d, const float (&t)[64], LAS float* scr, int lane) {
;     LAS float* sw = scr + (lane >> 4) * 65 + 4 * (lane & 15);
; #pragma unroll
;     for (int i = 0; i < 16; ++i) { sw[(4 * i) * 65] = t[4 * i]; sw[(4 * i) * 65 + 1] = t[4 * i + 1]; sw[(4 * i) * 65 + 2] = t[4 * i + 2]; sw[(4 * i) * 65 + 3] = t[4 * i + 3]; }
;     LDS_WAIT();
;     const int c = lane & 7;
;     if (d.f8) {
; #pragma unroll
;         for (int j = 0; j < 8; ++j) { const int n = (lane >> 3) + 8 * j; const LAS float* s = scr + (8 * c) * 65 + n;
;             int a = __builtin_amdgcn_cvt_pk_fp8_f32(clamp8(s[0 * 65] * W8_SCALE), clamp8(s[1 * 65] * W8_SCALE), 0, false); a = __builtin_amdgcn_cvt_pk_fp8_f32(clamp8(s[2 * 65] * W8_SCALE), clamp8(s[3 * 65] * W8_SCALE), a, true);
;             int b = __builtin_amdgcn_cvt_pk_fp8_f32(clamp8(s[4 * 65] * W8_SCALE), clamp8(s[5 * 65] * W8_SCALE), 0, false); b = __builtin_amdgcn_cvt_pk_fp8_f32(clamp8(s[6 * 65] * W8_SCALE), clamp8(s[7 * 65] * W8_SCALE), b, true);
;             __builtin_nontemporal_store((u32x2){(unsigned)a, (unsigned)b}, (u32x2*)(d.dst + (size_t)n * d.dKB + 8 * c)); }
.LBB0_174:
	v_mul_u32_u24_e32 v0, s16, v8
	v_lshlrev_b32_e32 v0, 2, v0
	v_lshl_add_u64 v[6:7], v[6:7], 0, v[0:1]
	v_mov_b32_e32 v5, v1
	v_lshl_add_u64 v[6:7], v[6:7], 0, v[4:5]
	global_load_dwordx4 v[42:45], v[6:7], off nt
	s_lshl_b32 s8, s16, 4
	v_lshl_add_u64 v[6:7], v[6:7], 0, s[8:9]
	global_load_dwordx4 v[46:49], v[6:7], off nt
	v_lshl_add_u64 v[6:7], v[6:7], 0, s[8:9]
	global_load_dwordx4 v[50:53], v[6:7], off nt
	v_lshl_add_u64 v[6:7], v[6:7], 0, s[8:9]
	global_load_dwordx4 v[54:57], v[6:7], off nt
	v_lshl_add_u64 v[6:7], v[6:7], 0, s[8:9]
	global_load_dwordx4 v[58:61], v[6:7], off nt
	v_lshl_add_u64 v[6:7], v[6:7], 0, s[8:9]
	global_load_dwordx4 v[62:65], v[6:7], off nt
	v_lshl_add_u64 v[6:7], v[6:7], 0, s[8:9]
	global_load_dwordx4 v[66:69], v[6:7], off nt
	v_lshl_add_u64 v[6:7], v[6:7], 0, s[8:9]
	global_load_dwordx4 v[70:73], v[6:7], off nt
	v_lshl_add_u64 v[6:7], v[6:7], 0, s[8:9]
	global_load_dwordx4 v[74:77], v[6:7], off nt
	v_lshl_add_u64 v[6:7], v[6:7], 0, s[8:9]
	global_load_dwordx4 v[78:81], v[6:7], off nt
	v_lshl_add_u64 v[6:7], v[6:7], 0, s[8:9]
	global_load_dwordx4 v[82:85], v[6:7], off nt
	v_lshl_add_u64 v[6:7], v[6:7], 0, s[8:9]
	global_load_dwordx4 v[86:89], v[6:7], off nt
	v_lshl_add_u64 v[6:7], v[6:7], 0, s[8:9]
	global_load_dwordx4 v[90:93], v[6:7], off nt
	v_lshl_add_u64 v[6:7], v[6:7], 0, s[8:9]
	global_load_dwordx4 v[94:97], v[6:7], off nt
	v_lshl_add_u64 v[6:7], v[6:7], 0, s[8:9]
	global_load_dwordx4 v[98:101], v[6:7], off nt
	v_lshl_add_u64 v[6:7], v[6:7], 0, s[8:9]
	global_load_dwordx4 v[102:105], v[6:7], off nt
	v_add_u32_e32 v0, 0x28a0, v9
	v_add_u32_e32 v5, 0x28a8, v9
	v_add_u32_e32 v6, 0x2cb0, v9
	v_add_u32_e32 v7, 0x2cb8, v9
	v_add_u32_e32 v41, 0x30c0, v9
	v_add_u32_e32 v108, 0x30c8, v9
	v_add_u32_e32 v109, 0x34d0, v9
	v_add_u32_e32 v110, 0x34d8, v9
	v_add_u32_e32 v111, 0x38e0, v9
	v_add_u32_e32 v112, 0x38e8, v9
	v_add_u32_e32 v113, 0x3cf0, v9
	v_add_u32_e32 v114, 0x3cf8, v9
	v_add_u32_e32 v115, 0x400, v11
	v_mov_b32_e32 v107, v1
	v_mov_b32_e32 v106, v1
	s_waitcnt vmcnt(0)
	ds_write2_b32 v9, v42, v43 offset1:1
	ds_write2_b32 v9, v44, v45 offset0:2 offset1:3
	ds_write2_b32 v21, v46, v47 offset1:1
	ds_write2_b32 v22, v48, v49 offset1:1
	ds_write2_b32 v23, v50, v51 offset1:1
	ds_write2_b32 v24, v52, v53 offset1:1
	ds_write2_b32 v25, v54, v55 offset1:1
	ds_write2_b32 v26, v56, v57 offset1:1
	ds_write2_b32 v27, v58, v59 offset1:1
	ds_write2_b32 v28, v60, v61 offset1:1
	ds_write2_b32 v29, v62, v63 offset1:1
	ds_write2_b32 v30, v64, v65 offset1:1
	ds_write2_b32 v31, v66, v67 offset1:1
	ds_write2_b32 v32, v68, v69 offset1:1
	ds_write2_b32 v33, v70, v71 offset1:1
	ds_write2_b32 v34, v72, v73 offset1:1
	ds_write2_b32 v35, v74, v75 offset1:1
	ds_write2_b32 v36, v76, v77 offset1:1
	ds_write2_b32 v37, v78, v79 offset1:1
	ds_write2_b32 v38, v80, v81 offset1:1
	ds_write2_b32 v0, v82, v83 offset1:1
	ds_write2_b32 v5, v84, v85 offset1:1
	ds_write2_b32 v6, v86, v87 offset1:1
	ds_write2_b32 v7, v88, v89 offset1:1
	ds_write2_b32 v41, v90, v91 offset1:1
	ds_write2_b32 v108, v92, v93 offset1:1
	ds_write2_b32 v109, v94, v95 offset1:1
	ds_write2_b32 v110, v96, v97 offset1:1
	ds_write2_b32 v111, v98, v99 offset1:1
	ds_write2_b32 v112, v100, v101 offset1:1
	ds_write2_b32 v113, v102, v103 offset1:1
	ds_write2_b32 v114, v104, v105 offset1:1
	s_waitcnt lgkmcnt(0)
	ds_read2_b32 v[42:43], v11 offset1:8
	ds_read2_b32 v[44:45], v11 offset0:65 offset1:73
	ds_read2_b32 v[46:47], v11 offset0:130 offset1:138
	ds_read2_b32 v[48:49], v11 offset0:195 offset1:203
	ds_read2_b32 v[50:51], v115 offset0:4 offset1:12
	ds_read2_b32 v[52:53], v115 offset0:69 offset1:77
	ds_read2_b32 v[54:55], v115 offset0:134 offset1:142
	ds_read2_b32 v[56:57], v115 offset0:199 offset1:207
	s_waitcnt lgkmcnt(7)
	v_mul_f32_e32 v0, 0x42800000, v42
	s_waitcnt lgkmcnt(3)
	v_mul_f32_e32 v41, 0x42800000, v50
	s_waitcnt lgkmcnt(2)
	v_mul_f32_e32 v42, 0x42800000, v52
	v_med3_f32 v41, v41, s33, v39
	v_med3_f32 v42, v42, s33, v39
	v_cvt_pk_fp8_f32 v107, v41, v42
	v_mul_f32_e32 v5, 0x42800000, v44
	v_mul_f32_e32 v6, 0x42800000, v46
	s_waitcnt lgkmcnt(1)
	v_mul_f32_e32 v44, 0x42800000, v54
	s_waitcnt lgkmcnt(0)
	v_mul_f32_e32 v46, 0x42800000, v56
	v_med3_f32 v0, v0, s33, v39
	v_med3_f32 v5, v5, s33, v39
	v_cvt_pk_fp8_f32 v106, v0, v5
	v_med3_f32 v0, v44, s33, v39
	v_med3_f32 v5, v46, s33, v39
	v_cvt_pk_fp8_f32 v107, v0, v5 op_sel:[0,0,1]
	v_mul_f32_e32 v0, 0x42800000, v43
	v_mul_f32_e32 v5, 0x42800000, v45
	v_med3_f32 v0, v0, s33, v39
	v_med3_f32 v5, v5, s33, v39
	v_mov_b32_e32 v42, v1
	v_cvt_pk_fp8_f32 v42, v0, v5
	v_mul_f32_e32 v0, 0x42800000, v47
	v_mul_f32_e32 v5, 0x42800000, v49
	v_med3_f32 v0, v0, s33, v39
	v_med3_f32 v5, v5, s33, v39
	v_cvt_pk_fp8_f32 v42, v0, v5 op_sel:[0,0,1]
	v_mul_f32_e32 v0, 0x42800000, v51
	v_mul_f32_e32 v5, 0x42800000, v53
	v_med3_f32 v0, v0, s33, v39
	v_med3_f32 v5, v5, s33, v39
	v_mov_b32_e32 v43, v1
	v_cvt_pk_fp8_f32 v43, v0, v5
	v_mul_f32_e32 v7, 0x42800000, v48
	v_mul_f32_e32 v0, 0x42800000, v55
	v_mul_f32_e32 v5, 0x42800000, v57
	v_med3_f32 v6, v6, s33, v39
	v_med3_f32 v7, v7, s33, v39
	v_med3_f32 v0, v0, s33, v39
	v_med3_f32 v5, v5, s33, v39
	v_cvt_pk_fp8_f32 v106, v6, v7 op_sel:[0,0,1]
	v_cvt_pk_fp8_f32 v43, v0, v5 op_sel:[0,0,1]
	ds_read2_b32 v[44:45], v11 offset0:16 offset1:24
	ds_read2_b32 v[48:49], v11 offset0:81 offset1:89
	v_mov_b64_e32 v[6:7], s[14:15]
	v_mad_u64_u32 v[58:59], s[14:15], s12, v10, v[6:7]
	v_mad_u64_u32 v[46:47], s[14:15], s12, v12, v[6:7]
	v_lshl_add_u64 v[58:59], v[58:59], 0, v[2:3]
	v_lshl_add_u64 v[46:47], v[46:47], 0, v[2:3]
	global_store_dwordx2 v[58:59], v[106:107], off
	global_store_dwordx2 v[46:47], v[42:43], off
	ds_read2_b32 v[42:43], v11 offset0:146 offset1:154
	ds_read2_b32 v[50:51], v11 offset0:211 offset1:219
	s_waitcnt lgkmcnt(3)
; #define LAS __attribute__((address_space(3)))
; __device__ __forceinline__ float clamp8(float x) { return __builtin_amdgcn_fmed3f(x, -448.f, 448.f); }
; __device__ __forceinline__ void cvt_finish(const CvtDesc& d, const float (&t)[64], LAS float* scr, int lane) {
;     ...
;     if (d.f8) {
; #pragma unroll
;         for (int j = 0; j < 8; ++j) { const int n = (lane >> 3) + 8 * j; const LAS float* s = scr + (8 * c) * 65 + n;
;             int a = __builtin_amdgcn_cvt_pk_fp8_f32(clamp8(s[0 * 65] * W8_SCALE), clamp8(s[1 * 65] * W8_SCALE), 0, false); a = __builtin_amdgcn_cvt_pk_fp8_f32(clamp8(s[2 * 65] * W8_SCALE), clamp8(s[3 * 65] * W8_SCALE), a, true);
;             int b = __builtin_amdgcn_cvt_pk_fp8_f32(clamp8(s[4 * 65] * W8_SCALE), clamp8(s[5 * 65] * W8_SCALE), 0, false); b = __builtin_amdgcn_cvt_pk_fp8_f32(clamp8(s[6 * 65] * W8_SCALE), clamp8(s[7 * 65] * W8_SCALE), b, true);
;             __builtin_nontemporal_store((u32x2){(unsigned)a, (unsigned)b}, (u32x2*)(d.dst + (size_t)n * d.dKB + 8 * c)); }
	v_mul_f32_e32 v0, 0x42800000, v44
	s_waitcnt lgkmcnt(2)
	v_mul_f32_e32 v5, 0x42800000, v48
	v_med3_f32 v0, v0, s33, v39
	v_med3_f32 v5, v5, s33, v39
	v_mov_b32_e32 v46, v1
	ds_read2_b32 v[52:53], v115 offset0:20 offset1:28
	ds_read2_b32 v[54:55], v115 offset0:85 offset1:93
	v_cvt_pk_fp8_f32 v46, v0, v5
	s_waitcnt lgkmcnt(3)
	v_mul_f32_e32 v0, 0x42800000, v42
	s_waitcnt lgkmcnt(2)
	v_mul_f32_e32 v5, 0x42800000, v50
	v_med3_f32 v0, v0, s33, v39
	v_med3_f32 v5, v5, s33, v39
	ds_read2_b32 v[56:57], v115 offset0:150 offset1:158
	ds_read2_b32 v[58:59], v115 offset0:215 offset1:223
	v_cvt_pk_fp8_f32 v46, v0, v5 op_sel:[0,0,1]
	s_waitcnt lgkmcnt(3)
	v_mul_f32_e32 v0, 0x42800000, v52
	s_waitcnt lgkmcnt(2)
	v_mul_f32_e32 v5, 0x42800000, v54
	v_med3_f32 v0, v0, s33, v39
	v_med3_f32 v5, v5, s33, v39
	v_mov_b32_e32 v47, v1
	v_cvt_pk_fp8_f32 v47, v0, v5
	s_waitcnt lgkmcnt(1)
	v_mul_f32_e32 v0, 0x42800000, v56
	s_waitcnt lgkmcnt(0)
	v_mul_f32_e32 v5, 0x42800000, v58
	v_med3_f32 v0, v0, s33, v39
	v_med3_f32 v5, v5, s33, v39
	v_cvt_pk_fp8_f32 v47, v0, v5 op_sel:[0,0,1]
	v_mul_f32_e32 v0, 0x42800000, v45
	v_mul_f32_e32 v5, 0x42800000, v49
	v_med3_f32 v0, v0, s33, v39
	v_med3_f32 v5, v5, s33, v39
	v_mov_b32_e32 v42, v1
	v_cvt_pk_fp8_f32 v42, v0, v5
	v_mul_f32_e32 v0, 0x42800000, v43
	v_mul_f32_e32 v5, 0x42800000, v51
	v_med3_f32 v0, v0, s33, v39
	v_med3_f32 v5, v5, s33, v39
	v_cvt_pk_fp8_f32 v42, v0, v5 op_sel:[0,0,1]
	v_mul_f32_e32 v0, 0x42800000, v53
	v_mul_f32_e32 v5, 0x42800000, v55
	v_med3_f32 v0, v0, s33, v39
	v_med3_f32 v5, v5, s33, v39
	v_mov_b32_e32 v43, v1
	v_cvt_pk_fp8_f32 v43, v0, v5
	v_mul_f32_e32 v0, 0x42800000, v57
	v_mul_f32_e32 v5, 0x42800000, v59
	v_med3_f32 v0, v0, s33, v39
	v_med3_f32 v5, v5, s33, v39
	v_mad_u64_u32 v[60:61], s[14:15], s12, v13, v[6:7]
	v_cvt_pk_fp8_f32 v43, v0, v5 op_sel:[0,0,1]
	ds_read2_b32 v[44:45], v11 offset0:32 offset1:40
	ds_read2_b32 v[48:49], v11 offset0:97 offset1:105
	v_lshl_add_u64 v[60:61], v[60:61], 0, v[2:3]
	global_store_dwordx2 v[60:61], v[46:47], off
	v_mad_u64_u32 v[46:47], s[14:15], s12, v14, v[6:7]
	v_lshl_add_u64 v[46:47], v[46:47], 0, v[2:3]
	global_store_dwordx2 v[46:47], v[42:43], off
	ds_read2_b32 v[42:43], v11 offset0:162 offset1:170
	ds_read2_b32 v[50:51], v11 offset0:227 offset1:235
	s_waitcnt lgkmcnt(3)
	v_mul_f32_e32 v0, 0x42800000, v44
	s_waitcnt lgkmcnt(2)
	v_mul_f32_e32 v5, 0x42800000, v48
	v_med3_f32 v0, v0, s33, v39
	v_med3_f32 v5, v5, s33, v39
	v_mov_b32_e32 v46, v1
	ds_read2_b32 v[52:53], v115 offset0:36 offset1:44
	ds_read2_b32 v[54:55], v115 offset0:101 offset1:109
	v_cvt_pk_fp8_f32 v46, v0, v5
	s_waitcnt lgkmcnt(3)
	v_mul_f32_e32 v0, 0x42800000, v42
	s_waitcnt lgkmcnt(2)
	v_mul_f32_e32 v5, 0x42800000, v50
	v_med3_f32 v0, v0, s33, v39
	v_med3_f32 v5, v5, s33, v39
	ds_read2_b32 v[56:57], v115 offset0:166 offset1:174
	ds_read2_b32 v[58:59], v115 offset0:231 offset1:239
	v_cvt_pk_fp8_f32 v46, v0, v5 op_sel:[0,0,1]
	s_waitcnt lgkmcnt(3)
	v_mul_f32_e32 v0, 0x42800000, v52
	s_waitcnt lgkmcnt(2)
	v_mul_f32_e32 v5, 0x42800000, v54
	v_med3_f32 v0, v0, s33, v39
	v_med3_f32 v5, v5, s33, v39
	v_mov_b32_e32 v47, v1
	v_cvt_pk_fp8_f32 v47, v0, v5
	s_waitcnt lgkmcnt(1)
	v_mul_f32_e32 v0, 0x42800000, v56
	s_waitcnt lgkmcnt(0)
	v_mul_f32_e32 v5, 0x42800000, v58
	v_med3_f32 v0, v0, s33, v39
	v_med3_f32 v5, v5, s33, v39
	v_cvt_pk_fp8_f32 v47, v0, v5 op_sel:[0,0,1]
	v_mul_f32_e32 v0, 0x42800000, v45
	v_mul_f32_e32 v5, 0x42800000, v49
	v_med3_f32 v0, v0, s33, v39
	v_med3_f32 v5, v5, s33, v39
	v_mov_b32_e32 v42, v1
	v_cvt_pk_fp8_f32 v42, v0, v5
	v_mul_f32_e32 v0, 0x42800000, v43
	v_mul_f32_e32 v5, 0x42800000, v51
	v_med3_f32 v0, v0, s33, v39
	v_med3_f32 v5, v5, s33, v39
	v_cvt_pk_fp8_f32 v42, v0, v5 op_sel:[0,0,1]
	v_mul_f32_e32 v0, 0x42800000, v53
	v_mul_f32_e32 v5, 0x42800000, v55
	v_med3_f32 v0, v0, s33, v39
	v_med3_f32 v5, v5, s33, v39
	v_mov_b32_e32 v43, v1
	v_cvt_pk_fp8_f32 v43, v0, v5
	v_mul_f32_e32 v0, 0x42800000, v57
	v_mul_f32_e32 v5, 0x42800000, v59
	v_med3_f32 v0, v0, s33, v39
	v_med3_f32 v5, v5, s33, v39
	v_mad_u64_u32 v[60:61], s[14:15], s12, v15, v[6:7]
	v_cvt_pk_fp8_f32 v43, v0, v5 op_sel:[0,0,1]
	ds_read2_b32 v[44:45], v11 offset0:48 offset1:56
	ds_read2_b32 v[48:49], v11 offset0:113 offset1:121
	v_lshl_add_u64 v[60:61], v[60:61], 0, v[2:3]
	global_store_dwordx2 v[60:61], v[46:47], off
	v_mad_u64_u32 v[46:47], s[14:15], s12, v16, v[6:7]
	v_lshl_add_u64 v[46:47], v[46:47], 0, v[2:3]
	global_store_dwordx2 v[46:47], v[42:43], off
	ds_read2_b32 v[42:43], v11 offset0:178 offset1:186
	ds_read2_b32 v[50:51], v11 offset0:243 offset1:251
	s_waitcnt lgkmcnt(3)
	v_mul_f32_e32 v0, 0x42800000, v44
	s_waitcnt lgkmcnt(2)
	v_mul_f32_e32 v5, 0x42800000, v48
	v_med3_f32 v0, v0, s33, v39
	v_med3_f32 v5, v5, s33, v39
	v_mov_b32_e32 v46, v1
	ds_read2_b32 v[52:53], v115 offset0:52 offset1:60
	ds_read2_b32 v[54:55], v115 offset0:117 offset1:125
	v_cvt_pk_fp8_f32 v46, v0, v5
	s_waitcnt lgkmcnt(3)
	v_mul_f32_e32 v0, 0x42800000, v42
	s_waitcnt lgkmcnt(2)
	v_mul_f32_e32 v5, 0x42800000, v50
	v_med3_f32 v0, v0, s33, v39
	v_med3_f32 v5, v5, s33, v39
	ds_read2_b32 v[56:57], v115 offset0:182 offset1:190
	ds_read2_b32 v[58:59], v115 offset0:247 offset1:255
	v_cvt_pk_fp8_f32 v46, v0, v5 op_sel:[0,0,1]
	s_waitcnt lgkmcnt(3)
	v_mul_f32_e32 v0, 0x42800000, v52
	s_waitcnt lgkmcnt(2)
	v_mul_f32_e32 v5, 0x42800000, v54
	v_med3_f32 v0, v0, s33, v39
	v_med3_f32 v5, v5, s33, v39
	v_mov_b32_e32 v47, v1
	v_cvt_pk_fp8_f32 v47, v0, v5
	s_waitcnt lgkmcnt(1)
	v_mul_f32_e32 v0, 0x42800000, v56
	s_waitcnt lgkmcnt(0)
	v_mul_f32_e32 v5, 0x42800000, v58
	v_med3_f32 v0, v0, s33, v39
	v_med3_f32 v5, v5, s33, v39
	v_cvt_pk_fp8_f32 v47, v0, v5 op_sel:[0,0,1]
	v_mul_f32_e32 v0, 0x42800000, v45
	v_mul_f32_e32 v5, 0x42800000, v49
	v_med3_f32 v0, v0, s33, v39
	v_med3_f32 v5, v5, s33, v39
	v_mov_b32_e32 v42, v1
	v_cvt_pk_fp8_f32 v42, v0, v5
	v_mul_f32_e32 v0, 0x42800000, v43
	v_mul_f32_e32 v5, 0x42800000, v51
	v_med3_f32 v0, v0, s33, v39
	v_med3_f32 v5, v5, s33, v39
	v_cvt_pk_fp8_f32 v42, v0, v5 op_sel:[0,0,1]
	v_mul_f32_e32 v0, 0x42800000, v53
	v_mul_f32_e32 v5, 0x42800000, v55
	v_med3_f32 v0, v0, s33, v39
	v_med3_f32 v5, v5, s33, v39
	v_mov_b32_e32 v43, v1
	v_cvt_pk_fp8_f32 v43, v0, v5
	v_mul_f32_e32 v0, 0x42800000, v57
	v_mul_f32_e32 v5, 0x42800000, v59
	v_med3_f32 v0, v0, s33, v39
	v_med3_f32 v5, v5, s33, v39
	v_cvt_pk_fp8_f32 v43, v0, v5 op_sel:[0,0,1]
	v_mad_u64_u32 v[60:61], s[14:15], s12, v17, v[6:7]
	v_mad_u64_u32 v[6:7], s[12:13], s12, v18, v[6:7]
	v_lshl_add_u64 v[60:61], v[60:61], 0, v[2:3]
	v_lshl_add_u64 v[6:7], v[6:7], 0, v[2:3]
	global_store_dwordx2 v[60:61], v[46:47], off
	global_store_dwordx2 v[6:7], v[42:43], off
	s_waitcnt lgkmcnt(0)

; #define LAS __attribute__((address_space(3)))
; __device__ __forceinline__ float clamp8(float x) { return __builtin_amdgcn_fmed3f(x, -448.f, 448.f); }
; #define LDS_WAIT() asm volatile("s_waitcnt lgkmcnt(0)" ::: "memory")
; __device__ __forceinline__ void cvt_load(const CvtDesc& d, float (&t)[64], int lane) {
;     const float* p = d.src + (size_t)(lane >> 4) * d.N + 4 * (lane & 15);
; #pragma unroll
;     for (int i = 0; i < 16; ++i) { const f32x4 v = __builtin_nontemporal_load((const f32x4*)(p + (size_t)(4 * i) * d.N));
;         t[4 * i] = v.x; t[4 * i + 1] = v.y; t[4 * i + 2] = v.z; t[4 * i + 3] = v.w; }
; }
; __device__ __forceinline__ void cvt_finish(const CvtDesc& d, const float (&t)[64], LAS float* scr, int lane) {
;     LAS float* sw = scr + (lane >> 4) * 65 + 4 * (lane & 15);
; #pragma unroll
;     for (int i = 0; i < 16; ++i) { sw[(4 * i) * 65] = t[4 * i]; sw[(4 * i) * 65 + 1] = t[4 * i + 1]; sw[(4 * i) * 65 + 2] = t[4 * i + 2]; sw[(4 * i) * 65 + 3] = t[4 * i + 3]; }
;     LDS_WAIT();
;     const int c = lane & 7;
;     if (d.f8) {
; #pragma unroll
;         for (int j = 0; j < 8; ++j) { const int n = (lane >> 3) + 8 * j; const LAS float* s = scr + (8 * c) * 65 + n;
;             int a = __builtin_amdgcn_cvt_pk_fp8_f32(clamp8(s[0 * 65] * W8_SCALE), clamp8(s[1 * 65] * W8_SCALE), 0, false); a = __builtin_amdgcn_cvt_pk_fp8_f32(clamp8(s[2 * 65] * W8_SCALE), clamp8(s[3 * 65] * W8_SCALE), a, true);
;             int b = __builtin_amdgcn_cvt_pk_fp8_f32(clamp8(s[4 * 65] * W8_SCALE), clamp8(s[5 * 65] * W8_SCALE), 0, false); b = __builtin_amdgcn_cvt_pk_fp8_f32(clamp8(s[6 * 65] * W8_SCALE), clamp8(s[7 * 65] * W8_SCALE), b, true);
;             __builtin_nontemporal_store((u32x2){(unsigned)a, (unsigned)b}, (u32x2*)(d.dst + (size_t)n * d.dKB + 8 * c)); }
.LBB0_295:
	v_mul_u32_u24_e32 v2, s0, v9
	v_lshlrev_b32_e32 v192, 2, v2
	v_lshl_add_u64 v[0:1], v[0:1], 0, v[192:193]
	v_mov_b32_e32 v7, v193
	v_lshl_add_u64 v[0:1], v[0:1], 0, v[6:7]
	s_lshl_b32 s68, s0, 4
	global_load_dwordx4 v[20:23], v[0:1], off nt
	v_lshl_add_u64 v[0:1], v[0:1], 0, s[68:69]
	global_load_dwordx4 v[24:27], v[0:1], off nt
	v_lshl_add_u64 v[0:1], v[0:1], 0, s[68:69]
	global_load_dwordx4 v[28:31], v[0:1], off nt
	v_lshl_add_u64 v[0:1], v[0:1], 0, s[68:69]
	global_load_dwordx4 v[32:35], v[0:1], off nt
	v_lshl_add_u64 v[0:1], v[0:1], 0, s[68:69]
	global_load_dwordx4 v[36:39], v[0:1], off nt
	v_lshl_add_u64 v[0:1], v[0:1], 0, s[68:69]
	global_load_dwordx4 v[40:43], v[0:1], off nt
	v_lshl_add_u64 v[0:1], v[0:1], 0, s[68:69]
	global_load_dwordx4 v[44:47], v[0:1], off nt
	v_lshl_add_u64 v[0:1], v[0:1], 0, s[68:69]
	global_load_dwordx4 v[48:51], v[0:1], off nt
	v_lshl_add_u64 v[0:1], v[0:1], 0, s[68:69]
	global_load_dwordx4 v[52:55], v[0:1], off nt
	v_lshl_add_u64 v[0:1], v[0:1], 0, s[68:69]
	global_load_dwordx4 v[56:59], v[0:1], off nt
	v_lshl_add_u64 v[0:1], v[0:1], 0, s[68:69]
	global_load_dwordx4 v[60:63], v[0:1], off nt
	v_lshl_add_u64 v[0:1], v[0:1], 0, s[68:69]
	global_load_dwordx4 v[64:67], v[0:1], off nt
	v_lshl_add_u64 v[0:1], v[0:1], 0, s[68:69]
	global_load_dwordx4 v[68:71], v[0:1], off nt
	v_lshl_add_u64 v[0:1], v[0:1], 0, s[68:69]
	global_load_dwordx4 v[72:75], v[0:1], off nt
	v_lshl_add_u64 v[0:1], v[0:1], 0, s[68:69]
	global_load_dwordx4 v[76:79], v[0:1], off nt
	v_lshl_add_u64 v[0:1], v[0:1], 0, s[68:69]
	global_load_dwordx4 v[0:3], v[0:1], off nt
	v_add_u32_e32 v7, 0x410, v10
	s_waitcnt vmcnt(0)
	ds_write2_b32 v10, v20, v21 offset1:1
	ds_write2_b32 v10, v22, v23 offset0:2 offset1:3
	v_mov_b32_e32 v22, v193
	ds_write2_b32 v7, v24, v25 offset1:1
	v_add_u32_e32 v7, 0x418, v10
	ds_write2_b32 v7, v26, v27 offset1:1
	v_add_u32_e32 v7, 0x820, v10
	ds_write2_b32 v7, v28, v29 offset1:1
	v_add_u32_e32 v7, 0x828, v10
	ds_write2_b32 v7, v30, v31 offset1:1
	v_add_u32_e32 v7, 0xc30, v10
	ds_write2_b32 v7, v32, v33 offset1:1
	v_add_u32_e32 v7, 0xc38, v10
	ds_write2_b32 v7, v34, v35 offset1:1
	v_add_u32_e32 v7, 0x1040, v10
	ds_write2_b32 v7, v36, v37 offset1:1
	v_add_u32_e32 v7, 0x1048, v10
	ds_write2_b32 v7, v38, v39 offset1:1
	v_add_u32_e32 v7, 0x1450, v10
	ds_write2_b32 v7, v40, v41 offset1:1
	v_add_u32_e32 v7, 0x1458, v10
	ds_write2_b32 v7, v42, v43 offset1:1
	v_add_u32_e32 v7, 0x1860, v10
	ds_write2_b32 v7, v44, v45 offset1:1
	v_add_u32_e32 v7, 0x1868, v10
	ds_write2_b32 v7, v46, v47 offset1:1
	v_add_u32_e32 v7, 0x1c70, v10
	ds_write2_b32 v7, v48, v49 offset1:1
	v_add_u32_e32 v7, 0x1c78, v10
	ds_write2_b32 v7, v50, v51 offset1:1
	v_add_u32_e32 v7, 0x2080, v10
	ds_write2_b32 v7, v52, v53 offset1:1
	v_add_u32_e32 v7, 0x2088, v10
	ds_write2_b32 v7, v54, v55 offset1:1
	v_add_u32_e32 v7, 0x2490, v10
	ds_write2_b32 v7, v56, v57 offset1:1
	v_add_u32_e32 v7, 0x2498, v10
	ds_write2_b32 v7, v58, v59 offset1:1
	v_add_u32_e32 v7, 0x28a0, v10
	ds_write2_b32 v7, v60, v61 offset1:1
	v_add_u32_e32 v7, 0x28a8, v10
	ds_write2_b32 v7, v62, v63 offset1:1
	v_add_u32_e32 v7, 0x2cb0, v10
	ds_write2_b32 v7, v64, v65 offset1:1
	v_add_u32_e32 v7, 0x2cb8, v10
	ds_write2_b32 v7, v66, v67 offset1:1
	v_add_u32_e32 v7, 0x30c0, v10
	ds_write2_b32 v7, v68, v69 offset1:1
	v_add_u32_e32 v7, 0x30c8, v10
	ds_write2_b32 v7, v70, v71 offset1:1
	v_add_u32_e32 v7, 0x34d0, v10
	ds_write2_b32 v7, v72, v73 offset1:1
	v_add_u32_e32 v7, 0x34d8, v10
	ds_write2_b32 v7, v74, v75 offset1:1
	v_add_u32_e32 v7, 0x38e0, v10
	ds_write2_b32 v7, v76, v77 offset1:1
	v_add_u32_e32 v7, 0x38e8, v10
	ds_write2_b32 v7, v78, v79 offset1:1
	v_add_u32_e32 v7, 0x3cf0, v10
	ds_write2_b32 v7, v0, v1 offset1:1
	v_add_u32_e32 v0, 0x3cf8, v10
	ds_write2_b32 v0, v2, v3 offset1:1
	s_waitcnt lgkmcnt(0)
	ds_read2_b32 v[2:3], v12 offset1:8
	ds_read2_b32 v[20:21], v12 offset0:65 offset1:73
	ds_read2_b32 v[24:25], v12 offset0:130 offset1:138
	ds_read2_b32 v[26:27], v12 offset0:195 offset1:203
	v_mov_b32_e32 v23, v193
	s_waitcnt lgkmcnt(3)
	v_mul_f32_e32 v0, 0x42800000, v2
	s_waitcnt lgkmcnt(2)
	v_mul_f32_e32 v1, 0x42800000, v20
	v_add_u32_e32 v2, 0x400, v12
	v_med3_f32 v0, v0, s93, v224
	v_med3_f32 v1, v1, s93, v224
	ds_read2_b32 v[28:29], v2 offset0:4 offset1:12
	ds_read2_b32 v[30:31], v2 offset0:69 offset1:77
	v_cvt_pk_fp8_f32 v22, v0, v1
	v_mul_f32_e32 v3, 0x42800000, v3
	v_mul_f32_e32 v7, 0x42800000, v21
	v_med3_f32 v3, v3, s93, v224
	v_med3_f32 v7, v7, s93, v224
	v_mov_b32_e32 v20, v193
	s_waitcnt lgkmcnt(3)
	v_mul_f32_e32 v0, 0x42800000, v24
	s_waitcnt lgkmcnt(2)
	v_mul_f32_e32 v1, 0x42800000, v26
	v_cvt_pk_fp8_f32 v20, v3, v7
	v_med3_f32 v0, v0, s93, v224
	v_med3_f32 v1, v1, s93, v224
	ds_read2_b32 v[32:33], v2 offset0:134 offset1:142
	ds_read2_b32 v[34:35], v2 offset0:199 offset1:207
	v_cvt_pk_fp8_f32 v22, v0, v1 op_sel:[0,0,1]
	s_waitcnt lgkmcnt(3)
	v_mul_f32_e32 v0, 0x42800000, v28
	s_waitcnt lgkmcnt(2)
	v_mul_f32_e32 v1, 0x42800000, v30
	v_mul_f32_e32 v3, 0x42800000, v25
	v_mul_f32_e32 v7, 0x42800000, v27
	v_med3_f32 v0, v0, s93, v224
	v_med3_f32 v1, v1, s93, v224
	v_med3_f32 v3, v3, s93, v224
	v_med3_f32 v7, v7, s93, v224
	v_cvt_pk_fp8_f32 v23, v0, v1
	v_cvt_pk_fp8_f32 v20, v3, v7 op_sel:[0,0,1]
	v_mul_f32_e32 v3, 0x42800000, v29
	v_mul_f32_e32 v7, 0x42800000, v31
	v_med3_f32 v3, v3, s93, v224
	v_med3_f32 v7, v7, s93, v224
	v_mov_b32_e32 v21, v193
	s_waitcnt lgkmcnt(1)
	v_mul_f32_e32 v0, 0x42800000, v32
	s_waitcnt lgkmcnt(0)
; #define LAS __attribute__((address_space(3)))
; __device__ __forceinline__ float clamp8(float x) { return __builtin_amdgcn_fmed3f(x, -448.f, 448.f); }
; __device__ __forceinline__ void cvt_finish(const CvtDesc& d, const float (&t)[64], LAS float* scr, int lane) {
;     ...
;     if (d.f8) {
; #pragma unroll
;         for (int j = 0; j < 8; ++j) { const int n = (lane >> 3) + 8 * j; const LAS float* s = scr + (8 * c) * 65 + n;
;             int a = __builtin_amdgcn_cvt_pk_fp8_f32(clamp8(s[0 * 65] * W8_SCALE), clamp8(s[1 * 65] * W8_SCALE), 0, false); a = __builtin_amdgcn_cvt_pk_fp8_f32(clamp8(s[2 * 65] * W8_SCALE), clamp8(s[3 * 65] * W8_SCALE), a, true);
;             int b = __builtin_amdgcn_cvt_pk_fp8_f32(clamp8(s[4 * 65] * W8_SCALE), clamp8(s[5 * 65] * W8_SCALE), 0, false); b = __builtin_amdgcn_cvt_pk_fp8_f32(clamp8(s[6 * 65] * W8_SCALE), clamp8(s[7 * 65] * W8_SCALE), b, true);
;             __builtin_nontemporal_store((u32x2){(unsigned)a, (unsigned)b}, (u32x2*)(d.dst + (size_t)n * d.dKB + 8 * c)); }
	v_mul_f32_e32 v1, 0x42800000, v34
	v_cvt_pk_fp8_f32 v21, v3, v7
	v_med3_f32 v0, v0, s93, v224
	v_med3_f32 v1, v1, s93, v224
	v_cvt_pk_fp8_f32 v23, v0, v1 op_sel:[0,0,1]
	v_mul_f32_e32 v3, 0x42800000, v33
	v_mul_f32_e32 v7, 0x42800000, v35
	v_mov_b64_e32 v[0:1], s[14:15]
	v_med3_f32 v3, v3, s93, v224
	v_med3_f32 v7, v7, s93, v224
	v_mad_u64_u32 v[36:37], s[0:1], s12, v11, v[0:1]
	v_cvt_pk_fp8_f32 v21, v3, v7 op_sel:[0,0,1]
	v_lshl_add_u64 v[36:37], v[36:37], 0, v[4:5]
	global_store_dwordx2 v[36:37], v[22:23], off
	v_mad_u64_u32 v[22:23], s[0:1], s12, v13, v[0:1]
	v_lshl_add_u64 v[22:23], v[22:23], 0, v[4:5]
	global_store_dwordx2 v[22:23], v[20:21], off
	ds_read2_b32 v[20:21], v12 offset0:16 offset1:24
	ds_read2_b32 v[22:23], v12 offset0:81 offset1:89
	ds_read2_b32 v[26:27], v12 offset0:146 offset1:154
	ds_read2_b32 v[28:29], v12 offset0:211 offset1:219
	v_mov_b32_e32 v24, v193
	s_waitcnt lgkmcnt(3)
	v_mul_f32_e32 v3, 0x42800000, v20
	s_waitcnt lgkmcnt(2)
	v_mul_f32_e32 v7, 0x42800000, v22
	v_med3_f32 v3, v3, s93, v224
	v_med3_f32 v7, v7, s93, v224
	ds_read2_b32 v[30:31], v2 offset0:20 offset1:28
	ds_read2_b32 v[32:33], v2 offset0:85 offset1:93
	v_cvt_pk_fp8_f32 v24, v3, v7
	s_waitcnt lgkmcnt(3)
	v_mul_f32_e32 v3, 0x42800000, v26
	s_waitcnt lgkmcnt(2)
	v_mul_f32_e32 v7, 0x42800000, v28
	v_med3_f32 v3, v3, s93, v224
	v_med3_f32 v7, v7, s93, v224
	ds_read2_b32 v[34:35], v2 offset0:150 offset1:158
	ds_read2_b32 v[36:37], v2 offset0:215 offset1:223
	v_cvt_pk_fp8_f32 v24, v3, v7 op_sel:[0,0,1]
	s_waitcnt lgkmcnt(3)
	v_mul_f32_e32 v3, 0x42800000, v30
	s_waitcnt lgkmcnt(2)
	v_mul_f32_e32 v7, 0x42800000, v32
	v_med3_f32 v3, v3, s93, v224
	v_med3_f32 v7, v7, s93, v224
	v_mov_b32_e32 v25, v193
	v_cvt_pk_fp8_f32 v25, v3, v7
	s_waitcnt lgkmcnt(1)
	v_mul_f32_e32 v3, 0x42800000, v34
	s_waitcnt lgkmcnt(0)
	v_mul_f32_e32 v7, 0x42800000, v36
	v_med3_f32 v3, v3, s93, v224
	v_med3_f32 v7, v7, s93, v224
	v_cvt_pk_fp8_f32 v25, v3, v7 op_sel:[0,0,1]
	v_mul_f32_e32 v3, 0x42800000, v21
	v_mul_f32_e32 v7, 0x42800000, v23
	v_med3_f32 v3, v3, s93, v224
	v_med3_f32 v7, v7, s93, v224
	v_mov_b32_e32 v20, v193
	v_cvt_pk_fp8_f32 v20, v3, v7
	v_mul_f32_e32 v3, 0x42800000, v27
	v_mul_f32_e32 v7, 0x42800000, v29
	v_med3_f32 v3, v3, s93, v224
	v_med3_f32 v7, v7, s93, v224
	v_cvt_pk_fp8_f32 v20, v3, v7 op_sel:[0,0,1]
	v_mul_f32_e32 v3, 0x42800000, v31
	v_mul_f32_e32 v7, 0x42800000, v33
	v_med3_f32 v3, v3, s93, v224
	v_med3_f32 v7, v7, s93, v224
	v_mov_b32_e32 v21, v193
	v_cvt_pk_fp8_f32 v21, v3, v7
	v_mul_f32_e32 v3, 0x42800000, v35
	v_mul_f32_e32 v7, 0x42800000, v37
	v_med3_f32 v3, v3, s93, v224
	v_med3_f32 v7, v7, s93, v224
	v_cvt_pk_fp8_f32 v21, v3, v7 op_sel:[0,0,1]
	v_mad_u64_u32 v[38:39], s[0:1], s12, v14, v[0:1]
	v_mad_u64_u32 v[22:23], s[0:1], s12, v15, v[0:1]
	v_lshl_add_u64 v[38:39], v[38:39], 0, v[4:5]
	v_lshl_add_u64 v[22:23], v[22:23], 0, v[4:5]
	global_store_dwordx2 v[38:39], v[24:25], off
	global_store_dwordx2 v[22:23], v[20:21], off
	ds_read2_b32 v[20:21], v12 offset0:32 offset1:40
	ds_read2_b32 v[22:23], v12 offset0:97 offset1:105
	ds_read2_b32 v[26:27], v12 offset0:162 offset1:170
	ds_read2_b32 v[28:29], v12 offset0:227 offset1:235
	v_mov_b32_e32 v24, v193
	s_waitcnt lgkmcnt(3)
	v_mul_f32_e32 v3, 0x42800000, v20
	s_waitcnt lgkmcnt(2)
	v_mul_f32_e32 v7, 0x42800000, v22
	v_med3_f32 v3, v3, s93, v224
	v_med3_f32 v7, v7, s93, v224
	ds_read2_b32 v[30:31], v2 offset0:36 offset1:44
	ds_read2_b32 v[32:33], v2 offset0:101 offset1:109
	v_cvt_pk_fp8_f32 v24, v3, v7
	s_waitcnt lgkmcnt(3)
	v_mul_f32_e32 v3, 0x42800000, v26
	s_waitcnt lgkmcnt(2)
	v_mul_f32_e32 v7, 0x42800000, v28
	v_med3_f32 v3, v3, s93, v224
	v_med3_f32 v7, v7, s93, v224
	ds_read2_b32 v[34:35], v2 offset0:166 offset1:174
	ds_read2_b32 v[36:37], v2 offset0:231 offset1:239
	v_cvt_pk_fp8_f32 v24, v3, v7 op_sel:[0,0,1]
	s_waitcnt lgkmcnt(3)
; #define LAS __attribute__((address_space(3)))
; __device__ __forceinline__ float clamp8(float x) { return __builtin_amdgcn_fmed3f(x, -448.f, 448.f); }
; __device__ __forceinline__ void cvt_finish(const CvtDesc& d, const float (&t)[64], LAS float* scr, int lane) {
;     ...
;     if (d.f8) {
; #pragma unroll
;         for (int j = 0; j < 8; ++j) { const int n = (lane >> 3) + 8 * j; const LAS float* s = scr + (8 * c) * 65 + n;
;             int a = __builtin_amdgcn_cvt_pk_fp8_f32(clamp8(s[0 * 65] * W8_SCALE), clamp8(s[1 * 65] * W8_SCALE), 0, false); a = __builtin_amdgcn_cvt_pk_fp8_f32(clamp8(s[2 * 65] * W8_SCALE), clamp8(s[3 * 65] * W8_SCALE), a, true);
;             int b = __builtin_amdgcn_cvt_pk_fp8_f32(clamp8(s[4 * 65] * W8_SCALE), clamp8(s[5 * 65] * W8_SCALE), 0, false); b = __builtin_amdgcn_cvt_pk_fp8_f32(clamp8(s[6 * 65] * W8_SCALE), clamp8(s[7 * 65] * W8_SCALE), b, true);
;             __builtin_nontemporal_store((u32x2){(unsigned)a, (unsigned)b}, (u32x2*)(d.dst + (size_t)n * d.dKB + 8 * c)); }
	v_mul_f32_e32 v3, 0x42800000, v30
	s_waitcnt lgkmcnt(2)
	v_mul_f32_e32 v7, 0x42800000, v32
	v_med3_f32 v3, v3, s93, v224
	v_med3_f32 v7, v7, s93, v224
	v_mov_b32_e32 v25, v193
	v_cvt_pk_fp8_f32 v25, v3, v7
	s_waitcnt lgkmcnt(1)
	v_mul_f32_e32 v3, 0x42800000, v34
	s_waitcnt lgkmcnt(0)
	v_mul_f32_e32 v7, 0x42800000, v36
	v_med3_f32 v3, v3, s93, v224
	v_med3_f32 v7, v7, s93, v224
	v_cvt_pk_fp8_f32 v25, v3, v7 op_sel:[0,0,1]
	v_mul_f32_e32 v3, 0x42800000, v21
	v_mul_f32_e32 v7, 0x42800000, v23
	v_med3_f32 v3, v3, s93, v224
	v_med3_f32 v7, v7, s93, v224
	v_mov_b32_e32 v20, v193
	v_cvt_pk_fp8_f32 v20, v3, v7
	v_mul_f32_e32 v3, 0x42800000, v27
	v_mul_f32_e32 v7, 0x42800000, v29
	v_med3_f32 v3, v3, s93, v224
	v_med3_f32 v7, v7, s93, v224
	v_cvt_pk_fp8_f32 v20, v3, v7 op_sel:[0,0,1]
	v_mul_f32_e32 v3, 0x42800000, v31
	v_mul_f32_e32 v7, 0x42800000, v33
	v_med3_f32 v3, v3, s93, v224
	v_med3_f32 v7, v7, s93, v224
	v_mov_b32_e32 v21, v193
	v_cvt_pk_fp8_f32 v21, v3, v7
	v_mul_f32_e32 v3, 0x42800000, v35
	v_mul_f32_e32 v7, 0x42800000, v37
	v_med3_f32 v3, v3, s93, v224
	v_med3_f32 v7, v7, s93, v224
	v_cvt_pk_fp8_f32 v21, v3, v7 op_sel:[0,0,1]
	v_mad_u64_u32 v[38:39], s[0:1], s12, v16, v[0:1]
	v_mad_u64_u32 v[22:23], s[0:1], s12, v17, v[0:1]
	v_lshl_add_u64 v[38:39], v[38:39], 0, v[4:5]
	v_lshl_add_u64 v[22:23], v[22:23], 0, v[4:5]
	global_store_dwordx2 v[38:39], v[24:25], off
	global_store_dwordx2 v[22:23], v[20:21], off
	ds_read2_b32 v[20:21], v12 offset0:48 offset1:56
	ds_read2_b32 v[22:23], v12 offset0:113 offset1:121
	ds_read2_b32 v[26:27], v12 offset0:178 offset1:186
	ds_read2_b32 v[28:29], v12 offset0:243 offset1:251
	v_mov_b32_e32 v24, v193
	s_waitcnt lgkmcnt(3)
	v_mul_f32_e32 v3, 0x42800000, v20
	s_waitcnt lgkmcnt(2)
	v_mul_f32_e32 v7, 0x42800000, v22
	v_med3_f32 v3, v3, s93, v224
	v_med3_f32 v7, v7, s93, v224
	ds_read2_b32 v[30:31], v2 offset0:52 offset1:60
	ds_read2_b32 v[32:33], v2 offset0:117 offset1:125
	v_cvt_pk_fp8_f32 v24, v3, v7
	ds_read2_b32 v[34:35], v2 offset0:182 offset1:190
	s_waitcnt lgkmcnt(4)
	v_mul_f32_e32 v3, 0x42800000, v26
	s_waitcnt lgkmcnt(3)
	v_mul_f32_e32 v7, 0x42800000, v28
	v_med3_f32 v3, v3, s93, v224
	v_med3_f32 v7, v7, s93, v224
	v_cvt_pk_fp8_f32 v24, v3, v7 op_sel:[0,0,1]
	s_waitcnt lgkmcnt(2)
	v_mul_f32_e32 v3, 0x42800000, v30
	s_waitcnt lgkmcnt(1)
	v_mul_f32_e32 v7, 0x42800000, v32
	v_med3_f32 v3, v3, s93, v224
	v_med3_f32 v7, v7, s93, v224
	v_mov_b32_e32 v25, v193
	v_cvt_pk_fp8_f32 v25, v3, v7
	s_waitcnt lgkmcnt(0)
	v_mul_f32_e32 v3, 0x42800000, v34
	v_med3_f32 v7, v3, s93, v224
	ds_read2_b32 v[2:3], v2 offset0:247 offset1:255
	v_mov_b32_e32 v20, v193
	v_mad_u64_u32 v[36:37], s[0:1], s12, v18, v[0:1]
	v_mad_u64_u32 v[0:1], s[0:1], s12, v19, v[0:1]
	s_waitcnt lgkmcnt(0)
	v_mul_f32_e32 v2, 0x42800000, v2
	v_med3_f32 v2, v2, s93, v224
	v_cvt_pk_fp8_f32 v25, v7, v2 op_sel:[0,0,1]
	v_mul_f32_e32 v2, 0x42800000, v21
	v_mul_f32_e32 v7, 0x42800000, v23
	v_med3_f32 v2, v2, s93, v224
	v_med3_f32 v7, v7, s93, v224
	v_cvt_pk_fp8_f32 v20, v2, v7
	v_mul_f32_e32 v2, 0x42800000, v27
	v_mul_f32_e32 v7, 0x42800000, v29
	v_med3_f32 v2, v2, s93, v224
	v_med3_f32 v7, v7, s93, v224
	v_cvt_pk_fp8_f32 v20, v2, v7 op_sel:[0,0,1]
	v_mul_f32_e32 v2, 0x42800000, v31
	v_mul_f32_e32 v7, 0x42800000, v33
	v_med3_f32 v2, v2, s93, v224
	v_med3_f32 v7, v7, s93, v224
	v_mov_b32_e32 v21, v193
	v_cvt_pk_fp8_f32 v21, v2, v7
	v_mul_f32_e32 v2, 0x42800000, v35
	v_mul_f32_e32 v3, 0x42800000, v3
	v_med3_f32 v2, v2, s93, v224
	v_med3_f32 v3, v3, s93, v224
	v_cvt_pk_fp8_f32 v21, v2, v3 op_sel:[0,0,1]
	v_lshl_add_u64 v[36:37], v[36:37], 0, v[4:5]
	v_lshl_add_u64 v[0:1], v[0:1], 0, v[4:5]
	global_store_dwordx2 v[36:37], v[24:25], off
	global_store_dwordx2 v[0:1], v[20:21], off
	s_waitcnt lgkmcnt(0)

; #define LAS __attribute__((address_space(3)))
; __device__ __forceinline__ float clamp8(float x) { return __builtin_amdgcn_fmed3f(x, -448.f, 448.f); }
;     __device__ __forceinline__ unsigned char* ws() const { return *(unsigned char* const __attribute__((address_space(4)))*)(p + 232); }
; __device__ __forceinline__ void cvt_finish(const CvtDesc& d, const float (&t)[64], LAS float* scr, int lane) {
;     ...
;     if (d.f8) {
; #pragma unroll
;         for (int j = 0; j < 8; ++j) { const int n = (lane >> 3) + 8 * j; const LAS float* s = scr + (8 * c) * 65 + n;
;             int a = __builtin_amdgcn_cvt_pk_fp8_f32(clamp8(s[0 * 65] * W8_SCALE), clamp8(s[1 * 65] * W8_SCALE), 0, false); a = __builtin_amdgcn_cvt_pk_fp8_f32(clamp8(s[2 * 65] * W8_SCALE), clamp8(s[3 * 65] * W8_SCALE), a, true);
;             int b = __builtin_amdgcn_cvt_pk_fp8_f32(clamp8(s[4 * 65] * W8_SCALE), clamp8(s[5 * 65] * W8_SCALE), 0, false); b = __builtin_amdgcn_cvt_pk_fp8_f32(clamp8(s[6 * 65] * W8_SCALE), clamp8(s[7 * 65] * W8_SCALE), b, true);
;             __builtin_nontemporal_store((u32x2){(unsigned)a, (unsigned)b}, (u32x2*)(d.dst + (size_t)n * d.dKB + 8 * c)); }
;     ...
;             const int q0 = (int)base + wave; const bool v0 = q0 < Q_TOTAL, v1 = q0 + 8 < Q_TOTAL, v2 = q0 + 16 < Q_TOTAL, v3 = q0 + 24 < Q_TOTAL;
;             float ta[64], tb[64]; CvtDesc da, db;
;             if (v0) { da = conv_expert_desc(a, ws, q0); cvt_load(da, ta, lane); }
;             if (v1) { db = conv_expert_desc(a, ws, q0 + 8); cvt_load(db, tb, lane); }
;             if (v0) cvt_finish(da, ta, scr, lane);
;             if (v2) { da = conv_expert_desc(a, ws, q0 + 16); cvt_load(da, ta, lane); }
;             if (v1) cvt_finish(db, tb, scr, lane);
;             if (v3) { db = conv_expert_desc(a, ws, q0 + 24); cvt_load(db, tb, lane); }
;             if (v2) cvt_finish(da, ta, scr, lane);
;             if (v3) cvt_finish(db, tb, scr, lane);
.Lcv_dd1:
	v_lshlrev_b32_e32 v166, 4, v165
	v_lshl_add_u32 v166, v164, s19, v166
	global_load_dwordx4 v[64:67], v166, s[10:11] nt
	v_add_u32_e32 v166, s15, v166
	global_load_dwordx4 v[68:71], v166, s[10:11] nt
	v_add_u32_e32 v166, s15, v166
	global_load_dwordx4 v[72:75], v166, s[10:11] nt
	v_add_u32_e32 v166, s15, v166
	global_load_dwordx4 v[76:79], v166, s[10:11] nt
	v_add_u32_e32 v166, s15, v166
	global_load_dwordx4 v[80:83], v166, s[10:11] nt
	v_add_u32_e32 v166, s15, v166
	global_load_dwordx4 v[84:87], v166, s[10:11] nt
	v_add_u32_e32 v166, s15, v166
	global_load_dwordx4 v[88:91], v166, s[10:11] nt
	v_add_u32_e32 v166, s15, v166
	global_load_dwordx4 v[92:95], v166, s[10:11] nt
	v_add_u32_e32 v166, s15, v166
	global_load_dwordx4 v[96:99], v166, s[10:11] nt
	v_add_u32_e32 v166, s15, v166
	global_load_dwordx4 v[100:103], v166, s[10:11] nt
	v_add_u32_e32 v166, s15, v166
	global_load_dwordx4 v[104:107], v166, s[10:11] nt
	v_add_u32_e32 v166, s15, v166
	global_load_dwordx4 v[108:111], v166, s[10:11] nt
	v_add_u32_e32 v166, s15, v166
	global_load_dwordx4 v[112:115], v166, s[10:11] nt
	v_add_u32_e32 v166, s15, v166
	global_load_dwordx4 v[116:119], v166, s[10:11] nt
	v_add_u32_e32 v166, s15, v166
	global_load_dwordx4 v[120:123], v166, s[10:11] nt
	v_add_u32_e32 v166, s15, v166
	global_load_dwordx4 v[124:127], v166, s[10:11] nt
	s_waitcnt vmcnt(16)
	v_mul_f32_e32 v0, 0x42800000, v0
	v_mul_f32_e32 v1, 0x42800000, v1
	v_mul_f32_e32 v2, 0x42800000, v2
	v_mul_f32_e32 v3, 0x42800000, v3
	v_mul_f32_e32 v4, 0x42800000, v4
	v_mul_f32_e32 v5, 0x42800000, v5
	v_mul_f32_e32 v6, 0x42800000, v6
	v_mul_f32_e32 v7, 0x42800000, v7
	v_mul_f32_e32 v8, 0x42800000, v8
	v_mul_f32_e32 v9, 0x42800000, v9
	v_mul_f32_e32 v10, 0x42800000, v10
	v_mul_f32_e32 v11, 0x42800000, v11
	v_mul_f32_e32 v12, 0x42800000, v12
	v_mul_f32_e32 v13, 0x42800000, v13
	v_mul_f32_e32 v14, 0x42800000, v14
	v_mul_f32_e32 v15, 0x42800000, v15
	v_mul_f32_e32 v16, 0x42800000, v16
	v_mul_f32_e32 v17, 0x42800000, v17
	v_mul_f32_e32 v18, 0x42800000, v18
	v_mul_f32_e32 v19, 0x42800000, v19
	v_mul_f32_e32 v20, 0x42800000, v20
	v_mul_f32_e32 v21, 0x42800000, v21
	v_mul_f32_e32 v22, 0x42800000, v22
	v_mul_f32_e32 v23, 0x42800000, v23
	v_mul_f32_e32 v24, 0x42800000, v24
	v_mul_f32_e32 v25, 0x42800000, v25
	v_mul_f32_e32 v26, 0x42800000, v26
	v_mul_f32_e32 v27, 0x42800000, v27
	v_mul_f32_e32 v28, 0x42800000, v28
	v_mul_f32_e32 v29, 0x42800000, v29
	v_mul_f32_e32 v30, 0x42800000, v30
	v_mul_f32_e32 v31, 0x42800000, v31
	v_mul_f32_e32 v32, 0x42800000, v32
	v_mul_f32_e32 v33, 0x42800000, v33
	v_mul_f32_e32 v34, 0x42800000, v34
	v_mul_f32_e32 v35, 0x42800000, v35
	v_mul_f32_e32 v36, 0x42800000, v36
	v_mul_f32_e32 v37, 0x42800000, v37
	v_mul_f32_e32 v38, 0x42800000, v38
	v_mul_f32_e32 v39, 0x42800000, v39
	v_mul_f32_e32 v40, 0x42800000, v40
	v_mul_f32_e32 v41, 0x42800000, v41
	v_mul_f32_e32 v42, 0x42800000, v42
	v_mul_f32_e32 v43, 0x42800000, v43
	v_mul_f32_e32 v44, 0x42800000, v44
	v_mul_f32_e32 v45, 0x42800000, v45
	v_mul_f32_e32 v46, 0x42800000, v46
	v_mul_f32_e32 v47, 0x42800000, v47
	v_mul_f32_e32 v48, 0x42800000, v48
	v_mul_f32_e32 v49, 0x42800000, v49
	v_mul_f32_e32 v50, 0x42800000, v50
	v_mul_f32_e32 v51, 0x42800000, v51
	v_mul_f32_e32 v52, 0x42800000, v52
	v_mul_f32_e32 v53, 0x42800000, v53
	v_mul_f32_e32 v54, 0x42800000, v54
	v_mul_f32_e32 v55, 0x42800000, v55
	v_mul_f32_e32 v56, 0x42800000, v56
	v_mul_f32_e32 v57, 0x42800000, v57
	v_mul_f32_e32 v58, 0x42800000, v58
	v_mul_f32_e32 v59, 0x42800000, v59
	v_mul_f32_e32 v60, 0x42800000, v60
	v_mul_f32_e32 v61, 0x42800000, v61
	v_mul_f32_e32 v62, 0x42800000, v62
	v_mul_f32_e32 v63, 0x42800000, v63
	v_med3_f32 v0, v0, s93, v224
	v_med3_f32 v1, v1, s93, v224
	v_med3_f32 v2, v2, s93, v224
	v_med3_f32 v3, v3, s93, v224
	v_med3_f32 v4, v4, s93, v224
	v_med3_f32 v5, v5, s93, v224
	v_med3_f32 v6, v6, s93, v224
	v_med3_f32 v7, v7, s93, v224
	v_med3_f32 v8, v8, s93, v224
	v_med3_f32 v9, v9, s93, v224
	v_med3_f32 v10, v10, s93, v224
	v_med3_f32 v11, v11, s93, v224
	v_med3_f32 v12, v12, s93, v224
	v_med3_f32 v13, v13, s93, v224
	v_med3_f32 v14, v14, s93, v224
	v_med3_f32 v15, v15, s93, v224
	v_med3_f32 v16, v16, s93, v224
	v_med3_f32 v17, v17, s93, v224
	v_med3_f32 v18, v18, s93, v224
	v_med3_f32 v19, v19, s93, v224
	v_med3_f32 v20, v20, s93, v224
	v_med3_f32 v21, v21, s93, v224
	v_med3_f32 v22, v22, s93, v224
; #define LAS __attribute__((address_space(3)))
; __device__ __forceinline__ float clamp8(float x) { return __builtin_amdgcn_fmed3f(x, -448.f, 448.f); }
;     __device__ __forceinline__ const float* in(int i) const { return *(const float* const __attribute__((address_space(4)))*)(p + 8 * i); }
;     __device__ __forceinline__ unsigned char* ws() const { return *(unsigned char* const __attribute__((address_space(4)))*)(p + 232); }
; __device__ __forceinline__ void cvt_finish(const CvtDesc& d, const float (&t)[64], LAS float* scr, int lane) {
;     ...
;     if (d.f8) {
; #pragma unroll
;         for (int j = 0; j < 8; ++j) { const int n = (lane >> 3) + 8 * j; const LAS float* s = scr + (8 * c) * 65 + n;
;             int a = __builtin_amdgcn_cvt_pk_fp8_f32(clamp8(s[0 * 65] * W8_SCALE), clamp8(s[1 * 65] * W8_SCALE), 0, false); a = __builtin_amdgcn_cvt_pk_fp8_f32(clamp8(s[2 * 65] * W8_SCALE), clamp8(s[3 * 65] * W8_SCALE), a, true);
;             int b = __builtin_amdgcn_cvt_pk_fp8_f32(clamp8(s[4 * 65] * W8_SCALE), clamp8(s[5 * 65] * W8_SCALE), 0, false); b = __builtin_amdgcn_cvt_pk_fp8_f32(clamp8(s[6 * 65] * W8_SCALE), clamp8(s[7 * 65] * W8_SCALE), b, true);
;             __builtin_nontemporal_store((u32x2){(unsigned)a, (unsigned)b}, (u32x2*)(d.dst + (size_t)n * d.dKB + 8 * c)); }
; __device__ __forceinline__ CvtDesc conv_expert_desc(const KA& a, unsigned char* ws, int q) {
;     const int l = q / Q_PER_L; int r = q - l * Q_PER_L;
;     unsigned char* wl = ws + WS_W + (size_t)l * W_LSTRIDE;
;     CvtDesc d; d.f8 = (MOE_FP8_LAST && (MOE_FP8_GU_ALL || l == NLAYER - 1)) ? 1 : 0;
;     if (MOE_FP8_LAST && MOE_FP8_DOWN_ALL && r >= 2 * Q_IG) d.f8 = 1;
;     const int eb = d.f8 ? 1 : 2;
;     if (r < 2 * Q_IG) { const int up = r >= Q_IG; if (up) r -= Q_IG; const int e = r >> 8, rr = r & 255, kb = rr >> 3, nb = rr & 7, n0 = nb * 64;
;         const float* src = e < 64 ? a.in(up ? 21 : 20) + ((size_t)l * 64 + e) * DM * FFE : a.in(up ? 24 : 23) + (size_t)l * DM * FFE;
;         d.src = src + (size_t)(kb * 64) * FFE + n0; d.N = FFE; d.dKB = DM * eb;
;         d.dst = wl + W_GU + ((size_t)e * 1024 * DM + (size_t)((n0 >> 7) * 256 + up * 128 + (n0 & 127)) * DM + kb * 64) * eb;
	v_med3_f32 v23, v23, s93, v224
	v_med3_f32 v24, v24, s93, v224
	v_med3_f32 v25, v25, s93, v224
	v_med3_f32 v26, v26, s93, v224
	v_med3_f32 v27, v27, s93, v224
	v_med3_f32 v28, v28, s93, v224
	v_med3_f32 v29, v29, s93, v224
	v_med3_f32 v30, v30, s93, v224
	v_med3_f32 v31, v31, s93, v224
	v_med3_f32 v32, v32, s93, v224
	v_med3_f32 v33, v33, s93, v224
	v_med3_f32 v34, v34, s93, v224
	v_med3_f32 v35, v35, s93, v224
	v_med3_f32 v36, v36, s93, v224
	v_med3_f32 v37, v37, s93, v224
	v_med3_f32 v38, v38, s93, v224
	v_med3_f32 v39, v39, s93, v224
	v_med3_f32 v40, v40, s93, v224
	v_med3_f32 v41, v41, s93, v224
	v_med3_f32 v42, v42, s93, v224
	v_med3_f32 v43, v43, s93, v224
	v_med3_f32 v44, v44, s93, v224
	v_med3_f32 v45, v45, s93, v224
	v_med3_f32 v46, v46, s93, v224
	v_med3_f32 v47, v47, s93, v224
	v_med3_f32 v48, v48, s93, v224
	v_med3_f32 v49, v49, s93, v224
	v_med3_f32 v50, v50, s93, v224
	v_med3_f32 v51, v51, s93, v224
	v_med3_f32 v52, v52, s93, v224
	v_med3_f32 v53, v53, s93, v224
	v_med3_f32 v54, v54, s93, v224
	v_med3_f32 v55, v55, s93, v224
	v_med3_f32 v56, v56, s93, v224
	v_med3_f32 v57, v57, s93, v224
	v_med3_f32 v58, v58, s93, v224
	v_med3_f32 v59, v59, s93, v224
	v_med3_f32 v60, v60, s93, v224
	v_med3_f32 v61, v61, s93, v224
	v_med3_f32 v62, v62, s93, v224
	v_med3_f32 v63, v63, s93, v224
	v_cvt_pk_fp8_f32 v148, v0, v4
	v_cvt_pk_fp8_f32 v149, v16, v20
	v_cvt_pk_fp8_f32 v150, v32, v36
	v_cvt_pk_fp8_f32 v151, v48, v52
	v_cvt_pk_fp8_f32 v152, v1, v5
	v_cvt_pk_fp8_f32 v153, v17, v21
	v_cvt_pk_fp8_f32 v154, v33, v37
	v_cvt_pk_fp8_f32 v155, v49, v53
	v_cvt_pk_fp8_f32 v156, v2, v6
	v_cvt_pk_fp8_f32 v157, v18, v22
	v_cvt_pk_fp8_f32 v158, v34, v38
	v_cvt_pk_fp8_f32 v159, v50, v54
	v_cvt_pk_fp8_f32 v160, v3, v7
	v_cvt_pk_fp8_f32 v161, v19, v23
	v_cvt_pk_fp8_f32 v162, v35, v39
	v_cvt_pk_fp8_f32 v163, v51, v55
	v_cvt_pk_fp8_f32 v148, v8, v12 op_sel:[0,0,1]
	v_cvt_pk_fp8_f32 v149, v24, v28 op_sel:[0,0,1]
	v_cvt_pk_fp8_f32 v150, v40, v44 op_sel:[0,0,1]
	v_cvt_pk_fp8_f32 v151, v56, v60 op_sel:[0,0,1]
	v_cvt_pk_fp8_f32 v152, v9, v13 op_sel:[0,0,1]
	v_cvt_pk_fp8_f32 v153, v25, v29 op_sel:[0,0,1]
	v_cvt_pk_fp8_f32 v154, v41, v45 op_sel:[0,0,1]
	v_cvt_pk_fp8_f32 v155, v57, v61 op_sel:[0,0,1]
	v_cvt_pk_fp8_f32 v156, v10, v14 op_sel:[0,0,1]
	v_cvt_pk_fp8_f32 v157, v26, v30 op_sel:[0,0,1]
	v_cvt_pk_fp8_f32 v158, v42, v46 op_sel:[0,0,1]
	v_cvt_pk_fp8_f32 v159, v58, v62 op_sel:[0,0,1]
	v_cvt_pk_fp8_f32 v160, v11, v15 op_sel:[0,0,1]
	v_cvt_pk_fp8_f32 v161, v27, v31 op_sel:[0,0,1]
	v_cvt_pk_fp8_f32 v162, v43, v47 op_sel:[0,0,1]
	v_cvt_pk_fp8_f32 v163, v59, v63 op_sel:[0,0,1]
	s_movk_i32 s1, 0x200
	s_cmp_eq_u32 s14, 0
	s_cselect_b32 s0, 13, 11
	s_cselect_b32 s1, 0x800, s1
	v_lshlrev_b32_e32 v167, 4, v164
	v_lshl_add_u32 v167, v165, s0, v167
	global_store_dwordx4 v167, v[148:151], s[12:13]
	v_add_u32_e32 v167, s1, v167
	global_store_dwordx4 v167, v[152:155], s[12:13]
	v_add_u32_e32 v167, s1, v167
	global_store_dwordx4 v167, v[156:159], s[12:13]
	v_add_u32_e32 v167, s1, v167
	global_store_dwordx4 v167, v[160:163], s[12:13]
	s_nop 1
	s_add_u32 s20, s38, 16
	s_cmp_ge_u32 s20, 0xc300
	s_cselect_b32 s21, 1, 0
	s_cselect_b32 s0, 0xc300, 0
	s_sub_u32 s20, s20, s0
	s_cmp_ge_u32 s20, 0x8200
	s_cbranch_scc1 .Lcv_dn2
	s_cmp_ge_u32 s20, 0x4100
	s_cselect_b32 s22, 1, 0
	s_cselect_b32 s0, 0x4100, 0
	s_sub_u32 s20, s20, s0
	s_lshr_b32 s23, s20, 8
	s_lshl_b32 s31, s21, 6
	s_add_u32 s31, s31, s23
	s_cmp_eq_u32 s23, 64
	s_cselect_b32 s0, 3, 0
	s_cselect_b32 s31, s21, s31
	s_add_u32 s0, s0, s22
	s_lshl_b32 s0, s0, 1
	s_nop 0
	v_readlane_b32 s10, v147, s0
	s_or_b32 s0, s0, 1
	s_nop 0
	v_readlane_b32 s11, v147, s0
	s_lshr_b32 s33, s20, 3
	s_and_b32 s33, s33, 31
	s_and_b32 s34, s20, 7
	s_lshl_b32 s0, s33, 17
	s_lshl_b32 s1, s34, 8
	s_or_b32 s0, s0, s1
	s_lshl_b32 s1, s31, 22
	s_or_b32 s0, s0, s1
	s_lshr_b32 s1, s31, 10
	s_add_u32 s10, s10, s0
	s_addc_u32 s11, s11, s1
	s_lshr_b32 s0, s34, 1
	s_lshl_b32 s0, s0, 8
	s_lshl_b32 s1, s22, 7
	s_add_u32 s0, s0, s1
	s_and_b32 s1, s34, 1
	s_lshl_b32 s1, s1, 6
	s_add_u32 s0, s0, s1
	s_lshl_b32 s0, s0, 11
	s_lshl_b32 s1, s33, 6
	s_add_u32 s0, s0, s1
	s_lshl_b32 s1, s23, 21
	s_add_u32 s0, s0, s1
	s_add_u32 s0, s0, 0x2000000
	s_mul_i32 s1, s21, 0x1a800000
	s_add_u32 s0, s0, s1
	s_add_u32 s12, s28, s0
	s_addc_u32 s13, s29, 0
	s_mov_b32 s14, 0
	s_movk_i32 s15, 0x800
	s_mov_b32 s19, 15
	s_branch .Lcv_dd2

; #define LAS __attribute__((address_space(3)))
; __device__ __forceinline__ float clamp8(float x) { return __builtin_amdgcn_fmed3f(x, -448.f, 448.f); }
;     __device__ __forceinline__ unsigned char* ws() const { return *(unsigned char* const __attribute__((address_space(4)))*)(p + 232); }
; __device__ __forceinline__ void cvt_finish(const CvtDesc& d, const float (&t)[64], LAS float* scr, int lane) {
;     ...
;     if (d.f8) {
; #pragma unroll
;         for (int j = 0; j < 8; ++j) { const int n = (lane >> 3) + 8 * j; const LAS float* s = scr + (8 * c) * 65 + n;
;             int a = __builtin_amdgcn_cvt_pk_fp8_f32(clamp8(s[0 * 65] * W8_SCALE), clamp8(s[1 * 65] * W8_SCALE), 0, false); a = __builtin_amdgcn_cvt_pk_fp8_f32(clamp8(s[2 * 65] * W8_SCALE), clamp8(s[3 * 65] * W8_SCALE), a, true);
;             int b = __builtin_amdgcn_cvt_pk_fp8_f32(clamp8(s[4 * 65] * W8_SCALE), clamp8(s[5 * 65] * W8_SCALE), 0, false); b = __builtin_amdgcn_cvt_pk_fp8_f32(clamp8(s[6 * 65] * W8_SCALE), clamp8(s[7 * 65] * W8_SCALE), b, true);
;             __builtin_nontemporal_store((u32x2){(unsigned)a, (unsigned)b}, (u32x2*)(d.dst + (size_t)n * d.dKB + 8 * c)); }
;     ...
;             const int q0 = (int)base + wave; const bool v0 = q0 < Q_TOTAL, v1 = q0 + 8 < Q_TOTAL, v2 = q0 + 16 < Q_TOTAL, v3 = q0 + 24 < Q_TOTAL;
;             float ta[64], tb[64]; CvtDesc da, db;
;             if (v0) { da = conv_expert_desc(a, ws, q0); cvt_load(da, ta, lane); }
;             if (v1) { db = conv_expert_desc(a, ws, q0 + 8); cvt_load(db, tb, lane); }
;             if (v0) cvt_finish(da, ta, scr, lane);
;             if (v2) { da = conv_expert_desc(a, ws, q0 + 16); cvt_load(da, ta, lane); }
;             if (v1) cvt_finish(db, tb, scr, lane);
;             if (v3) { db = conv_expert_desc(a, ws, q0 + 24); cvt_load(db, tb, lane); }
;             if (v2) cvt_finish(da, ta, scr, lane);
;             if (v3) cvt_finish(db, tb, scr, lane);
.Lcv_dd2:
	v_lshlrev_b32_e32 v166, 4, v165
	v_lshl_add_u32 v166, v164, s19, v166
	global_load_dwordx4 v[0:3], v166, s[10:11] nt
	v_add_u32_e32 v166, s15, v166
	global_load_dwordx4 v[4:7], v166, s[10:11] nt
	v_add_u32_e32 v166, s15, v166
	global_load_dwordx4 v[8:11], v166, s[10:11] nt
	v_add_u32_e32 v166, s15, v166
	global_load_dwordx4 v[12:15], v166, s[10:11] nt
	v_add_u32_e32 v166, s15, v166
	global_load_dwordx4 v[16:19], v166, s[10:11] nt
	v_add_u32_e32 v166, s15, v166
	global_load_dwordx4 v[20:23], v166, s[10:11] nt
	v_add_u32_e32 v166, s15, v166
	global_load_dwordx4 v[24:27], v166, s[10:11] nt
	v_add_u32_e32 v166, s15, v166
	global_load_dwordx4 v[28:31], v166, s[10:11] nt
	v_add_u32_e32 v166, s15, v166
	global_load_dwordx4 v[32:35], v166, s[10:11] nt
	v_add_u32_e32 v166, s15, v166
	global_load_dwordx4 v[36:39], v166, s[10:11] nt
	v_add_u32_e32 v166, s15, v166
	global_load_dwordx4 v[40:43], v166, s[10:11] nt
	v_add_u32_e32 v166, s15, v166
	global_load_dwordx4 v[44:47], v166, s[10:11] nt
	v_add_u32_e32 v166, s15, v166
	global_load_dwordx4 v[48:51], v166, s[10:11] nt
	v_add_u32_e32 v166, s15, v166
	global_load_dwordx4 v[52:55], v166, s[10:11] nt
	v_add_u32_e32 v166, s15, v166
	global_load_dwordx4 v[56:59], v166, s[10:11] nt
	v_add_u32_e32 v166, s15, v166
	global_load_dwordx4 v[60:63], v166, s[10:11] nt
	s_waitcnt vmcnt(16)
	v_mul_f32_e32 v64, 0x42800000, v64
	v_mul_f32_e32 v65, 0x42800000, v65
	v_mul_f32_e32 v66, 0x42800000, v66
	v_mul_f32_e32 v67, 0x42800000, v67
	v_mul_f32_e32 v68, 0x42800000, v68
	v_mul_f32_e32 v69, 0x42800000, v69
	v_mul_f32_e32 v70, 0x42800000, v70
	v_mul_f32_e32 v71, 0x42800000, v71
	v_mul_f32_e32 v72, 0x42800000, v72
	v_mul_f32_e32 v73, 0x42800000, v73
	v_mul_f32_e32 v74, 0x42800000, v74
	v_mul_f32_e32 v75, 0x42800000, v75
	v_mul_f32_e32 v76, 0x42800000, v76
	v_mul_f32_e32 v77, 0x42800000, v77
	v_mul_f32_e32 v78, 0x42800000, v78
	v_mul_f32_e32 v79, 0x42800000, v79
	v_mul_f32_e32 v80, 0x42800000, v80
	v_mul_f32_e32 v81, 0x42800000, v81
	v_mul_f32_e32 v82, 0x42800000, v82
	v_mul_f32_e32 v83, 0x42800000, v83
	v_mul_f32_e32 v84, 0x42800000, v84
	v_mul_f32_e32 v85, 0x42800000, v85
	v_mul_f32_e32 v86, 0x42800000, v86
	v_mul_f32_e32 v87, 0x42800000, v87
	v_mul_f32_e32 v88, 0x42800000, v88
	v_mul_f32_e32 v89, 0x42800000, v89
	v_mul_f32_e32 v90, 0x42800000, v90
	v_mul_f32_e32 v91, 0x42800000, v91
	v_mul_f32_e32 v92, 0x42800000, v92
	v_mul_f32_e32 v93, 0x42800000, v93
	v_mul_f32_e32 v94, 0x42800000, v94
	v_mul_f32_e32 v95, 0x42800000, v95
	v_mul_f32_e32 v96, 0x42800000, v96
	v_mul_f32_e32 v97, 0x42800000, v97
	v_mul_f32_e32 v98, 0x42800000, v98
	v_mul_f32_e32 v99, 0x42800000, v99
	v_mul_f32_e32 v100, 0x42800000, v100
	v_mul_f32_e32 v101, 0x42800000, v101
	v_mul_f32_e32 v102, 0x42800000, v102
	v_mul_f32_e32 v103, 0x42800000, v103
	v_mul_f32_e32 v104, 0x42800000, v104
	v_mul_f32_e32 v105, 0x42800000, v105
	v_mul_f32_e32 v106, 0x42800000, v106
	v_mul_f32_e32 v107, 0x42800000, v107
	v_mul_f32_e32 v108, 0x42800000, v108
	v_mul_f32_e32 v109, 0x42800000, v109
	v_mul_f32_e32 v110, 0x42800000, v110
	v_mul_f32_e32 v111, 0x42800000, v111
	v_mul_f32_e32 v112, 0x42800000, v112
	v_mul_f32_e32 v113, 0x42800000, v113
	v_mul_f32_e32 v114, 0x42800000, v114
	v_mul_f32_e32 v115, 0x42800000, v115
	v_mul_f32_e32 v116, 0x42800000, v116
	v_mul_f32_e32 v117, 0x42800000, v117
	v_mul_f32_e32 v118, 0x42800000, v118
	v_mul_f32_e32 v119, 0x42800000, v119
	v_mul_f32_e32 v120, 0x42800000, v120
	v_mul_f32_e32 v121, 0x42800000, v121
	v_mul_f32_e32 v122, 0x42800000, v122
	v_mul_f32_e32 v123, 0x42800000, v123
	v_mul_f32_e32 v124, 0x42800000, v124
	v_mul_f32_e32 v125, 0x42800000, v125
	v_mul_f32_e32 v126, 0x42800000, v126
	v_mul_f32_e32 v127, 0x42800000, v127
	v_med3_f32 v64, v64, s93, v224
	v_med3_f32 v65, v65, s93, v224
	v_med3_f32 v66, v66, s93, v224
	v_med3_f32 v67, v67, s93, v224
	v_med3_f32 v68, v68, s93, v224
	v_med3_f32 v69, v69, s93, v224
	v_med3_f32 v70, v70, s93, v224
	v_med3_f32 v71, v71, s93, v224
	v_med3_f32 v72, v72, s93, v224
	v_med3_f32 v73, v73, s93, v224
	v_med3_f32 v74, v74, s93, v224
	v_med3_f32 v75, v75, s93, v224
	v_med3_f32 v76, v76, s93, v224
	v_med3_f32 v77, v77, s93, v224
	v_med3_f32 v78, v78, s93, v224
	v_med3_f32 v79, v79, s93, v224
	v_med3_f32 v80, v80, s93, v224
	v_med3_f32 v81, v81, s93, v224
	v_med3_f32 v82, v82, s93, v224
	v_med3_f32 v83, v83, s93, v224
	v_med3_f32 v84, v84, s93, v224
	v_med3_f32 v85, v85, s93, v224
	v_med3_f32 v86, v86, s93, v224
; #define LAS __attribute__((address_space(3)))
; __device__ __forceinline__ float clamp8(float x) { return __builtin_amdgcn_fmed3f(x, -448.f, 448.f); }
;     __device__ __forceinline__ const float* in(int i) const { return *(const float* const __attribute__((address_space(4)))*)(p + 8 * i); }
;     __device__ __forceinline__ unsigned char* ws() const { return *(unsigned char* const __attribute__((address_space(4)))*)(p + 232); }
; __device__ __forceinline__ void cvt_finish(const CvtDesc& d, const float (&t)[64], LAS float* scr, int lane) {
;     ...
;     if (d.f8) {
; #pragma unroll
;         for (int j = 0; j < 8; ++j) { const int n = (lane >> 3) + 8 * j; const LAS float* s = scr + (8 * c) * 65 + n;
;             int a = __builtin_amdgcn_cvt_pk_fp8_f32(clamp8(s[0 * 65] * W8_SCALE), clamp8(s[1 * 65] * W8_SCALE), 0, false); a = __builtin_amdgcn_cvt_pk_fp8_f32(clamp8(s[2 * 65] * W8_SCALE), clamp8(s[3 * 65] * W8_SCALE), a, true);
;             int b = __builtin_amdgcn_cvt_pk_fp8_f32(clamp8(s[4 * 65] * W8_SCALE), clamp8(s[5 * 65] * W8_SCALE), 0, false); b = __builtin_amdgcn_cvt_pk_fp8_f32(clamp8(s[6 * 65] * W8_SCALE), clamp8(s[7 * 65] * W8_SCALE), b, true);
;             __builtin_nontemporal_store((u32x2){(unsigned)a, (unsigned)b}, (u32x2*)(d.dst + (size_t)n * d.dKB + 8 * c)); }
; __device__ __forceinline__ CvtDesc conv_expert_desc(const KA& a, unsigned char* ws, int q) {
;     const int l = q / Q_PER_L; int r = q - l * Q_PER_L;
;     unsigned char* wl = ws + WS_W + (size_t)l * W_LSTRIDE;
;     CvtDesc d; d.f8 = (MOE_FP8_LAST && (MOE_FP8_GU_ALL || l == NLAYER - 1)) ? 1 : 0;
;     if (MOE_FP8_LAST && MOE_FP8_DOWN_ALL && r >= 2 * Q_IG) d.f8 = 1;
;     const int eb = d.f8 ? 1 : 2;
;     if (r < 2 * Q_IG) { const int up = r >= Q_IG; if (up) r -= Q_IG; const int e = r >> 8, rr = r & 255, kb = rr >> 3, nb = rr & 7, n0 = nb * 64;
;         const float* src = e < 64 ? a.in(up ? 21 : 20) + ((size_t)l * 64 + e) * DM * FFE : a.in(up ? 24 : 23) + (size_t)l * DM * FFE;
;         d.src = src + (size_t)(kb * 64) * FFE + n0; d.N = FFE; d.dKB = DM * eb;
;         d.dst = wl + W_GU + ((size_t)e * 1024 * DM + (size_t)((n0 >> 7) * 256 + up * 128 + (n0 & 127)) * DM + kb * 64) * eb;
	v_med3_f32 v87, v87, s93, v224
	v_med3_f32 v88, v88, s93, v224
	v_med3_f32 v89, v89, s93, v224
	v_med3_f32 v90, v90, s93, v224
	v_med3_f32 v91, v91, s93, v224
	v_med3_f32 v92, v92, s93, v224
	v_med3_f32 v93, v93, s93, v224
	v_med3_f32 v94, v94, s93, v224
	v_med3_f32 v95, v95, s93, v224
	v_med3_f32 v96, v96, s93, v224
	v_med3_f32 v97, v97, s93, v224
	v_med3_f32 v98, v98, s93, v224
	v_med3_f32 v99, v99, s93, v224
	v_med3_f32 v100, v100, s93, v224
	v_med3_f32 v101, v101, s93, v224
	v_med3_f32 v102, v102, s93, v224
	v_med3_f32 v103, v103, s93, v224
	v_med3_f32 v104, v104, s93, v224
	v_med3_f32 v105, v105, s93, v224
	v_med3_f32 v106, v106, s93, v224
	v_med3_f32 v107, v107, s93, v224
	v_med3_f32 v108, v108, s93, v224
	v_med3_f32 v109, v109, s93, v224
	v_med3_f32 v110, v110, s93, v224
	v_med3_f32 v111, v111, s93, v224
	v_med3_f32 v112, v112, s93, v224
	v_med3_f32 v113, v113, s93, v224
	v_med3_f32 v114, v114, s93, v224
	v_med3_f32 v115, v115, s93, v224
	v_med3_f32 v116, v116, s93, v224
	v_med3_f32 v117, v117, s93, v224
	v_med3_f32 v118, v118, s93, v224
	v_med3_f32 v119, v119, s93, v224
	v_med3_f32 v120, v120, s93, v224
	v_med3_f32 v121, v121, s93, v224
	v_med3_f32 v122, v122, s93, v224
	v_med3_f32 v123, v123, s93, v224
	v_med3_f32 v124, v124, s93, v224
	v_med3_f32 v125, v125, s93, v224
	v_med3_f32 v126, v126, s93, v224
	v_med3_f32 v127, v127, s93, v224
	v_cvt_pk_fp8_f32 v148, v64, v68
	v_cvt_pk_fp8_f32 v149, v80, v84
	v_cvt_pk_fp8_f32 v150, v96, v100
	v_cvt_pk_fp8_f32 v151, v112, v116
	v_cvt_pk_fp8_f32 v152, v65, v69
	v_cvt_pk_fp8_f32 v153, v81, v85
	v_cvt_pk_fp8_f32 v154, v97, v101
	v_cvt_pk_fp8_f32 v155, v113, v117
	v_cvt_pk_fp8_f32 v156, v66, v70
	v_cvt_pk_fp8_f32 v157, v82, v86
	v_cvt_pk_fp8_f32 v158, v98, v102
	v_cvt_pk_fp8_f32 v159, v114, v118
	v_cvt_pk_fp8_f32 v160, v67, v71
	v_cvt_pk_fp8_f32 v161, v83, v87
	v_cvt_pk_fp8_f32 v162, v99, v103
	v_cvt_pk_fp8_f32 v163, v115, v119
	v_cvt_pk_fp8_f32 v148, v72, v76 op_sel:[0,0,1]
	v_cvt_pk_fp8_f32 v149, v88, v92 op_sel:[0,0,1]
	v_cvt_pk_fp8_f32 v150, v104, v108 op_sel:[0,0,1]
	v_cvt_pk_fp8_f32 v151, v120, v124 op_sel:[0,0,1]
	v_cvt_pk_fp8_f32 v152, v73, v77 op_sel:[0,0,1]
	v_cvt_pk_fp8_f32 v153, v89, v93 op_sel:[0,0,1]
	v_cvt_pk_fp8_f32 v154, v105, v109 op_sel:[0,0,1]
	v_cvt_pk_fp8_f32 v155, v121, v125 op_sel:[0,0,1]
	v_cvt_pk_fp8_f32 v156, v74, v78 op_sel:[0,0,1]
	v_cvt_pk_fp8_f32 v157, v90, v94 op_sel:[0,0,1]
	v_cvt_pk_fp8_f32 v158, v106, v110 op_sel:[0,0,1]
	v_cvt_pk_fp8_f32 v159, v122, v126 op_sel:[0,0,1]
	v_cvt_pk_fp8_f32 v160, v75, v79 op_sel:[0,0,1]
	v_cvt_pk_fp8_f32 v161, v91, v95 op_sel:[0,0,1]
	v_cvt_pk_fp8_f32 v162, v107, v111 op_sel:[0,0,1]
	v_cvt_pk_fp8_f32 v163, v123, v127 op_sel:[0,0,1]
	s_movk_i32 s1, 0x200
	s_cmp_eq_u32 s18, 0
	s_cselect_b32 s0, 13, 11
	s_cselect_b32 s1, 0x800, s1
	v_lshlrev_b32_e32 v167, 4, v164
	v_lshl_add_u32 v167, v165, s0, v167
	global_store_dwordx4 v167, v[148:151], s[16:17]
	v_add_u32_e32 v167, s1, v167
	global_store_dwordx4 v167, v[152:155], s[16:17]
	v_add_u32_e32 v167, s1, v167
	global_store_dwordx4 v167, v[156:159], s[16:17]
	v_add_u32_e32 v167, s1, v167
	global_store_dwordx4 v167, v[160:163], s[16:17]
	s_nop 1
	s_add_u32 s20, s38, 24
	s_cmp_ge_u32 s20, 0xc300
	s_cselect_b32 s21, 1, 0
	s_cselect_b32 s0, 0xc300, 0
	s_sub_u32 s20, s20, s0
	s_cmp_ge_u32 s20, 0x8200
	s_cbranch_scc1 .Lcv_dn3
	s_cmp_ge_u32 s20, 0x4100
	s_cselect_b32 s22, 1, 0
	s_cselect_b32 s0, 0x4100, 0
	s_sub_u32 s20, s20, s0
	s_lshr_b32 s23, s20, 8
	s_lshl_b32 s31, s21, 6
	s_add_u32 s31, s31, s23
	s_cmp_eq_u32 s23, 64
	s_cselect_b32 s0, 3, 0
	s_cselect_b32 s31, s21, s31
	s_add_u32 s0, s0, s22
	s_lshl_b32 s0, s0, 1
	s_nop 0
	v_readlane_b32 s10, v147, s0
	s_or_b32 s0, s0, 1
	s_nop 0
	v_readlane_b32 s11, v147, s0
	s_lshr_b32 s33, s20, 3
	s_and_b32 s33, s33, 31
	s_and_b32 s34, s20, 7
	s_lshl_b32 s0, s33, 17
	s_lshl_b32 s1, s34, 8
	s_or_b32 s0, s0, s1
	s_lshl_b32 s1, s31, 22
	s_or_b32 s0, s0, s1
	s_lshr_b32 s1, s31, 10
	s_add_u32 s10, s10, s0
	s_addc_u32 s11, s11, s1
	s_lshr_b32 s0, s34, 1
	s_lshl_b32 s0, s0, 8
	s_lshl_b32 s1, s22, 7
	s_add_u32 s0, s0, s1
	s_and_b32 s1, s34, 1
	s_lshl_b32 s1, s1, 6
	s_add_u32 s0, s0, s1
	s_lshl_b32 s0, s0, 11
	s_lshl_b32 s1, s33, 6
	s_add_u32 s0, s0, s1
	s_lshl_b32 s1, s23, 21
	s_add_u32 s0, s0, s1
	s_add_u32 s0, s0, 0x2000000
	s_mul_i32 s1, s21, 0x1a800000
	s_add_u32 s0, s0, s1
	s_add_u32 s16, s28, s0
	s_addc_u32 s17, s29, 0
	s_mov_b32 s18, 0
	s_movk_i32 s15, 0x800
	s_mov_b32 s19, 15
	s_branch .Lcv_dd3

; #define LAS __attribute__((address_space(3)))
; __device__ __forceinline__ float clamp8(float x) { return __builtin_amdgcn_fmed3f(x, -448.f, 448.f); }
;     __device__ __forceinline__ unsigned char* ws() const { return *(unsigned char* const __attribute__((address_space(4)))*)(p + 232); }
; __device__ __forceinline__ void cvt_finish(const CvtDesc& d, const float (&t)[64], LAS float* scr, int lane) {
;     ...
;     if (d.f8) {
; #pragma unroll
;         for (int j = 0; j < 8; ++j) { const int n = (lane >> 3) + 8 * j; const LAS float* s = scr + (8 * c) * 65 + n;
;             int a = __builtin_amdgcn_cvt_pk_fp8_f32(clamp8(s[0 * 65] * W8_SCALE), clamp8(s[1 * 65] * W8_SCALE), 0, false); a = __builtin_amdgcn_cvt_pk_fp8_f32(clamp8(s[2 * 65] * W8_SCALE), clamp8(s[3 * 65] * W8_SCALE), a, true);
;             int b = __builtin_amdgcn_cvt_pk_fp8_f32(clamp8(s[4 * 65] * W8_SCALE), clamp8(s[5 * 65] * W8_SCALE), 0, false); b = __builtin_amdgcn_cvt_pk_fp8_f32(clamp8(s[6 * 65] * W8_SCALE), clamp8(s[7 * 65] * W8_SCALE), b, true);
;             __builtin_nontemporal_store((u32x2){(unsigned)a, (unsigned)b}, (u32x2*)(d.dst + (size_t)n * d.dKB + 8 * c)); }
;     ...
;             const int q0 = (int)base + wave; const bool v0 = q0 < Q_TOTAL, v1 = q0 + 8 < Q_TOTAL, v2 = q0 + 16 < Q_TOTAL, v3 = q0 + 24 < Q_TOTAL;
;             float ta[64], tb[64]; CvtDesc da, db;
;             if (v0) { da = conv_expert_desc(a, ws, q0); cvt_load(da, ta, lane); }
;             if (v1) { db = conv_expert_desc(a, ws, q0 + 8); cvt_load(db, tb, lane); }
;             if (v0) cvt_finish(da, ta, scr, lane);
;             if (v2) { da = conv_expert_desc(a, ws, q0 + 16); cvt_load(da, ta, lane); }
;             if (v1) cvt_finish(db, tb, scr, lane);
;             if (v3) { db = conv_expert_desc(a, ws, q0 + 24); cvt_load(db, tb, lane); }
;             if (v2) cvt_finish(da, ta, scr, lane);
;             if (v3) cvt_finish(db, tb, scr, lane);
.Lcv_dd3:
	v_lshlrev_b32_e32 v166, 4, v165
	v_lshl_add_u32 v166, v164, s19, v166
	global_load_dwordx4 v[64:67], v166, s[10:11] nt
	v_add_u32_e32 v166, s15, v166
	global_load_dwordx4 v[68:71], v166, s[10:11] nt
	v_add_u32_e32 v166, s15, v166
	global_load_dwordx4 v[72:75], v166, s[10:11] nt
	v_add_u32_e32 v166, s15, v166
	global_load_dwordx4 v[76:79], v166, s[10:11] nt
	v_add_u32_e32 v166, s15, v166
	global_load_dwordx4 v[80:83], v166, s[10:11] nt
	v_add_u32_e32 v166, s15, v166
	global_load_dwordx4 v[84:87], v166, s[10:11] nt
	v_add_u32_e32 v166, s15, v166
	global_load_dwordx4 v[88:91], v166, s[10:11] nt
	v_add_u32_e32 v166, s15, v166
	global_load_dwordx4 v[92:95], v166, s[10:11] nt
	v_add_u32_e32 v166, s15, v166
	global_load_dwordx4 v[96:99], v166, s[10:11] nt
	v_add_u32_e32 v166, s15, v166
	global_load_dwordx4 v[100:103], v166, s[10:11] nt
	v_add_u32_e32 v166, s15, v166
	global_load_dwordx4 v[104:107], v166, s[10:11] nt
	v_add_u32_e32 v166, s15, v166
	global_load_dwordx4 v[108:111], v166, s[10:11] nt
	v_add_u32_e32 v166, s15, v166
	global_load_dwordx4 v[112:115], v166, s[10:11] nt
	v_add_u32_e32 v166, s15, v166
	global_load_dwordx4 v[116:119], v166, s[10:11] nt
	v_add_u32_e32 v166, s15, v166
	global_load_dwordx4 v[120:123], v166, s[10:11] nt
	v_add_u32_e32 v166, s15, v166
	global_load_dwordx4 v[124:127], v166, s[10:11] nt
	s_waitcnt vmcnt(16)
	v_mul_f32_e32 v0, 0x42800000, v0
	v_mul_f32_e32 v1, 0x42800000, v1
	v_mul_f32_e32 v2, 0x42800000, v2
	v_mul_f32_e32 v3, 0x42800000, v3
	v_mul_f32_e32 v4, 0x42800000, v4
	v_mul_f32_e32 v5, 0x42800000, v5
	v_mul_f32_e32 v6, 0x42800000, v6
	v_mul_f32_e32 v7, 0x42800000, v7
	v_mul_f32_e32 v8, 0x42800000, v8
	v_mul_f32_e32 v9, 0x42800000, v9
	v_mul_f32_e32 v10, 0x42800000, v10
	v_mul_f32_e32 v11, 0x42800000, v11
	v_mul_f32_e32 v12, 0x42800000, v12
	v_mul_f32_e32 v13, 0x42800000, v13
	v_mul_f32_e32 v14, 0x42800000, v14
	v_mul_f32_e32 v15, 0x42800000, v15
	v_mul_f32_e32 v16, 0x42800000, v16
	v_mul_f32_e32 v17, 0x42800000, v17
	v_mul_f32_e32 v18, 0x42800000, v18
	v_mul_f32_e32 v19, 0x42800000, v19
	v_mul_f32_e32 v20, 0x42800000, v20
	v_mul_f32_e32 v21, 0x42800000, v21
	v_mul_f32_e32 v22, 0x42800000, v22
	v_mul_f32_e32 v23, 0x42800000, v23
	v_mul_f32_e32 v24, 0x42800000, v24
	v_mul_f32_e32 v25, 0x42800000, v25
	v_mul_f32_e32 v26, 0x42800000, v26
	v_mul_f32_e32 v27, 0x42800000, v27
	v_mul_f32_e32 v28, 0x42800000, v28
	v_mul_f32_e32 v29, 0x42800000, v29
	v_mul_f32_e32 v30, 0x42800000, v30
	v_mul_f32_e32 v31, 0x42800000, v31
	v_mul_f32_e32 v32, 0x42800000, v32
	v_mul_f32_e32 v33, 0x42800000, v33
	v_mul_f32_e32 v34, 0x42800000, v34
	v_mul_f32_e32 v35, 0x42800000, v35
	v_mul_f32_e32 v36, 0x42800000, v36
	v_mul_f32_e32 v37, 0x42800000, v37
	v_mul_f32_e32 v38, 0x42800000, v38
	v_mul_f32_e32 v39, 0x42800000, v39
	v_mul_f32_e32 v40, 0x42800000, v40
	v_mul_f32_e32 v41, 0x42800000, v41
	v_mul_f32_e32 v42, 0x42800000, v42
	v_mul_f32_e32 v43, 0x42800000, v43
	v_mul_f32_e32 v44, 0x42800000, v44
	v_mul_f32_e32 v45, 0x42800000, v45
	v_mul_f32_e32 v46, 0x42800000, v46
	v_mul_f32_e32 v47, 0x42800000, v47
	v_mul_f32_e32 v48, 0x42800000, v48
	v_mul_f32_e32 v49, 0x42800000, v49
	v_mul_f32_e32 v50, 0x42800000, v50
	v_mul_f32_e32 v51, 0x42800000, v51
	v_mul_f32_e32 v52, 0x42800000, v52
	v_mul_f32_e32 v53, 0x42800000, v53
	v_mul_f32_e32 v54, 0x42800000, v54
	v_mul_f32_e32 v55, 0x42800000, v55
	v_mul_f32_e32 v56, 0x42800000, v56
	v_mul_f32_e32 v57, 0x42800000, v57
	v_mul_f32_e32 v58, 0x42800000, v58
	v_mul_f32_e32 v59, 0x42800000, v59
	v_mul_f32_e32 v60, 0x42800000, v60
	v_mul_f32_e32 v61, 0x42800000, v61
	v_mul_f32_e32 v62, 0x42800000, v62
	v_mul_f32_e32 v63, 0x42800000, v63
	v_med3_f32 v0, v0, s93, v224
	v_med3_f32 v1, v1, s93, v224
	v_med3_f32 v2, v2, s93, v224
	v_med3_f32 v3, v3, s93, v224
	v_med3_f32 v4, v4, s93, v224
	v_med3_f32 v5, v5, s93, v224
	v_med3_f32 v6, v6, s93, v224
	v_med3_f32 v7, v7, s93, v224
	v_med3_f32 v8, v8, s93, v224
	v_med3_f32 v9, v9, s93, v224
	v_med3_f32 v10, v10, s93, v224
	v_med3_f32 v11, v11, s93, v224
	v_med3_f32 v12, v12, s93, v224
	v_med3_f32 v13, v13, s93, v224
	v_med3_f32 v14, v14, s93, v224
	v_med3_f32 v15, v15, s93, v224
	v_med3_f32 v16, v16, s93, v224
	v_med3_f32 v17, v17, s93, v224
	v_med3_f32 v18, v18, s93, v224
	v_med3_f32 v19, v19, s93, v224
	v_med3_f32 v20, v20, s93, v224
	v_med3_f32 v21, v21, s93, v224
	v_med3_f32 v22, v22, s93, v224
	v_med3_f32 v23, v23, s93, v224
	v_med3_f32 v24, v24, s93, v224
	v_med3_f32 v25, v25, s93, v224
	v_med3_f32 v26, v26, s93, v224
	v_med3_f32 v27, v27, s93, v224
	v_med3_f32 v28, v28, s93, v224
	v_med3_f32 v29, v29, s93, v224
	v_med3_f32 v30, v30, s93, v224
	v_med3_f32 v31, v31, s93, v224
	v_med3_f32 v32, v32, s93, v224
	v_med3_f32 v33, v33, s93, v224
	v_med3_f32 v34, v34, s93, v224
	v_med3_f32 v35, v35, s93, v224
	v_med3_f32 v36, v36, s93, v224
	v_med3_f32 v37, v37, s93, v224
	v_med3_f32 v38, v38, s93, v224
	v_med3_f32 v39, v39, s93, v224
	v_med3_f32 v40, v40, s93, v224
	v_med3_f32 v41, v41, s93, v224
	v_med3_f32 v42, v42, s93, v224
	v_med3_f32 v43, v43, s93, v224
	v_med3_f32 v44, v44, s93, v224
	v_med3_f32 v45, v45, s93, v224
	v_med3_f32 v46, v46, s93, v224
	v_med3_f32 v47, v47, s93, v224
	v_med3_f32 v48, v48, s93, v224
	v_med3_f32 v49, v49, s93, v224
	v_med3_f32 v50, v50, s93, v224
	v_med3_f32 v51, v51, s93, v224
	v_med3_f32 v52, v52, s93, v224
	v_med3_f32 v53, v53, s93, v224
	v_med3_f32 v54, v54, s93, v224
	v_med3_f32 v55, v55, s93, v224
	v_med3_f32 v56, v56, s93, v224
	v_med3_f32 v57, v57, s93, v224
	v_med3_f32 v58, v58, s93, v224
	v_med3_f32 v59, v59, s93, v224
	v_med3_f32 v60, v60, s93, v224
	v_med3_f32 v61, v61, s93, v224
	v_med3_f32 v62, v62, s93, v224
; #define LAS __attribute__((address_space(3)))
; __device__ __forceinline__ float clamp8(float x) { return __builtin_amdgcn_fmed3f(x, -448.f, 448.f); }
; __device__ __forceinline__ void cvt_finish(const CvtDesc& d, const float (&t)[64], LAS float* scr, int lane) {
;     ...
;     if (d.f8) {
; #pragma unroll
;         for (int j = 0; j < 8; ++j) { const int n = (lane >> 3) + 8 * j; const LAS float* s = scr + (8 * c) * 65 + n;
;             int a = __builtin_amdgcn_cvt_pk_fp8_f32(clamp8(s[0 * 65] * W8_SCALE), clamp8(s[1 * 65] * W8_SCALE), 0, false); a = __builtin_amdgcn_cvt_pk_fp8_f32(clamp8(s[2 * 65] * W8_SCALE), clamp8(s[3 * 65] * W8_SCALE), a, true);
;             int b = __builtin_amdgcn_cvt_pk_fp8_f32(clamp8(s[4 * 65] * W8_SCALE), clamp8(s[5 * 65] * W8_SCALE), 0, false); b = __builtin_amdgcn_cvt_pk_fp8_f32(clamp8(s[6 * 65] * W8_SCALE), clamp8(s[7 * 65] * W8_SCALE), b, true);
;             __builtin_nontemporal_store((u32x2){(unsigned)a, (unsigned)b}, (u32x2*)(d.dst + (size_t)n * d.dKB + 8 * c)); }
	v_med3_f32 v63, v63, s93, v224
	v_cvt_pk_fp8_f32 v148, v0, v4
	v_cvt_pk_fp8_f32 v149, v16, v20
	v_cvt_pk_fp8_f32 v150, v32, v36
	v_cvt_pk_fp8_f32 v151, v48, v52
	v_cvt_pk_fp8_f32 v152, v1, v5
	v_cvt_pk_fp8_f32 v153, v17, v21
	v_cvt_pk_fp8_f32 v154, v33, v37
	v_cvt_pk_fp8_f32 v155, v49, v53
	v_cvt_pk_fp8_f32 v156, v2, v6
	v_cvt_pk_fp8_f32 v157, v18, v22
	v_cvt_pk_fp8_f32 v158, v34, v38
	v_cvt_pk_fp8_f32 v159, v50, v54
	v_cvt_pk_fp8_f32 v160, v3, v7
	v_cvt_pk_fp8_f32 v161, v19, v23
	v_cvt_pk_fp8_f32 v162, v35, v39
	v_cvt_pk_fp8_f32 v163, v51, v55
	v_cvt_pk_fp8_f32 v148, v8, v12 op_sel:[0,0,1]
	v_cvt_pk_fp8_f32 v149, v24, v28 op_sel:[0,0,1]
	v_cvt_pk_fp8_f32 v150, v40, v44 op_sel:[0,0,1]
	v_cvt_pk_fp8_f32 v151, v56, v60 op_sel:[0,0,1]
	v_cvt_pk_fp8_f32 v152, v9, v13 op_sel:[0,0,1]
	v_cvt_pk_fp8_f32 v153, v25, v29 op_sel:[0,0,1]
	v_cvt_pk_fp8_f32 v154, v41, v45 op_sel:[0,0,1]
	v_cvt_pk_fp8_f32 v155, v57, v61 op_sel:[0,0,1]
	v_cvt_pk_fp8_f32 v156, v10, v14 op_sel:[0,0,1]
	v_cvt_pk_fp8_f32 v157, v26, v30 op_sel:[0,0,1]
	v_cvt_pk_fp8_f32 v158, v42, v46 op_sel:[0,0,1]
	v_cvt_pk_fp8_f32 v159, v58, v62 op_sel:[0,0,1]
	v_cvt_pk_fp8_f32 v160, v11, v15 op_sel:[0,0,1]
	v_cvt_pk_fp8_f32 v161, v27, v31 op_sel:[0,0,1]
	v_cvt_pk_fp8_f32 v162, v43, v47 op_sel:[0,0,1]
	v_cvt_pk_fp8_f32 v163, v59, v63 op_sel:[0,0,1]
	s_movk_i32 s1, 0x200
	s_cmp_eq_u32 s14, 0
	s_cselect_b32 s0, 13, 11
	s_cselect_b32 s1, 0x800, s1
	v_lshlrev_b32_e32 v167, 4, v164
	v_lshl_add_u32 v167, v165, s0, v167
	global_store_dwordx4 v167, v[148:151], s[12:13]
	v_add_u32_e32 v167, s1, v167
	global_store_dwordx4 v167, v[152:155], s[12:13]
	v_add_u32_e32 v167, s1, v167
	global_store_dwordx4 v167, v[156:159], s[12:13]
	v_add_u32_e32 v167, s1, v167
	global_store_dwordx4 v167, v[160:163], s[12:13]
	s_nop 1
	s_waitcnt vmcnt(0)
; #define LAS __attribute__((address_space(3)))
; __device__ __forceinline__ float clamp8(float x) { return __builtin_amdgcn_fmed3f(x, -448.f, 448.f); }
; __device__ __forceinline__ void cvt_finish(const CvtDesc& d, const float (&t)[64], LAS float* scr, int lane) {
;     ...
;     if (d.f8) {
; #pragma unroll
;         for (int j = 0; j < 8; ++j) { const int n = (lane >> 3) + 8 * j; const LAS float* s = scr + (8 * c) * 65 + n;
;             int a = __builtin_amdgcn_cvt_pk_fp8_f32(clamp8(s[0 * 65] * W8_SCALE), clamp8(s[1 * 65] * W8_SCALE), 0, false); a = __builtin_amdgcn_cvt_pk_fp8_f32(clamp8(s[2 * 65] * W8_SCALE), clamp8(s[3 * 65] * W8_SCALE), a, true);
;             int b = __builtin_amdgcn_cvt_pk_fp8_f32(clamp8(s[4 * 65] * W8_SCALE), clamp8(s[5 * 65] * W8_SCALE), 0, false); b = __builtin_amdgcn_cvt_pk_fp8_f32(clamp8(s[6 * 65] * W8_SCALE), clamp8(s[7 * 65] * W8_SCALE), b, true);
;             __builtin_nontemporal_store((u32x2){(unsigned)a, (unsigned)b}, (u32x2*)(d.dst + (size_t)n * d.dKB + 8 * c)); }
	v_mul_f32_e32 v64, 0x42800000, v64
	v_mul_f32_e32 v65, 0x42800000, v65
	v_mul_f32_e32 v66, 0x42800000, v66
	v_mul_f32_e32 v67, 0x42800000, v67
	v_mul_f32_e32 v68, 0x42800000, v68
	v_mul_f32_e32 v69, 0x42800000, v69
	v_mul_f32_e32 v70, 0x42800000, v70
	v_mul_f32_e32 v71, 0x42800000, v71
	v_mul_f32_e32 v72, 0x42800000, v72
	v_mul_f32_e32 v73, 0x42800000, v73
	v_mul_f32_e32 v74, 0x42800000, v74
	v_mul_f32_e32 v75, 0x42800000, v75
	v_mul_f32_e32 v76, 0x42800000, v76
	v_mul_f32_e32 v77, 0x42800000, v77
	v_mul_f32_e32 v78, 0x42800000, v78
	v_mul_f32_e32 v79, 0x42800000, v79
	v_mul_f32_e32 v80, 0x42800000, v80
	v_mul_f32_e32 v81, 0x42800000, v81
	v_mul_f32_e32 v82, 0x42800000, v82
	v_mul_f32_e32 v83, 0x42800000, v83
	v_mul_f32_e32 v84, 0x42800000, v84
	v_mul_f32_e32 v85, 0x42800000, v85
	v_mul_f32_e32 v86, 0x42800000, v86
	v_mul_f32_e32 v87, 0x42800000, v87
	v_mul_f32_e32 v88, 0x42800000, v88
	v_mul_f32_e32 v89, 0x42800000, v89
	v_mul_f32_e32 v90, 0x42800000, v90
	v_mul_f32_e32 v91, 0x42800000, v91
	v_mul_f32_e32 v92, 0x42800000, v92
	v_mul_f32_e32 v93, 0x42800000, v93
	v_mul_f32_e32 v94, 0x42800000, v94
	v_mul_f32_e32 v95, 0x42800000, v95
	v_mul_f32_e32 v96, 0x42800000, v96
	v_mul_f32_e32 v97, 0x42800000, v97
	v_mul_f32_e32 v98, 0x42800000, v98
	v_mul_f32_e32 v99, 0x42800000, v99
	v_mul_f32_e32 v100, 0x42800000, v100
	v_mul_f32_e32 v101, 0x42800000, v101
	v_mul_f32_e32 v102, 0x42800000, v102
	v_mul_f32_e32 v103, 0x42800000, v103
	v_mul_f32_e32 v104, 0x42800000, v104
	v_mul_f32_e32 v105, 0x42800000, v105
	v_mul_f32_e32 v106, 0x42800000, v106
	v_mul_f32_e32 v107, 0x42800000, v107
	v_mul_f32_e32 v108, 0x42800000, v108
	v_mul_f32_e32 v109, 0x42800000, v109
	v_mul_f32_e32 v110, 0x42800000, v110
	v_mul_f32_e32 v111, 0x42800000, v111
	v_mul_f32_e32 v112, 0x42800000, v112
	v_mul_f32_e32 v113, 0x42800000, v113
	v_mul_f32_e32 v114, 0x42800000, v114
	v_mul_f32_e32 v115, 0x42800000, v115
	v_mul_f32_e32 v116, 0x42800000, v116
	v_mul_f32_e32 v117, 0x42800000, v117
	v_mul_f32_e32 v118, 0x42800000, v118
	v_mul_f32_e32 v119, 0x42800000, v119
	v_mul_f32_e32 v120, 0x42800000, v120
	v_mul_f32_e32 v121, 0x42800000, v121
	v_mul_f32_e32 v122, 0x42800000, v122
	v_mul_f32_e32 v123, 0x42800000, v123
	v_mul_f32_e32 v124, 0x42800000, v124
	v_mul_f32_e32 v125, 0x42800000, v125
	v_mul_f32_e32 v126, 0x42800000, v126
	v_mul_f32_e32 v127, 0x42800000, v127
	v_med3_f32 v64, v64, s93, v224
	v_med3_f32 v65, v65, s93, v224
	v_med3_f32 v66, v66, s93, v224
	v_med3_f32 v67, v67, s93, v224
	v_med3_f32 v68, v68, s93, v224
	v_med3_f32 v69, v69, s93, v224
	v_med3_f32 v70, v70, s93, v224
	v_med3_f32 v71, v71, s93, v224
	v_med3_f32 v72, v72, s93, v224
	v_med3_f32 v73, v73, s93, v224
	v_med3_f32 v74, v74, s93, v224
	v_med3_f32 v75, v75, s93, v224
	v_med3_f32 v76, v76, s93, v224
	v_med3_f32 v77, v77, s93, v224
	v_med3_f32 v78, v78, s93, v224
	v_med3_f32 v79, v79, s93, v224
	v_med3_f32 v80, v80, s93, v224
	v_med3_f32 v81, v81, s93, v224
	v_med3_f32 v82, v82, s93, v224
	v_med3_f32 v83, v83, s93, v224
	v_med3_f32 v84, v84, s93, v224
	v_med3_f32 v85, v85, s93, v224
	v_med3_f32 v86, v86, s93, v224
	v_med3_f32 v87, v87, s93, v224
	v_med3_f32 v88, v88, s93, v224
	v_med3_f32 v89, v89, s93, v224
	v_med3_f32 v90, v90, s93, v224
	v_med3_f32 v91, v91, s93, v224
	v_med3_f32 v92, v92, s93, v224
	v_med3_f32 v93, v93, s93, v224
	v_med3_f32 v94, v94, s93, v224
	v_med3_f32 v95, v95, s93, v224
	v_med3_f32 v96, v96, s93, v224
	v_med3_f32 v97, v97, s93, v224
	v_med3_f32 v98, v98, s93, v224
	v_med3_f32 v99, v99, s93, v224
	v_med3_f32 v100, v100, s93, v224
	v_med3_f32 v101, v101, s93, v224
	v_med3_f32 v102, v102, s93, v224
	v_med3_f32 v103, v103, s93, v224
	v_med3_f32 v104, v104, s93, v224
	v_med3_f32 v105, v105, s93, v224
	v_med3_f32 v106, v106, s93, v224
	v_med3_f32 v107, v107, s93, v224
	v_med3_f32 v108, v108, s93, v224
	v_med3_f32 v109, v109, s93, v224
	v_med3_f32 v110, v110, s93, v224
	v_med3_f32 v111, v111, s93, v224
	v_med3_f32 v112, v112, s93, v224
	v_med3_f32 v113, v113, s93, v224
	v_med3_f32 v114, v114, s93, v224
	v_med3_f32 v115, v115, s93, v224
	v_med3_f32 v116, v116, s93, v224
	v_med3_f32 v117, v117, s93, v224
	v_med3_f32 v118, v118, s93, v224
	v_med3_f32 v119, v119, s93, v224
	v_med3_f32 v120, v120, s93, v224
	v_med3_f32 v121, v121, s93, v224
	v_med3_f32 v122, v122, s93, v224
	v_med3_f32 v123, v123, s93, v224
	v_med3_f32 v124, v124, s93, v224
	v_med3_f32 v125, v125, s93, v224
	v_med3_f32 v126, v126, s93, v224
	v_med3_f32 v127, v127, s93, v224
	v_cvt_pk_fp8_f32 v148, v64, v68
	v_cvt_pk_fp8_f32 v149, v80, v84
	v_cvt_pk_fp8_f32 v150, v96, v100
	v_cvt_pk_fp8_f32 v151, v112, v116
	v_cvt_pk_fp8_f32 v152, v65, v69
	v_cvt_pk_fp8_f32 v153, v81, v85
	v_cvt_pk_fp8_f32 v154, v97, v101
	v_cvt_pk_fp8_f32 v155, v113, v117
	v_cvt_pk_fp8_f32 v156, v66, v70
	v_cvt_pk_fp8_f32 v157, v82, v86
	v_cvt_pk_fp8_f32 v158, v98, v102
	v_cvt_pk_fp8_f32 v159, v114, v118
	v_cvt_pk_fp8_f32 v160, v67, v71
	v_cvt_pk_fp8_f32 v161, v83, v87
	v_cvt_pk_fp8_f32 v162, v99, v103
	v_cvt_pk_fp8_f32 v163, v115, v119
	v_cvt_pk_fp8_f32 v148, v72, v76 op_sel:[0,0,1]
	v_cvt_pk_fp8_f32 v149, v88, v92 op_sel:[0,0,1]
	v_cvt_pk_fp8_f32 v150, v104, v108 op_sel:[0,0,1]
	v_cvt_pk_fp8_f32 v151, v120, v124 op_sel:[0,0,1]
	v_cvt_pk_fp8_f32 v152, v73, v77 op_sel:[0,0,1]
	v_cvt_pk_fp8_f32 v153, v89, v93 op_sel:[0,0,1]
	v_cvt_pk_fp8_f32 v154, v105, v109 op_sel:[0,0,1]
	v_cvt_pk_fp8_f32 v155, v121, v125 op_sel:[0,0,1]
	v_cvt_pk_fp8_f32 v156, v74, v78 op_sel:[0,0,1]
	v_cvt_pk_fp8_f32 v157, v90, v94 op_sel:[0,0,1]
	v_cvt_pk_fp8_f32 v158, v106, v110 op_sel:[0,0,1]
	v_cvt_pk_fp8_f32 v159, v122, v126 op_sel:[0,0,1]
	v_cvt_pk_fp8_f32 v160, v75, v79 op_sel:[0,0,1]
	v_cvt_pk_fp8_f32 v161, v91, v95 op_sel:[0,0,1]
	v_cvt_pk_fp8_f32 v162, v107, v111 op_sel:[0,0,1]
	v_cvt_pk_fp8_f32 v163, v123, v127 op_sel:[0,0,1]
	s_movk_i32 s1, 0x200
	s_cmp_eq_u32 s18, 0
	s_cselect_b32 s0, 13, 11
	s_cselect_b32 s1, 0x800, s1
	v_lshlrev_b32_e32 v167, 4, v164
	v_lshl_add_u32 v167, v165, s0, v167
	global_store_dwordx4 v167, v[148:151], s[16:17]
	v_add_u32_e32 v167, s1, v167
	global_store_dwordx4 v167, v[152:155], s[16:17]
	v_add_u32_e32 v167, s1, v167
	global_store_dwordx4 v167, v[156:159], s[16:17]
	v_add_u32_e32 v167, s1, v167
	global_store_dwordx4 v167, v[160:163], s[16:17]
	s_nop 1
	s_branch .LBB0_779

; __device__ __forceinline__ void cvt_load(const CvtDesc& d, float (&t)[64], int lane) {
;     const float* p = d.src + (size_t)(lane >> 4) * d.N + 4 * (lane & 15);
; #pragma unroll
;     for (int i = 0; i < 16; ++i) { const f32x4 v = __builtin_nontemporal_load((const f32x4*)(p + (size_t)(4 * i) * d.N));
;         t[4 * i] = v.x; t[4 * i + 1] = v.y; t[4 * i + 2] = v.z; t[4 * i + 3] = v.w; }
; }
.Lcv_dd4:
	v_lshlrev_b32_e32 v166, 4, v165
	v_lshl_add_u32 v166, v164, s19, v166
	global_load_dwordx4 v[0:3], v166, s[10:11] nt
	v_add_u32_e32 v166, s15, v166
	global_load_dwordx4 v[4:7], v166, s[10:11] nt
	v_add_u32_e32 v166, s15, v166
	global_load_dwordx4 v[8:11], v166, s[10:11] nt
	v_add_u32_e32 v166, s15, v166
	global_load_dwordx4 v[12:15], v166, s[10:11] nt
	v_add_u32_e32 v166, s15, v166
	global_load_dwordx4 v[16:19], v166, s[10:11] nt
	v_add_u32_e32 v166, s15, v166
	global_load_dwordx4 v[20:23], v166, s[10:11] nt
	v_add_u32_e32 v166, s15, v166
	global_load_dwordx4 v[24:27], v166, s[10:11] nt
	v_add_u32_e32 v166, s15, v166
	global_load_dwordx4 v[28:31], v166, s[10:11] nt
	v_add_u32_e32 v166, s15, v166
	global_load_dwordx4 v[32:35], v166, s[10:11] nt
	v_add_u32_e32 v166, s15, v166
	global_load_dwordx4 v[36:39], v166, s[10:11] nt
	v_add_u32_e32 v166, s15, v166
	global_load_dwordx4 v[40:43], v166, s[10:11] nt
	v_add_u32_e32 v166, s15, v166
	global_load_dwordx4 v[44:47], v166, s[10:11] nt
	v_add_u32_e32 v166, s15, v166
	global_load_dwordx4 v[48:51], v166, s[10:11] nt
	v_add_u32_e32 v166, s15, v166
	global_load_dwordx4 v[52:55], v166, s[10:11] nt
	v_add_u32_e32 v166, s15, v166
	global_load_dwordx4 v[56:59], v166, s[10:11] nt
	v_add_u32_e32 v166, s15, v166
	global_load_dwordx4 v[60:63], v166, s[10:11] nt
	s_waitcnt vmcnt(0)
; #define LAS __attribute__((address_space(3)))
; __device__ __forceinline__ float clamp8(float x) { return __builtin_amdgcn_fmed3f(x, -448.f, 448.f); }
; #define LDS_WAIT() asm volatile("s_waitcnt lgkmcnt(0)" ::: "memory")
; __device__ __forceinline__ void cvt_load(const CvtDesc& d, float (&t)[64], int lane) {
;     const float* p = d.src + (size_t)(lane >> 4) * d.N + 4 * (lane & 15);
; #pragma unroll
;     for (int i = 0; i < 16; ++i) { const f32x4 v = __builtin_nontemporal_load((const f32x4*)(p + (size_t)(4 * i) * d.N));
;         t[4 * i] = v.x; t[4 * i + 1] = v.y; t[4 * i + 2] = v.z; t[4 * i + 3] = v.w; }
; }
; __device__ __forceinline__ void cvt_finish(const CvtDesc& d, const float (&t)[64], LAS float* scr, int lane) {
;     LAS float* sw = scr + (lane >> 4) * 65 + 4 * (lane & 15);
; #pragma unroll
;     for (int i = 0; i < 16; ++i) { sw[(4 * i) * 65] = t[4 * i]; sw[(4 * i) * 65 + 1] = t[4 * i + 1]; sw[(4 * i) * 65 + 2] = t[4 * i + 2]; sw[(4 * i) * 65 + 3] = t[4 * i + 3]; }
;     LDS_WAIT();
;     const int c = lane & 7;
;     if (d.f8) {
; #pragma unroll
;         for (int j = 0; j < 8; ++j) { const int n = (lane >> 3) + 8 * j; const LAS float* s = scr + (8 * c) * 65 + n;
;             int a = __builtin_amdgcn_cvt_pk_fp8_f32(clamp8(s[0 * 65] * W8_SCALE), clamp8(s[1 * 65] * W8_SCALE), 0, false); a = __builtin_amdgcn_cvt_pk_fp8_f32(clamp8(s[2 * 65] * W8_SCALE), clamp8(s[3 * 65] * W8_SCALE), a, true);
;             int b = __builtin_amdgcn_cvt_pk_fp8_f32(clamp8(s[4 * 65] * W8_SCALE), clamp8(s[5 * 65] * W8_SCALE), 0, false); b = __builtin_amdgcn_cvt_pk_fp8_f32(clamp8(s[6 * 65] * W8_SCALE), clamp8(s[7 * 65] * W8_SCALE), b, true);
;             __builtin_nontemporal_store((u32x2){(unsigned)a, (unsigned)b}, (u32x2*)(d.dst + (size_t)n * d.dKB + 8 * c)); }
	v_mul_f32_e32 v0, 0x42800000, v0
	v_mul_f32_e32 v1, 0x42800000, v1
	v_mul_f32_e32 v2, 0x42800000, v2
	v_mul_f32_e32 v3, 0x42800000, v3
	v_mul_f32_e32 v4, 0x42800000, v4
	v_mul_f32_e32 v5, 0x42800000, v5
	v_mul_f32_e32 v6, 0x42800000, v6
	v_mul_f32_e32 v7, 0x42800000, v7
	v_mul_f32_e32 v8, 0x42800000, v8
	v_mul_f32_e32 v9, 0x42800000, v9
	v_mul_f32_e32 v10, 0x42800000, v10
	v_mul_f32_e32 v11, 0x42800000, v11
	v_mul_f32_e32 v12, 0x42800000, v12
	v_mul_f32_e32 v13, 0x42800000, v13
	v_mul_f32_e32 v14, 0x42800000, v14
	v_mul_f32_e32 v15, 0x42800000, v15
	v_mul_f32_e32 v16, 0x42800000, v16
	v_mul_f32_e32 v17, 0x42800000, v17
	v_mul_f32_e32 v18, 0x42800000, v18
	v_mul_f32_e32 v19, 0x42800000, v19
	v_mul_f32_e32 v20, 0x42800000, v20
	v_mul_f32_e32 v21, 0x42800000, v21
	v_mul_f32_e32 v22, 0x42800000, v22
	v_mul_f32_e32 v23, 0x42800000, v23
	v_mul_f32_e32 v24, 0x42800000, v24
	v_mul_f32_e32 v25, 0x42800000, v25
	v_mul_f32_e32 v26, 0x42800000, v26
	v_mul_f32_e32 v27, 0x42800000, v27
	v_mul_f32_e32 v28, 0x42800000, v28
	v_mul_f32_e32 v29, 0x42800000, v29
	v_mul_f32_e32 v30, 0x42800000, v30
	v_mul_f32_e32 v31, 0x42800000, v31
	v_mul_f32_e32 v32, 0x42800000, v32
	v_mul_f32_e32 v33, 0x42800000, v33
	v_mul_f32_e32 v34, 0x42800000, v34
	v_mul_f32_e32 v35, 0x42800000, v35
	v_mul_f32_e32 v36, 0x42800000, v36
	v_mul_f32_e32 v37, 0x42800000, v37
	v_mul_f32_e32 v38, 0x42800000, v38
	v_mul_f32_e32 v39, 0x42800000, v39
	v_mul_f32_e32 v40, 0x42800000, v40
	v_mul_f32_e32 v41, 0x42800000, v41
	v_mul_f32_e32 v42, 0x42800000, v42
	v_mul_f32_e32 v43, 0x42800000, v43
	v_mul_f32_e32 v44, 0x42800000, v44
	v_mul_f32_e32 v45, 0x42800000, v45
	v_mul_f32_e32 v46, 0x42800000, v46
	v_mul_f32_e32 v47, 0x42800000, v47
	v_mul_f32_e32 v48, 0x42800000, v48
	v_mul_f32_e32 v49, 0x42800000, v49
	v_mul_f32_e32 v50, 0x42800000, v50
	v_mul_f32_e32 v51, 0x42800000, v51
	v_mul_f32_e32 v52, 0x42800000, v52
	v_mul_f32_e32 v53, 0x42800000, v53
	v_mul_f32_e32 v54, 0x42800000, v54
	v_mul_f32_e32 v55, 0x42800000, v55
	v_mul_f32_e32 v56, 0x42800000, v56
	v_mul_f32_e32 v57, 0x42800000, v57
	v_mul_f32_e32 v58, 0x42800000, v58
	v_mul_f32_e32 v59, 0x42800000, v59
	v_mul_f32_e32 v60, 0x42800000, v60
	v_mul_f32_e32 v61, 0x42800000, v61
	v_mul_f32_e32 v62, 0x42800000, v62
	v_mul_f32_e32 v63, 0x42800000, v63
	v_med3_f32 v0, v0, s93, v224
	v_med3_f32 v1, v1, s93, v224
	v_med3_f32 v2, v2, s93, v224
	v_med3_f32 v3, v3, s93, v224
	v_med3_f32 v4, v4, s93, v224
	v_med3_f32 v5, v5, s93, v224
	v_med3_f32 v6, v6, s93, v224
	v_med3_f32 v7, v7, s93, v224
	v_med3_f32 v8, v8, s93, v224
	v_med3_f32 v9, v9, s93, v224
	v_med3_f32 v10, v10, s93, v224
	v_med3_f32 v11, v11, s93, v224
	v_med3_f32 v12, v12, s93, v224
	v_med3_f32 v13, v13, s93, v224
	v_med3_f32 v14, v14, s93, v224
	v_med3_f32 v15, v15, s93, v224
	v_med3_f32 v16, v16, s93, v224
	v_med3_f32 v17, v17, s93, v224
	v_med3_f32 v18, v18, s93, v224
	v_med3_f32 v19, v19, s93, v224
	v_med3_f32 v20, v20, s93, v224
	v_med3_f32 v21, v21, s93, v224
	v_med3_f32 v22, v22, s93, v224
	v_med3_f32 v23, v23, s93, v224
	v_med3_f32 v24, v24, s93, v224
	v_med3_f32 v25, v25, s93, v224
	v_med3_f32 v26, v26, s93, v224
	v_med3_f32 v27, v27, s93, v224
	v_med3_f32 v28, v28, s93, v224
	v_med3_f32 v29, v29, s93, v224
	v_med3_f32 v30, v30, s93, v224
	v_med3_f32 v31, v31, s93, v224
	v_med3_f32 v32, v32, s93, v224
	v_med3_f32 v33, v33, s93, v224
	v_med3_f32 v34, v34, s93, v224
	v_med3_f32 v35, v35, s93, v224
	v_med3_f32 v36, v36, s93, v224
	v_med3_f32 v37, v37, s93, v224
	v_med3_f32 v38, v38, s93, v224
	v_med3_f32 v39, v39, s93, v224
	v_med3_f32 v40, v40, s93, v224
	v_med3_f32 v41, v41, s93, v224
	v_med3_f32 v42, v42, s93, v224
	v_med3_f32 v43, v43, s93, v224
	v_med3_f32 v44, v44, s93, v224
	v_med3_f32 v45, v45, s93, v224
	v_med3_f32 v46, v46, s93, v224
	v_med3_f32 v47, v47, s93, v224
	v_med3_f32 v48, v48, s93, v224
	v_med3_f32 v49, v49, s93, v224
	v_med3_f32 v50, v50, s93, v224
	v_med3_f32 v51, v51, s93, v224
	v_med3_f32 v52, v52, s93, v224
	v_med3_f32 v53, v53, s93, v224
	v_med3_f32 v54, v54, s93, v224
	v_med3_f32 v55, v55, s93, v224
	v_med3_f32 v56, v56, s93, v224
	v_med3_f32 v57, v57, s93, v224
	v_med3_f32 v58, v58, s93, v224
	v_med3_f32 v59, v59, s93, v224
	v_med3_f32 v60, v60, s93, v224
	v_med3_f32 v61, v61, s93, v224
	v_med3_f32 v62, v62, s93, v224
	v_med3_f32 v63, v63, s93, v224
	v_cvt_pk_fp8_f32 v148, v0, v4
	v_cvt_pk_fp8_f32 v149, v16, v20
	v_cvt_pk_fp8_f32 v150, v32, v36
	v_cvt_pk_fp8_f32 v151, v48, v52
	v_cvt_pk_fp8_f32 v152, v1, v5
	v_cvt_pk_fp8_f32 v153, v17, v21
	v_cvt_pk_fp8_f32 v154, v33, v37
	v_cvt_pk_fp8_f32 v155, v49, v53
	v_cvt_pk_fp8_f32 v156, v2, v6
	v_cvt_pk_fp8_f32 v157, v18, v22
	v_cvt_pk_fp8_f32 v158, v34, v38
	v_cvt_pk_fp8_f32 v159, v50, v54
	v_cvt_pk_fp8_f32 v160, v3, v7
	v_cvt_pk_fp8_f32 v161, v19, v23
	v_cvt_pk_fp8_f32 v162, v35, v39
	v_cvt_pk_fp8_f32 v163, v51, v55
	v_cvt_pk_fp8_f32 v148, v8, v12 op_sel:[0,0,1]
	v_cvt_pk_fp8_f32 v149, v24, v28 op_sel:[0,0,1]
	v_cvt_pk_fp8_f32 v150, v40, v44 op_sel:[0,0,1]
	v_cvt_pk_fp8_f32 v151, v56, v60 op_sel:[0,0,1]
	v_cvt_pk_fp8_f32 v152, v9, v13 op_sel:[0,0,1]
	v_cvt_pk_fp8_f32 v153, v25, v29 op_sel:[0,0,1]
	v_cvt_pk_fp8_f32 v154, v41, v45 op_sel:[0,0,1]
	v_cvt_pk_fp8_f32 v155, v57, v61 op_sel:[0,0,1]
	v_cvt_pk_fp8_f32 v156, v10, v14 op_sel:[0,0,1]
	v_cvt_pk_fp8_f32 v157, v26, v30 op_sel:[0,0,1]
	v_cvt_pk_fp8_f32 v158, v42, v46 op_sel:[0,0,1]
	v_cvt_pk_fp8_f32 v159, v58, v62 op_sel:[0,0,1]
	v_cvt_pk_fp8_f32 v160, v11, v15 op_sel:[0,0,1]
	v_cvt_pk_fp8_f32 v161, v27, v31 op_sel:[0,0,1]
	v_cvt_pk_fp8_f32 v162, v43, v47 op_sel:[0,0,1]
	v_cvt_pk_fp8_f32 v163, v59, v63 op_sel:[0,0,1]
	s_movk_i32 s1, 0x200
	s_cmp_eq_u32 s14, 0
	s_cselect_b32 s0, 13, 11
	s_cselect_b32 s1, 0x800, s1
	v_lshlrev_b32_e32 v167, 4, v164
	v_lshl_add_u32 v167, v165, s0, v167
	global_store_dwordx4 v167, v[148:151], s[12:13]
	v_add_u32_e32 v167, s1, v167
	global_store_dwordx4 v167, v[152:155], s[12:13]
	v_add_u32_e32 v167, s1, v167
	global_store_dwordx4 v167, v[156:159], s[12:13]
	v_add_u32_e32 v167, s1, v167
	global_store_dwordx4 v167, v[160:163], s[12:13]
	s_nop 1
	s_add_u32 s68, s68, 1
	s_cmp_lt_u32 s68, 4
	s_cbranch_scc1 .Lcv_sl_cv1
	s_branch .LBB0_779

; #define LAS __attribute__((address_space(3)))
; #define LDS_WAIT() asm volatile("s_waitcnt lgkmcnt(0)" ::: "memory")
; __device__ __forceinline__ void cvt_load(const CvtDesc& d, float (&t)[64], int lane) {
;     const float* p = d.src + (size_t)(lane >> 4) * d.N + 4 * (lane & 15);
; #pragma unroll
;     for (int i = 0; i < 16; ++i) { const f32x4 v = __builtin_nontemporal_load((const f32x4*)(p + (size_t)(4 * i) * d.N));
;         t[4 * i] = v.x; t[4 * i + 1] = v.y; t[4 * i + 2] = v.z; t[4 * i + 3] = v.w; }
; }
; __device__ __forceinline__ void cvt_finish(const CvtDesc& d, const float (&t)[64], LAS float* scr, int lane) {
;     LAS float* sw = scr + (lane >> 4) * 65 + 4 * (lane & 15);
; #pragma unroll
;     for (int i = 0; i < 16; ++i) { sw[(4 * i) * 65] = t[4 * i]; sw[(4 * i) * 65 + 1] = t[4 * i + 1]; sw[(4 * i) * 65 + 2] = t[4 * i + 2]; sw[(4 * i) * 65 + 3] = t[4 * i + 3]; }
;     LDS_WAIT();
;     const int c = lane & 7;
;     if (d.f8) {
; #pragma unroll
;         for (int j = 0; j < 8; ++j) { const int n = (lane >> 3) + 8 * j; const LAS float* s = scr + (8 * c) * 65 + n;
.LBB0_902:
	v_mul_u32_u24_e32 v2, s0, v9
	v_lshlrev_b32_e32 v192, 2, v2
	v_lshl_add_u64 v[0:1], v[0:1], 0, v[192:193]
	v_mov_b32_e32 v7, v193
	v_lshl_add_u64 v[0:1], v[0:1], 0, v[6:7]
	s_lshl_b32 s68, s0, 4
	global_load_dwordx4 v[20:23], v[0:1], off nt
	v_lshl_add_u64 v[0:1], v[0:1], 0, s[68:69]
	global_load_dwordx4 v[24:27], v[0:1], off nt
	v_lshl_add_u64 v[0:1], v[0:1], 0, s[68:69]
	global_load_dwordx4 v[28:31], v[0:1], off nt
	v_lshl_add_u64 v[0:1], v[0:1], 0, s[68:69]
	global_load_dwordx4 v[32:35], v[0:1], off nt
	v_lshl_add_u64 v[0:1], v[0:1], 0, s[68:69]
	global_load_dwordx4 v[36:39], v[0:1], off nt
	v_lshl_add_u64 v[0:1], v[0:1], 0, s[68:69]
	global_load_dwordx4 v[40:43], v[0:1], off nt
	v_lshl_add_u64 v[0:1], v[0:1], 0, s[68:69]
	global_load_dwordx4 v[44:47], v[0:1], off nt
	v_lshl_add_u64 v[0:1], v[0:1], 0, s[68:69]
	global_load_dwordx4 v[48:51], v[0:1], off nt
	v_lshl_add_u64 v[0:1], v[0:1], 0, s[68:69]
	global_load_dwordx4 v[52:55], v[0:1], off nt
	v_lshl_add_u64 v[0:1], v[0:1], 0, s[68:69]
	global_load_dwordx4 v[56:59], v[0:1], off nt
	v_lshl_add_u64 v[0:1], v[0:1], 0, s[68:69]
	global_load_dwordx4 v[60:63], v[0:1], off nt
	v_lshl_add_u64 v[0:1], v[0:1], 0, s[68:69]
	global_load_dwordx4 v[64:67], v[0:1], off nt
	v_lshl_add_u64 v[0:1], v[0:1], 0, s[68:69]
	global_load_dwordx4 v[68:71], v[0:1], off nt
	v_lshl_add_u64 v[0:1], v[0:1], 0, s[68:69]
	global_load_dwordx4 v[72:75], v[0:1], off nt
	v_lshl_add_u64 v[0:1], v[0:1], 0, s[68:69]
	global_load_dwordx4 v[76:79], v[0:1], off nt
	v_lshl_add_u64 v[0:1], v[0:1], 0, s[68:69]
	global_load_dwordx4 v[0:3], v[0:1], off nt
	v_add_u32_e32 v7, 0x410, v10
	s_waitcnt vmcnt(0)
	ds_write2_b32 v10, v20, v21 offset1:1
	ds_write2_b32 v10, v22, v23 offset0:2 offset1:3
	v_mov_b32_e32 v22, v193
	ds_write2_b32 v7, v24, v25 offset1:1
	v_add_u32_e32 v7, 0x418, v10
	ds_write2_b32 v7, v26, v27 offset1:1
	v_add_u32_e32 v7, 0x820, v10
	ds_write2_b32 v7, v28, v29 offset1:1
	v_add_u32_e32 v7, 0x828, v10
	ds_write2_b32 v7, v30, v31 offset1:1
	v_add_u32_e32 v7, 0xc30, v10
	ds_write2_b32 v7, v32, v33 offset1:1
	v_add_u32_e32 v7, 0xc38, v10
	ds_write2_b32 v7, v34, v35 offset1:1
	v_add_u32_e32 v7, 0x1040, v10
	ds_write2_b32 v7, v36, v37 offset1:1
	v_add_u32_e32 v7, 0x1048, v10
	ds_write2_b32 v7, v38, v39 offset1:1
	v_add_u32_e32 v7, 0x1450, v10
	ds_write2_b32 v7, v40, v41 offset1:1
	v_add_u32_e32 v7, 0x1458, v10
	ds_write2_b32 v7, v42, v43 offset1:1
	v_add_u32_e32 v7, 0x1860, v10
	ds_write2_b32 v7, v44, v45 offset1:1
	v_add_u32_e32 v7, 0x1868, v10
	ds_write2_b32 v7, v46, v47 offset1:1
	v_add_u32_e32 v7, 0x1c70, v10
	ds_write2_b32 v7, v48, v49 offset1:1
	v_add_u32_e32 v7, 0x1c78, v10
	ds_write2_b32 v7, v50, v51 offset1:1
	v_add_u32_e32 v7, 0x2080, v10
	ds_write2_b32 v7, v52, v53 offset1:1
	v_add_u32_e32 v7, 0x2088, v10
	ds_write2_b32 v7, v54, v55 offset1:1
	v_add_u32_e32 v7, 0x2490, v10
	ds_write2_b32 v7, v56, v57 offset1:1
	v_add_u32_e32 v7, 0x2498, v10
	ds_write2_b32 v7, v58, v59 offset1:1
	v_add_u32_e32 v7, 0x28a0, v10
	ds_write2_b32 v7, v60, v61 offset1:1
	v_add_u32_e32 v7, 0x28a8, v10
	ds_write2_b32 v7, v62, v63 offset1:1
	v_add_u32_e32 v7, 0x2cb0, v10
	ds_write2_b32 v7, v64, v65 offset1:1
	v_add_u32_e32 v7, 0x2cb8, v10
	ds_write2_b32 v7, v66, v67 offset1:1
	v_add_u32_e32 v7, 0x30c0, v10
	ds_write2_b32 v7, v68, v69 offset1:1
	v_add_u32_e32 v7, 0x30c8, v10
	ds_write2_b32 v7, v70, v71 offset1:1
	v_add_u32_e32 v7, 0x34d0, v10
	ds_write2_b32 v7, v72, v73 offset1:1
	v_add_u32_e32 v7, 0x34d8, v10
	ds_write2_b32 v7, v74, v75 offset1:1
	v_add_u32_e32 v7, 0x38e0, v10
	ds_write2_b32 v7, v76, v77 offset1:1
	v_add_u32_e32 v7, 0x38e8, v10
	ds_write2_b32 v7, v78, v79 offset1:1
	v_add_u32_e32 v7, 0x3cf0, v10
	ds_write2_b32 v7, v0, v1 offset1:1
	v_add_u32_e32 v0, 0x3cf8, v10
	ds_write2_b32 v0, v2, v3 offset1:1
	s_waitcnt lgkmcnt(0)
	ds_read2_b32 v[2:3], v12 offset1:8
	ds_read2_b32 v[20:21], v12 offset0:65 offset1:73
	ds_read2_b32 v[24:25], v12 offset0:130 offset1:138
	ds_read2_b32 v[26:27], v12 offset0:195 offset1:203
	v_mov_b32_e32 v23, v193
	s_waitcnt lgkmcnt(3)
	v_mul_f32_e32 v0, 0x42800000, v2
	s_waitcnt lgkmcnt(2)
	v_mul_f32_e32 v1, 0x42800000, v20
	v_add_u32_e32 v2, 0x400, v12
	v_med3_f32 v0, v0, s93, v224
	v_med3_f32 v1, v1, s93, v224
	ds_read2_b32 v[28:29], v2 offset0:4 offset1:12
	ds_read2_b32 v[30:31], v2 offset0:69 offset1:77
	v_cvt_pk_fp8_f32 v22, v0, v1
	v_mul_f32_e32 v3, 0x42800000, v3
	v_mul_f32_e32 v7, 0x42800000, v21
	v_med3_f32 v3, v3, s93, v224
	v_med3_f32 v7, v7, s93, v224
	v_mov_b32_e32 v20, v193
	s_waitcnt lgkmcnt(3)
	v_mul_f32_e32 v0, 0x42800000, v24
	s_waitcnt lgkmcnt(2)
	v_mul_f32_e32 v1, 0x42800000, v26
	v_cvt_pk_fp8_f32 v20, v3, v7
	v_med3_f32 v0, v0, s93, v224
	v_med3_f32 v1, v1, s93, v224
	ds_read2_b32 v[32:33], v2 offset0:134 offset1:142
	ds_read2_b32 v[34:35], v2 offset0:199 offset1:207
	v_cvt_pk_fp8_f32 v22, v0, v1 op_sel:[0,0,1]
	s_waitcnt lgkmcnt(3)
	v_mul_f32_e32 v0, 0x42800000, v28
	s_waitcnt lgkmcnt(2)
	v_mul_f32_e32 v1, 0x42800000, v30
	v_mul_f32_e32 v3, 0x42800000, v25
	v_mul_f32_e32 v7, 0x42800000, v27
	v_med3_f32 v0, v0, s93, v224
	v_med3_f32 v1, v1, s93, v224
	v_med3_f32 v3, v3, s93, v224
	v_med3_f32 v7, v7, s93, v224
	v_cvt_pk_fp8_f32 v23, v0, v1
	v_cvt_pk_fp8_f32 v20, v3, v7 op_sel:[0,0,1]
	v_mul_f32_e32 v3, 0x42800000, v29
	v_mul_f32_e32 v7, 0x42800000, v31
	v_med3_f32 v3, v3, s93, v224
	v_med3_f32 v7, v7, s93, v224
	v_mov_b32_e32 v21, v193
	s_waitcnt lgkmcnt(1)
	v_mul_f32_e32 v0, 0x42800000, v32
	s_waitcnt lgkmcnt(0)
; #define LAS __attribute__((address_space(3)))
; __device__ __forceinline__ float clamp8(float x) { return __builtin_amdgcn_fmed3f(x, -448.f, 448.f); }
; __device__ __forceinline__ void cvt_finish(const CvtDesc& d, const float (&t)[64], LAS float* scr, int lane) {
;     ...
;     if (d.f8) {
; #pragma unroll
;         for (int j = 0; j < 8; ++j) { const int n = (lane >> 3) + 8 * j; const LAS float* s = scr + (8 * c) * 65 + n;
;             int a = __builtin_amdgcn_cvt_pk_fp8_f32(clamp8(s[0 * 65] * W8_SCALE), clamp8(s[1 * 65] * W8_SCALE), 0, false); a = __builtin_amdgcn_cvt_pk_fp8_f32(clamp8(s[2 * 65] * W8_SCALE), clamp8(s[3 * 65] * W8_SCALE), a, true);
;             int b = __builtin_amdgcn_cvt_pk_fp8_f32(clamp8(s[4 * 65] * W8_SCALE), clamp8(s[5 * 65] * W8_SCALE), 0, false); b = __builtin_amdgcn_cvt_pk_fp8_f32(clamp8(s[6 * 65] * W8_SCALE), clamp8(s[7 * 65] * W8_SCALE), b, true);
;             __builtin_nontemporal_store((u32x2){(unsigned)a, (unsigned)b}, (u32x2*)(d.dst + (size_t)n * d.dKB + 8 * c)); }
	v_mul_f32_e32 v1, 0x42800000, v34
	v_cvt_pk_fp8_f32 v21, v3, v7
	v_med3_f32 v0, v0, s93, v224
	v_med3_f32 v1, v1, s93, v224
	v_cvt_pk_fp8_f32 v23, v0, v1 op_sel:[0,0,1]
	v_mul_f32_e32 v3, 0x42800000, v33
	v_mul_f32_e32 v7, 0x42800000, v35
	v_mov_b64_e32 v[0:1], s[12:13]
	v_med3_f32 v3, v3, s93, v224
	v_med3_f32 v7, v7, s93, v224
	v_mad_u64_u32 v[36:37], s[0:1], s10, v11, v[0:1]
	v_cvt_pk_fp8_f32 v21, v3, v7 op_sel:[0,0,1]
	v_lshl_add_u64 v[36:37], v[36:37], 0, v[4:5]
	global_store_dwordx2 v[36:37], v[22:23], off
	v_mad_u64_u32 v[22:23], s[0:1], s10, v13, v[0:1]
	v_lshl_add_u64 v[22:23], v[22:23], 0, v[4:5]
	global_store_dwordx2 v[22:23], v[20:21], off
	ds_read2_b32 v[20:21], v12 offset0:16 offset1:24
	ds_read2_b32 v[22:23], v12 offset0:81 offset1:89
	ds_read2_b32 v[26:27], v12 offset0:146 offset1:154
	ds_read2_b32 v[28:29], v12 offset0:211 offset1:219
	v_mov_b32_e32 v24, v193
	s_waitcnt lgkmcnt(3)
	v_mul_f32_e32 v3, 0x42800000, v20
	s_waitcnt lgkmcnt(2)
	v_mul_f32_e32 v7, 0x42800000, v22
	v_med3_f32 v3, v3, s93, v224
	v_med3_f32 v7, v7, s93, v224
	ds_read2_b32 v[30:31], v2 offset0:20 offset1:28
	ds_read2_b32 v[32:33], v2 offset0:85 offset1:93
	v_cvt_pk_fp8_f32 v24, v3, v7
	s_waitcnt lgkmcnt(3)
	v_mul_f32_e32 v3, 0x42800000, v26
	s_waitcnt lgkmcnt(2)
	v_mul_f32_e32 v7, 0x42800000, v28
	v_med3_f32 v3, v3, s93, v224
	v_med3_f32 v7, v7, s93, v224
	ds_read2_b32 v[34:35], v2 offset0:150 offset1:158
	ds_read2_b32 v[36:37], v2 offset0:215 offset1:223
	v_cvt_pk_fp8_f32 v24, v3, v7 op_sel:[0,0,1]
	s_waitcnt lgkmcnt(3)
	v_mul_f32_e32 v3, 0x42800000, v30
	s_waitcnt lgkmcnt(2)
	v_mul_f32_e32 v7, 0x42800000, v32
	v_med3_f32 v3, v3, s93, v224
	v_med3_f32 v7, v7, s93, v224
	v_mov_b32_e32 v25, v193
	v_cvt_pk_fp8_f32 v25, v3, v7
	s_waitcnt lgkmcnt(1)
	v_mul_f32_e32 v3, 0x42800000, v34
	s_waitcnt lgkmcnt(0)
	v_mul_f32_e32 v7, 0x42800000, v36
	v_med3_f32 v3, v3, s93, v224
	v_med3_f32 v7, v7, s93, v224
	v_cvt_pk_fp8_f32 v25, v3, v7 op_sel:[0,0,1]
	v_mul_f32_e32 v3, 0x42800000, v21
	v_mul_f32_e32 v7, 0x42800000, v23
	v_med3_f32 v3, v3, s93, v224
	v_med3_f32 v7, v7, s93, v224
	v_mov_b32_e32 v20, v193
	v_cvt_pk_fp8_f32 v20, v3, v7
	v_mul_f32_e32 v3, 0x42800000, v27
	v_mul_f32_e32 v7, 0x42800000, v29
	v_med3_f32 v3, v3, s93, v224
	v_med3_f32 v7, v7, s93, v224
	v_cvt_pk_fp8_f32 v20, v3, v7 op_sel:[0,0,1]
	v_mul_f32_e32 v3, 0x42800000, v31
	v_mul_f32_e32 v7, 0x42800000, v33
	v_med3_f32 v3, v3, s93, v224
	v_med3_f32 v7, v7, s93, v224
	v_mov_b32_e32 v21, v193
	v_cvt_pk_fp8_f32 v21, v3, v7
	v_mul_f32_e32 v3, 0x42800000, v35
	v_mul_f32_e32 v7, 0x42800000, v37
	v_med3_f32 v3, v3, s93, v224
	v_med3_f32 v7, v7, s93, v224
	v_cvt_pk_fp8_f32 v21, v3, v7 op_sel:[0,0,1]
	v_mad_u64_u32 v[38:39], s[0:1], s10, v14, v[0:1]
	v_mad_u64_u32 v[22:23], s[0:1], s10, v15, v[0:1]
	v_lshl_add_u64 v[38:39], v[38:39], 0, v[4:5]
	v_lshl_add_u64 v[22:23], v[22:23], 0, v[4:5]
	global_store_dwordx2 v[38:39], v[24:25], off
	global_store_dwordx2 v[22:23], v[20:21], off
	ds_read2_b32 v[20:21], v12 offset0:32 offset1:40
	ds_read2_b32 v[22:23], v12 offset0:97 offset1:105
	ds_read2_b32 v[26:27], v12 offset0:162 offset1:170
	ds_read2_b32 v[28:29], v12 offset0:227 offset1:235
	v_mov_b32_e32 v24, v193
	s_waitcnt lgkmcnt(3)
	v_mul_f32_e32 v3, 0x42800000, v20
	s_waitcnt lgkmcnt(2)
	v_mul_f32_e32 v7, 0x42800000, v22
	v_med3_f32 v3, v3, s93, v224
	v_med3_f32 v7, v7, s93, v224
	ds_read2_b32 v[30:31], v2 offset0:36 offset1:44
	ds_read2_b32 v[32:33], v2 offset0:101 offset1:109
	v_cvt_pk_fp8_f32 v24, v3, v7
	s_waitcnt lgkmcnt(3)
	v_mul_f32_e32 v3, 0x42800000, v26
	s_waitcnt lgkmcnt(2)
	v_mul_f32_e32 v7, 0x42800000, v28
	v_med3_f32 v3, v3, s93, v224
	v_med3_f32 v7, v7, s93, v224
	ds_read2_b32 v[34:35], v2 offset0:166 offset1:174
	ds_read2_b32 v[36:37], v2 offset0:231 offset1:239
	v_cvt_pk_fp8_f32 v24, v3, v7 op_sel:[0,0,1]
	s_waitcnt lgkmcnt(3)
; #define LAS __attribute__((address_space(3)))
; __device__ __forceinline__ float clamp8(float x) { return __builtin_amdgcn_fmed3f(x, -448.f, 448.f); }
; __device__ __forceinline__ void cvt_finish(const CvtDesc& d, const float (&t)[64], LAS float* scr, int lane) {
;     ...
;     if (d.f8) {
; #pragma unroll
;         for (int j = 0; j < 8; ++j) { const int n = (lane >> 3) + 8 * j; const LAS float* s = scr + (8 * c) * 65 + n;
;             int a = __builtin_amdgcn_cvt_pk_fp8_f32(clamp8(s[0 * 65] * W8_SCALE), clamp8(s[1 * 65] * W8_SCALE), 0, false); a = __builtin_amdgcn_cvt_pk_fp8_f32(clamp8(s[2 * 65] * W8_SCALE), clamp8(s[3 * 65] * W8_SCALE), a, true);
;             int b = __builtin_amdgcn_cvt_pk_fp8_f32(clamp8(s[4 * 65] * W8_SCALE), clamp8(s[5 * 65] * W8_SCALE), 0, false); b = __builtin_amdgcn_cvt_pk_fp8_f32(clamp8(s[6 * 65] * W8_SCALE), clamp8(s[7 * 65] * W8_SCALE), b, true);
;             __builtin_nontemporal_store((u32x2){(unsigned)a, (unsigned)b}, (u32x2*)(d.dst + (size_t)n * d.dKB + 8 * c)); }
	v_mul_f32_e32 v3, 0x42800000, v30
	s_waitcnt lgkmcnt(2)
	v_mul_f32_e32 v7, 0x42800000, v32
	v_med3_f32 v3, v3, s93, v224
	v_med3_f32 v7, v7, s93, v224
	v_mov_b32_e32 v25, v193
	v_cvt_pk_fp8_f32 v25, v3, v7
	s_waitcnt lgkmcnt(1)
	v_mul_f32_e32 v3, 0x42800000, v34
	s_waitcnt lgkmcnt(0)
	v_mul_f32_e32 v7, 0x42800000, v36
	v_med3_f32 v3, v3, s93, v224
	v_med3_f32 v7, v7, s93, v224
	v_cvt_pk_fp8_f32 v25, v3, v7 op_sel:[0,0,1]
	v_mul_f32_e32 v3, 0x42800000, v21
	v_mul_f32_e32 v7, 0x42800000, v23
	v_med3_f32 v3, v3, s93, v224
	v_med3_f32 v7, v7, s93, v224
	v_mov_b32_e32 v20, v193
	v_cvt_pk_fp8_f32 v20, v3, v7
	v_mul_f32_e32 v3, 0x42800000, v27
	v_mul_f32_e32 v7, 0x42800000, v29
	v_med3_f32 v3, v3, s93, v224
	v_med3_f32 v7, v7, s93, v224
	v_cvt_pk_fp8_f32 v20, v3, v7 op_sel:[0,0,1]
	v_mul_f32_e32 v3, 0x42800000, v31
	v_mul_f32_e32 v7, 0x42800000, v33
	v_med3_f32 v3, v3, s93, v224
	v_med3_f32 v7, v7, s93, v224
	v_mov_b32_e32 v21, v193
	v_cvt_pk_fp8_f32 v21, v3, v7
	v_mul_f32_e32 v3, 0x42800000, v35
	v_mul_f32_e32 v7, 0x42800000, v37
	v_med3_f32 v3, v3, s93, v224
	v_med3_f32 v7, v7, s93, v224
	v_cvt_pk_fp8_f32 v21, v3, v7 op_sel:[0,0,1]
	v_mad_u64_u32 v[38:39], s[0:1], s10, v16, v[0:1]
	v_mad_u64_u32 v[22:23], s[0:1], s10, v17, v[0:1]
	v_lshl_add_u64 v[38:39], v[38:39], 0, v[4:5]
	v_lshl_add_u64 v[22:23], v[22:23], 0, v[4:5]
	global_store_dwordx2 v[38:39], v[24:25], off
	global_store_dwordx2 v[22:23], v[20:21], off
	ds_read2_b32 v[20:21], v12 offset0:48 offset1:56
	ds_read2_b32 v[22:23], v12 offset0:113 offset1:121
	ds_read2_b32 v[26:27], v12 offset0:178 offset1:186
	ds_read2_b32 v[28:29], v12 offset0:243 offset1:251
	v_mov_b32_e32 v24, v193
	s_waitcnt lgkmcnt(3)
	v_mul_f32_e32 v3, 0x42800000, v20
	s_waitcnt lgkmcnt(2)
	v_mul_f32_e32 v7, 0x42800000, v22
	v_med3_f32 v3, v3, s93, v224
	v_med3_f32 v7, v7, s93, v224
	ds_read2_b32 v[30:31], v2 offset0:52 offset1:60
	ds_read2_b32 v[32:33], v2 offset0:117 offset1:125
	v_cvt_pk_fp8_f32 v24, v3, v7
	ds_read2_b32 v[34:35], v2 offset0:182 offset1:190
	s_waitcnt lgkmcnt(4)
	v_mul_f32_e32 v3, 0x42800000, v26
	s_waitcnt lgkmcnt(3)
	v_mul_f32_e32 v7, 0x42800000, v28
	v_med3_f32 v3, v3, s93, v224
	v_med3_f32 v7, v7, s93, v224
	v_cvt_pk_fp8_f32 v24, v3, v7 op_sel:[0,0,1]
	s_waitcnt lgkmcnt(2)
	v_mul_f32_e32 v3, 0x42800000, v30
	s_waitcnt lgkmcnt(1)
	v_mul_f32_e32 v7, 0x42800000, v32
	v_med3_f32 v3, v3, s93, v224
	v_med3_f32 v7, v7, s93, v224
	v_mov_b32_e32 v25, v193
	v_cvt_pk_fp8_f32 v25, v3, v7
	s_waitcnt lgkmcnt(0)
	v_mul_f32_e32 v3, 0x42800000, v34
	v_med3_f32 v7, v3, s93, v224
	ds_read2_b32 v[2:3], v2 offset0:247 offset1:255
	v_mov_b32_e32 v20, v193
	v_mad_u64_u32 v[36:37], s[0:1], s10, v18, v[0:1]
	v_mad_u64_u32 v[0:1], s[0:1], s10, v19, v[0:1]
	s_waitcnt lgkmcnt(0)
	v_mul_f32_e32 v2, 0x42800000, v2
	v_med3_f32 v2, v2, s93, v224
	v_cvt_pk_fp8_f32 v25, v7, v2 op_sel:[0,0,1]
	v_mul_f32_e32 v2, 0x42800000, v21
	v_mul_f32_e32 v7, 0x42800000, v23
	v_med3_f32 v2, v2, s93, v224
	v_med3_f32 v7, v7, s93, v224
	v_cvt_pk_fp8_f32 v20, v2, v7
	v_mul_f32_e32 v2, 0x42800000, v27
	v_mul_f32_e32 v7, 0x42800000, v29
	v_med3_f32 v2, v2, s93, v224
	v_med3_f32 v7, v7, s93, v224
	v_cvt_pk_fp8_f32 v20, v2, v7 op_sel:[0,0,1]
	v_mul_f32_e32 v2, 0x42800000, v31
	v_mul_f32_e32 v7, 0x42800000, v33
	v_med3_f32 v2, v2, s93, v224
	v_med3_f32 v7, v7, s93, v224
	v_mov_b32_e32 v21, v193
	v_cvt_pk_fp8_f32 v21, v2, v7
	v_mul_f32_e32 v2, 0x42800000, v35
	v_mul_f32_e32 v3, 0x42800000, v3
	v_med3_f32 v2, v2, s93, v224
	v_med3_f32 v3, v3, s93, v224
	v_cvt_pk_fp8_f32 v21, v2, v3 op_sel:[0,0,1]
	v_lshl_add_u64 v[36:37], v[36:37], 0, v[4:5]
	v_lshl_add_u64 v[0:1], v[0:1], 0, v[4:5]
	global_store_dwordx2 v[36:37], v[24:25], off
	global_store_dwordx2 v[0:1], v[20:21], off
	s_waitcnt lgkmcnt(0)

; #define LAS __attribute__((address_space(3)))
; __device__ __forceinline__ float clamp8(float x) { return __builtin_amdgcn_fmed3f(x, -448.f, 448.f); }
; #define LDS_WAIT() asm volatile("s_waitcnt lgkmcnt(0)" ::: "memory")
;     __device__ __forceinline__ unsigned char* ws() const { return *(unsigned char* const __attribute__((address_space(4)))*)(p + 232); }
; __device__ __forceinline__ void cvt_finish(const CvtDesc& d, const float (&t)[64], LAS float* scr, int lane) {
;     LAS float* sw = scr + (lane >> 4) * 65 + 4 * (lane & 15);
; #pragma unroll
;     for (int i = 0; i < 16; ++i) { sw[(4 * i) * 65] = t[4 * i]; sw[(4 * i) * 65 + 1] = t[4 * i + 1]; sw[(4 * i) * 65 + 2] = t[4 * i + 2]; sw[(4 * i) * 65 + 3] = t[4 * i + 3]; }
;     LDS_WAIT();
;     const int c = lane & 7;
;     if (d.f8) {
; #pragma unroll
;         for (int j = 0; j < 8; ++j) { const int n = (lane >> 3) + 8 * j; const LAS float* s = scr + (8 * c) * 65 + n;
;             int a = __builtin_amdgcn_cvt_pk_fp8_f32(clamp8(s[0 * 65] * W8_SCALE), clamp8(s[1 * 65] * W8_SCALE), 0, false); a = __builtin_amdgcn_cvt_pk_fp8_f32(clamp8(s[2 * 65] * W8_SCALE), clamp8(s[3 * 65] * W8_SCALE), a, true);
;             int b = __builtin_amdgcn_cvt_pk_fp8_f32(clamp8(s[4 * 65] * W8_SCALE), clamp8(s[5 * 65] * W8_SCALE), 0, false); b = __builtin_amdgcn_cvt_pk_fp8_f32(clamp8(s[6 * 65] * W8_SCALE), clamp8(s[7 * 65] * W8_SCALE), b, true);
;             __builtin_nontemporal_store((u32x2){(unsigned)a, (unsigned)b}, (u32x2*)(d.dst + (size_t)n * d.dKB + 8 * c)); }
;     ...
;             if (v0) cvt_finish(da, ta, scr, lane);
;             if (v2) { da = conv_expert_desc(a, ws, q0 + 16); cvt_load(da, ta, lane); }
;             if (v1) cvt_finish(db, tb, scr, lane);
;             if (v3) { db = conv_expert_desc(a, ws, q0 + 24); cvt_load(db, tb, lane); }
;             if (v2) cvt_finish(da, ta, scr, lane);
;             if (v3) cvt_finish(db, tb, scr, lane);
.LBB0_1282:
	s_andn2_b64 vcc, exec, s[12:13]
	v_add_u32_e32 v141, 0x410, v135
	v_add_u32_e32 v143, 0x418, v135
	v_add_u32_e32 v145, 0x820, v135
	v_add_u32_e32 v147, 0x828, v135
	v_add_u32_e32 v150, 0xc30, v135
	v_add_u32_e32 v151, 0xc38, v135
	v_add_u32_e32 v152, 0x1040, v135
	v_add_u32_e32 v153, 0x1048, v135
	v_add_u32_e32 v154, 0x1450, v135
	v_add_u32_e32 v155, 0x1458, v135
	v_add_u32_e32 v156, 0x1860, v135
	v_add_u32_e32 v157, 0x1868, v135
	v_add_u32_e32 v158, 0x1c70, v135
	v_add_u32_e32 v159, 0x1c78, v135
	v_add_u32_e32 v160, 0x2080, v135
	v_add_u32_e32 v161, 0x2088, v135
	v_add_u32_e32 v162, 0x2490, v135
	v_add_u32_e32 v163, 0x2498, v135
	v_add_u32_e32 v164, 0x28a0, v135
	v_add_u32_e32 v165, 0x28a8, v135
	v_add_u32_e32 v166, 0x2cb0, v135
	v_add_u32_e32 v167, 0x2cb8, v135
	v_add_u32_e32 v168, 0x30c0, v135
	v_add_u32_e32 v169, 0x30c8, v135
	v_add_u32_e32 v170, 0x34d0, v135
	v_add_u32_e32 v171, 0x34d8, v135
	v_add_u32_e32 v172, 0x38e0, v135
	v_add_u32_e32 v173, 0x38e8, v135
	v_add_u32_e32 v174, 0x3cf0, v135
	v_add_u32_e32 v175, 0x3cf8, v135
	v_add_u32_e32 v139, 0x400, v137
	s_cbranch_vccnz .LBB0_1288
	s_waitcnt vmcnt(0)
	ds_write2_b32 v135, v16, v17 offset1:1
	ds_write2_b32 v135, v18, v19 offset0:2 offset1:3
	ds_write2_b32 v141, v24, v25 offset1:1
	ds_write2_b32 v143, v26, v27 offset1:1
	ds_write2_b32 v145, v32, v33 offset1:1
	ds_write2_b32 v147, v34, v35 offset1:1
	ds_write2_b32 v150, v40, v41 offset1:1
	ds_write2_b32 v151, v42, v43 offset1:1
	ds_write2_b32 v152, v52, v53 offset1:1
	ds_write2_b32 v153, v54, v55 offset1:1
	ds_write2_b32 v154, v56, v57 offset1:1
	ds_write2_b32 v155, v58, v59 offset1:1
	ds_write2_b32 v156, v68, v69 offset1:1
	ds_write2_b32 v157, v70, v71 offset1:1
	ds_write2_b32 v158, v72, v73 offset1:1
	ds_write2_b32 v159, v74, v75 offset1:1
	ds_write2_b32 v160, v80, v81 offset1:1
	ds_write2_b32 v161, v82, v83 offset1:1
	ds_write2_b32 v162, v88, v89 offset1:1
	ds_write2_b32 v163, v90, v91 offset1:1
	ds_write2_b32 v164, v96, v97 offset1:1
	ds_write2_b32 v165, v98, v99 offset1:1
	ds_write2_b32 v166, v104, v105 offset1:1
	ds_write2_b32 v167, v106, v107 offset1:1
	ds_write2_b32 v168, v112, v113 offset1:1
	ds_write2_b32 v169, v114, v115 offset1:1
	ds_write2_b32 v170, v116, v117 offset1:1
	ds_write2_b32 v171, v118, v119 offset1:1
	ds_write2_b32 v172, v120, v121 offset1:1
	ds_write2_b32 v173, v122, v123 offset1:1
	ds_write2_b32 v174, v124, v125 offset1:1
	ds_write2_b32 v175, v126, v127 offset1:1
	s_waitcnt lgkmcnt(0)
	ds_read2_b32 v[176:177], v137 offset1:8
	ds_read2_b32 v[178:179], v137 offset0:65 offset1:73
	ds_read2_b32 v[180:181], v137 offset0:130 offset1:138
	ds_read2_b32 v[184:185], v137 offset0:195 offset1:203
	v_mov_b32_e32 v182, v193
	s_waitcnt lgkmcnt(3)
	v_mul_f32_e32 v148, 0x42800000, v176
	s_waitcnt lgkmcnt(2)
	v_mul_f32_e32 v149, 0x42800000, v178
	v_mul_f32_e32 v176, 0x42800000, v177
	v_med3_f32 v148, v148, s93, v224
	v_med3_f32 v149, v149, s93, v224
	ds_read2_b32 v[186:187], v139 offset0:4 offset1:12
	ds_read2_b32 v[188:189], v139 offset0:69 offset1:77
	v_med3_f32 v177, v176, s93, v224
	v_mul_f32_e32 v176, 0x42800000, v179
	v_cvt_pk_fp8_f32 v182, v148, v149
	v_med3_f32 v178, v176, s93, v224
	v_mov_b32_e32 v176, v193
	v_cvt_pk_fp8_f32 v176, v177, v178
	s_waitcnt lgkmcnt(3)
	v_mul_f32_e32 v148, 0x42800000, v180
	s_waitcnt lgkmcnt(2)
	v_mul_f32_e32 v149, 0x42800000, v184
	v_med3_f32 v148, v148, s93, v224
	v_med3_f32 v149, v149, s93, v224
	ds_read2_b32 v[190:191], v139 offset0:134 offset1:142
	ds_read2_b32 v[194:195], v139 offset0:199 offset1:207
	v_mul_f32_e32 v177, 0x42800000, v181
	v_mul_f32_e32 v178, 0x42800000, v185
	v_cvt_pk_fp8_f32 v182, v148, v149 op_sel:[0,0,1]
	s_waitcnt lgkmcnt(3)
	v_mul_f32_e32 v148, 0x42800000, v186
	s_waitcnt lgkmcnt(2)
	v_mul_f32_e32 v149, 0x42800000, v188
	v_med3_f32 v177, v177, s93, v224
	v_med3_f32 v178, v178, s93, v224
	v_med3_f32 v148, v148, s93, v224
	v_med3_f32 v149, v149, s93, v224
	v_mov_b32_e32 v183, v193
	v_cvt_pk_fp8_f32 v176, v177, v178 op_sel:[0,0,1]
	v_mul_f32_e32 v177, 0x42800000, v187
	v_cvt_pk_fp8_f32 v183, v148, v149
	v_med3_f32 v178, v177, s93, v224
	v_mul_f32_e32 v177, 0x42800000, v189
	v_med3_f32 v179, v177, s93, v224
	v_mov_b32_e32 v177, v193
	s_waitcnt lgkmcnt(1)
	v_mul_f32_e32 v148, 0x42800000, v190
	s_waitcnt lgkmcnt(0)
	v_mul_f32_e32 v149, 0x42800000, v194
	v_cvt_pk_fp8_f32 v177, v178, v179
	v_med3_f32 v148, v148, s93, v224
	v_med3_f32 v149, v149, s93, v224
	v_cvt_pk_fp8_f32 v183, v148, v149 op_sel:[0,0,1]
	v_mul_f32_e32 v178, 0x42800000, v191
	v_mul_f32_e32 v179, 0x42800000, v195
	v_mov_b64_e32 v[148:149], s[8:9]
	v_med3_f32 v178, v178, s93, v224
	v_med3_f32 v179, v179, s93, v224
	v_mad_i64_i32 v[196:197], s[0:1], s25, v130, v[148:149]
	v_cvt_pk_fp8_f32 v177, v178, v179 op_sel:[0,0,1]
	ds_read2_b32 v[178:179], v137 offset0:16 offset1:24
	v_lshl_add_u64 v[196:197], v[196:197], 0, v[132:133]
	global_store_dwordx2 v[196:197], v[182:183], off
	ds_read2_b32 v[182:183], v137 offset0:81 offset1:89
	v_mad_i64_i32 v[180:181], s[0:1], s25, v134, v[148:149]
	v_lshl_add_u64 v[180:181], v[180:181], 0, v[132:133]
	global_store_dwordx2 v[180:181], v[176:177], off
	s_waitcnt lgkmcnt(1)
	v_mul_f32_e32 v176, 0x42800000, v178
	v_med3_f32 v178, v176, s93, v224
	ds_read2_b32 v[176:177], v137 offset0:146 offset1:154
	ds_read2_b32 v[184:185], v137 offset0:211 offset1:219
	s_waitcnt lgkmcnt(2)
	v_mul_f32_e32 v180, 0x42800000, v182
	v_med3_f32 v181, v180, s93, v224
	v_mov_b32_e32 v180, v193
	ds_read2_b32 v[186:187], v139 offset0:20 offset1:28
	ds_read2_b32 v[188:189], v139 offset0:85 offset1:93
	v_cvt_pk_fp8_f32 v180, v178, v181
	s_waitcnt lgkmcnt(3)
; #define LAS __attribute__((address_space(3)))
; __device__ __forceinline__ float clamp8(float x) { return __builtin_amdgcn_fmed3f(x, -448.f, 448.f); }
; #define LDS_WAIT() asm volatile("s_waitcnt lgkmcnt(0)" ::: "memory")
; __device__ __forceinline__ void cvt_finish(const CvtDesc& d, const float (&t)[64], LAS float* scr, int lane) {
;     LAS float* sw = scr + (lane >> 4) * 65 + 4 * (lane & 15);
; #pragma unroll
;     for (int i = 0; i < 16; ++i) { sw[(4 * i) * 65] = t[4 * i]; sw[(4 * i) * 65 + 1] = t[4 * i + 1]; sw[(4 * i) * 65 + 2] = t[4 * i + 2]; sw[(4 * i) * 65 + 3] = t[4 * i + 3]; }
;     LDS_WAIT();
;     const int c = lane & 7;
;     if (d.f8) {
; #pragma unroll
;         for (int j = 0; j < 8; ++j) { const int n = (lane >> 3) + 8 * j; const LAS float* s = scr + (8 * c) * 65 + n;
;             int a = __builtin_amdgcn_cvt_pk_fp8_f32(clamp8(s[0 * 65] * W8_SCALE), clamp8(s[1 * 65] * W8_SCALE), 0, false); a = __builtin_amdgcn_cvt_pk_fp8_f32(clamp8(s[2 * 65] * W8_SCALE), clamp8(s[3 * 65] * W8_SCALE), a, true);
;             int b = __builtin_amdgcn_cvt_pk_fp8_f32(clamp8(s[4 * 65] * W8_SCALE), clamp8(s[5 * 65] * W8_SCALE), 0, false); b = __builtin_amdgcn_cvt_pk_fp8_f32(clamp8(s[6 * 65] * W8_SCALE), clamp8(s[7 * 65] * W8_SCALE), b, true);
;             __builtin_nontemporal_store((u32x2){(unsigned)a, (unsigned)b}, (u32x2*)(d.dst + (size_t)n * d.dKB + 8 * c)); }
	v_mul_f32_e32 v176, 0x42800000, v176
	s_waitcnt lgkmcnt(2)
	v_mul_f32_e32 v178, 0x42800000, v184
	v_med3_f32 v176, v176, s93, v224
	v_med3_f32 v178, v178, s93, v224
	ds_read2_b32 v[190:191], v139 offset0:150 offset1:158
	ds_read2_b32 v[194:195], v139 offset0:215 offset1:223
	v_cvt_pk_fp8_f32 v180, v176, v178 op_sel:[0,0,1]
	s_waitcnt lgkmcnt(3)
	v_mul_f32_e32 v176, 0x42800000, v186
	s_waitcnt lgkmcnt(2)
	v_mul_f32_e32 v178, 0x42800000, v188
	v_med3_f32 v176, v176, s93, v224
	v_med3_f32 v178, v178, s93, v224
	v_mov_b32_e32 v181, v193
	v_cvt_pk_fp8_f32 v181, v176, v178
	s_waitcnt lgkmcnt(1)
	v_mul_f32_e32 v176, 0x42800000, v190
	s_waitcnt lgkmcnt(0)
	v_mul_f32_e32 v178, 0x42800000, v194
	v_med3_f32 v176, v176, s93, v224
	v_med3_f32 v178, v178, s93, v224
	v_cvt_pk_fp8_f32 v181, v176, v178 op_sel:[0,0,1]
	v_mul_f32_e32 v176, 0x42800000, v179
	v_med3_f32 v178, v176, s93, v224
	v_mul_f32_e32 v176, 0x42800000, v183
	v_med3_f32 v179, v176, s93, v224
	v_mov_b32_e32 v176, v193
	v_cvt_pk_fp8_f32 v176, v178, v179
	v_mul_f32_e32 v177, 0x42800000, v177
	v_mul_f32_e32 v178, 0x42800000, v185
	v_med3_f32 v177, v177, s93, v224
	v_med3_f32 v178, v178, s93, v224
	v_cvt_pk_fp8_f32 v176, v177, v178 op_sel:[0,0,1]
	v_mul_f32_e32 v177, 0x42800000, v187
	v_med3_f32 v178, v177, s93, v224
	v_mul_f32_e32 v177, 0x42800000, v189
	v_med3_f32 v179, v177, s93, v224
	v_mov_b32_e32 v177, v193
	v_cvt_pk_fp8_f32 v177, v178, v179
	v_mul_f32_e32 v178, 0x42800000, v191
	v_mul_f32_e32 v179, 0x42800000, v195
	v_med3_f32 v178, v178, s93, v224
	v_med3_f32 v179, v179, s93, v224
	v_cvt_pk_fp8_f32 v177, v178, v179 op_sel:[0,0,1]
	ds_read2_b32 v[178:179], v137 offset0:32 offset1:40
	v_mad_i64_i32 v[196:197], s[0:1], s25, v136, v[148:149]
	v_lshl_add_u64 v[196:197], v[196:197], 0, v[132:133]
	ds_read2_b32 v[182:183], v137 offset0:97 offset1:105
	global_store_dwordx2 v[196:197], v[180:181], off
	v_mad_i64_i32 v[180:181], s[0:1], s25, v138, v[148:149]
	v_lshl_add_u64 v[180:181], v[180:181], 0, v[132:133]
	global_store_dwordx2 v[180:181], v[176:177], off
	s_waitcnt lgkmcnt(1)
	v_mul_f32_e32 v176, 0x42800000, v178
	v_med3_f32 v178, v176, s93, v224
	ds_read2_b32 v[176:177], v137 offset0:162 offset1:170
	ds_read2_b32 v[184:185], v137 offset0:227 offset1:235
	s_waitcnt lgkmcnt(2)
	v_mul_f32_e32 v180, 0x42800000, v182
	v_med3_f32 v181, v180, s93, v224
	v_mov_b32_e32 v180, v193
	ds_read2_b32 v[186:187], v139 offset0:36 offset1:44
	ds_read2_b32 v[188:189], v139 offset0:101 offset1:109
	v_cvt_pk_fp8_f32 v180, v178, v181
	s_waitcnt lgkmcnt(3)
	v_mul_f32_e32 v176, 0x42800000, v176
	s_waitcnt lgkmcnt(2)
	v_mul_f32_e32 v178, 0x42800000, v184
	v_med3_f32 v176, v176, s93, v224
	v_med3_f32 v178, v178, s93, v224
	ds_read2_b32 v[190:191], v139 offset0:166 offset1:174
	ds_read2_b32 v[194:195], v139 offset0:231 offset1:239
	v_cvt_pk_fp8_f32 v180, v176, v178 op_sel:[0,0,1]
	s_waitcnt lgkmcnt(3)
	v_mul_f32_e32 v176, 0x42800000, v186
	s_waitcnt lgkmcnt(2)
	v_mul_f32_e32 v178, 0x42800000, v188
	v_med3_f32 v176, v176, s93, v224
	v_med3_f32 v178, v178, s93, v224
	v_mov_b32_e32 v181, v193
	v_cvt_pk_fp8_f32 v181, v176, v178
	s_waitcnt lgkmcnt(1)
	v_mul_f32_e32 v176, 0x42800000, v190
	s_waitcnt lgkmcnt(0)
; #define LAS __attribute__((address_space(3)))
; __device__ __forceinline__ float clamp8(float x) { return __builtin_amdgcn_fmed3f(x, -448.f, 448.f); }
; #define LDS_WAIT() asm volatile("s_waitcnt lgkmcnt(0)" ::: "memory")
;     __device__ __forceinline__ unsigned char* ws() const { return *(unsigned char* const __attribute__((address_space(4)))*)(p + 232); }
; __device__ __forceinline__ void cvt_finish(const CvtDesc& d, const float (&t)[64], LAS float* scr, int lane) {
;     LAS float* sw = scr + (lane >> 4) * 65 + 4 * (lane & 15);
; #pragma unroll
;     for (int i = 0; i < 16; ++i) { sw[(4 * i) * 65] = t[4 * i]; sw[(4 * i) * 65 + 1] = t[4 * i + 1]; sw[(4 * i) * 65 + 2] = t[4 * i + 2]; sw[(4 * i) * 65 + 3] = t[4 * i + 3]; }
;     LDS_WAIT();
;     const int c = lane & 7;
;     if (d.f8) {
; #pragma unroll
;         for (int j = 0; j < 8; ++j) { const int n = (lane >> 3) + 8 * j; const LAS float* s = scr + (8 * c) * 65 + n;
;             int a = __builtin_amdgcn_cvt_pk_fp8_f32(clamp8(s[0 * 65] * W8_SCALE), clamp8(s[1 * 65] * W8_SCALE), 0, false); a = __builtin_amdgcn_cvt_pk_fp8_f32(clamp8(s[2 * 65] * W8_SCALE), clamp8(s[3 * 65] * W8_SCALE), a, true);
;             int b = __builtin_amdgcn_cvt_pk_fp8_f32(clamp8(s[4 * 65] * W8_SCALE), clamp8(s[5 * 65] * W8_SCALE), 0, false); b = __builtin_amdgcn_cvt_pk_fp8_f32(clamp8(s[6 * 65] * W8_SCALE), clamp8(s[7 * 65] * W8_SCALE), b, true);
;             __builtin_nontemporal_store((u32x2){(unsigned)a, (unsigned)b}, (u32x2*)(d.dst + (size_t)n * d.dKB + 8 * c)); }
;     ...
;             if (v0) cvt_finish(da, ta, scr, lane);
;             if (v2) { da = conv_expert_desc(a, ws, q0 + 16); cvt_load(da, ta, lane); }
;             if (v1) cvt_finish(db, tb, scr, lane);
;             if (v3) { db = conv_expert_desc(a, ws, q0 + 24); cvt_load(db, tb, lane); }
;             if (v2) cvt_finish(da, ta, scr, lane);
;             if (v3) cvt_finish(db, tb, scr, lane);
	v_mul_f32_e32 v178, 0x42800000, v194
	v_med3_f32 v176, v176, s93, v224
	v_med3_f32 v178, v178, s93, v224
	v_cvt_pk_fp8_f32 v181, v176, v178 op_sel:[0,0,1]
	v_mul_f32_e32 v176, 0x42800000, v179
	v_med3_f32 v178, v176, s93, v224
	v_mul_f32_e32 v176, 0x42800000, v183
	v_med3_f32 v179, v176, s93, v224
	v_mov_b32_e32 v176, v193
	v_cvt_pk_fp8_f32 v176, v178, v179
	v_mul_f32_e32 v177, 0x42800000, v177
	v_mul_f32_e32 v178, 0x42800000, v185
	v_med3_f32 v177, v177, s93, v224
	v_med3_f32 v178, v178, s93, v224
	v_cvt_pk_fp8_f32 v176, v177, v178 op_sel:[0,0,1]
	v_mul_f32_e32 v177, 0x42800000, v187
	v_med3_f32 v178, v177, s93, v224
	v_mul_f32_e32 v177, 0x42800000, v189
	v_med3_f32 v179, v177, s93, v224
	v_mov_b32_e32 v177, v193
	v_cvt_pk_fp8_f32 v177, v178, v179
	v_mul_f32_e32 v178, 0x42800000, v191
	v_mul_f32_e32 v179, 0x42800000, v195
	v_med3_f32 v178, v178, s93, v224
	v_med3_f32 v179, v179, s93, v224
	v_cvt_pk_fp8_f32 v177, v178, v179 op_sel:[0,0,1]
	ds_read2_b32 v[178:179], v137 offset0:48 offset1:56
	v_mad_i64_i32 v[196:197], s[0:1], s25, v140, v[148:149]
	v_lshl_add_u64 v[196:197], v[196:197], 0, v[132:133]
	ds_read2_b32 v[182:183], v137 offset0:113 offset1:121
	global_store_dwordx2 v[196:197], v[180:181], off
	v_mad_i64_i32 v[180:181], s[0:1], s25, v142, v[148:149]
	v_lshl_add_u64 v[180:181], v[180:181], 0, v[132:133]
	global_store_dwordx2 v[180:181], v[176:177], off
	s_waitcnt lgkmcnt(1)
	v_mul_f32_e32 v176, 0x42800000, v178
	v_med3_f32 v178, v176, s93, v224
	ds_read2_b32 v[176:177], v137 offset0:178 offset1:186
	ds_read2_b32 v[184:185], v137 offset0:243 offset1:251
	s_waitcnt lgkmcnt(2)
	v_mul_f32_e32 v180, 0x42800000, v182
	v_med3_f32 v181, v180, s93, v224
	v_mov_b32_e32 v180, v193
	ds_read2_b32 v[186:187], v139 offset0:52 offset1:60
	ds_read2_b32 v[188:189], v139 offset0:117 offset1:125
	v_cvt_pk_fp8_f32 v180, v178, v181
	s_waitcnt lgkmcnt(3)
	v_mul_f32_e32 v176, 0x42800000, v176
	s_waitcnt lgkmcnt(2)
	v_mul_f32_e32 v178, 0x42800000, v184
	v_med3_f32 v176, v176, s93, v224
	v_med3_f32 v178, v178, s93, v224
	ds_read2_b32 v[190:191], v139 offset0:182 offset1:190
	ds_read2_b32 v[194:195], v139 offset0:247 offset1:255
	v_cvt_pk_fp8_f32 v180, v176, v178 op_sel:[0,0,1]
	s_waitcnt lgkmcnt(3)
	v_mul_f32_e32 v176, 0x42800000, v186
	s_waitcnt lgkmcnt(2)
	v_mul_f32_e32 v178, 0x42800000, v188
	v_med3_f32 v176, v176, s93, v224
	v_med3_f32 v178, v178, s93, v224
	v_mov_b32_e32 v181, v193
	v_cvt_pk_fp8_f32 v181, v176, v178
	s_waitcnt lgkmcnt(1)
	v_mul_f32_e32 v176, 0x42800000, v190
	s_waitcnt lgkmcnt(0)
	v_mul_f32_e32 v178, 0x42800000, v194
	v_med3_f32 v176, v176, s93, v224
	v_med3_f32 v178, v178, s93, v224
	v_cvt_pk_fp8_f32 v181, v176, v178 op_sel:[0,0,1]
	v_mul_f32_e32 v176, 0x42800000, v179
	v_med3_f32 v178, v176, s93, v224
	v_mul_f32_e32 v176, 0x42800000, v183
	v_med3_f32 v179, v176, s93, v224
	v_mov_b32_e32 v176, v193
	v_cvt_pk_fp8_f32 v176, v178, v179
	v_mul_f32_e32 v177, 0x42800000, v177
	v_mul_f32_e32 v178, 0x42800000, v185
	v_med3_f32 v177, v177, s93, v224
	v_med3_f32 v178, v178, s93, v224
	v_cvt_pk_fp8_f32 v176, v177, v178 op_sel:[0,0,1]
	v_mul_f32_e32 v177, 0x42800000, v187
	v_med3_f32 v178, v177, s93, v224
	v_mul_f32_e32 v177, 0x42800000, v189
	v_med3_f32 v179, v177, s93, v224
	v_mov_b32_e32 v177, v193
	v_cvt_pk_fp8_f32 v177, v178, v179
	v_mul_f32_e32 v178, 0x42800000, v191
	v_mul_f32_e32 v179, 0x42800000, v195
	v_med3_f32 v178, v178, s93, v224
	v_med3_f32 v179, v179, s93, v224
	v_cvt_pk_fp8_f32 v177, v178, v179 op_sel:[0,0,1]
	v_mad_i64_i32 v[196:197], s[0:1], s25, v144, v[148:149]
	v_mad_i64_i32 v[148:149], s[0:1], s25, v146, v[148:149]
	v_lshl_add_u64 v[196:197], v[196:197], 0, v[132:133]
	v_lshl_add_u64 v[148:149], v[148:149], 0, v[132:133]
	global_store_dwordx2 v[196:197], v[180:181], off
	global_store_dwordx2 v[148:149], v[176:177], off
	s_waitcnt lgkmcnt(0)
	s_cmp_lt_i32 s29, 0x185f0
	s_cselect_b64 s[12:13], -1, 0
	s_cmp_gt_i32 s29, 0x185ef
	s_cbranch_scc0 .LBB0_1289

; #define LAS __attribute__((address_space(3)))
; __device__ __forceinline__ float clamp8(float x) { return __builtin_amdgcn_fmed3f(x, -448.f, 448.f); }
; #define LDS_WAIT() asm volatile("s_waitcnt lgkmcnt(0)" ::: "memory")
;     __device__ __forceinline__ unsigned char* ws() const { return *(unsigned char* const __attribute__((address_space(4)))*)(p + 232); }
; __device__ __forceinline__ void cvt_finish(const CvtDesc& d, const float (&t)[64], LAS float* scr, int lane) {
;     LAS float* sw = scr + (lane >> 4) * 65 + 4 * (lane & 15);
; #pragma unroll
;     for (int i = 0; i < 16; ++i) { sw[(4 * i) * 65] = t[4 * i]; sw[(4 * i) * 65 + 1] = t[4 * i + 1]; sw[(4 * i) * 65 + 2] = t[4 * i + 2]; sw[(4 * i) * 65 + 3] = t[4 * i + 3]; }
;     LDS_WAIT();
;     const int c = lane & 7;
;     if (d.f8) {
; #pragma unroll
;         for (int j = 0; j < 8; ++j) { const int n = (lane >> 3) + 8 * j; const LAS float* s = scr + (8 * c) * 65 + n;
;             int a = __builtin_amdgcn_cvt_pk_fp8_f32(clamp8(s[0 * 65] * W8_SCALE), clamp8(s[1 * 65] * W8_SCALE), 0, false); a = __builtin_amdgcn_cvt_pk_fp8_f32(clamp8(s[2 * 65] * W8_SCALE), clamp8(s[3 * 65] * W8_SCALE), a, true);
;             int b = __builtin_amdgcn_cvt_pk_fp8_f32(clamp8(s[4 * 65] * W8_SCALE), clamp8(s[5 * 65] * W8_SCALE), 0, false); b = __builtin_amdgcn_cvt_pk_fp8_f32(clamp8(s[6 * 65] * W8_SCALE), clamp8(s[7 * 65] * W8_SCALE), b, true);
;             __builtin_nontemporal_store((u32x2){(unsigned)a, (unsigned)b}, (u32x2*)(d.dst + (size_t)n * d.dKB + 8 * c)); }
;     ...
;             if (v1) cvt_finish(db, tb, scr, lane);
;             if (v3) { db = conv_expert_desc(a, ws, q0 + 24); cvt_load(db, tb, lane); }
;             if (v2) cvt_finish(da, ta, scr, lane);
;             if (v3) cvt_finish(db, tb, scr, lane);
.LBB0_1285:
	s_waitcnt vmcnt(0)
	ds_write2_b32 v135, v0, v1 offset1:1
	ds_write2_b32 v135, v2, v3 offset0:2 offset1:3
	ds_write2_b32 v141, v4, v5 offset1:1
	ds_write2_b32 v143, v6, v7 offset1:1
	ds_write2_b32 v145, v8, v9 offset1:1
	ds_write2_b32 v147, v10, v11 offset1:1
	ds_write2_b32 v150, v12, v13 offset1:1
	ds_write2_b32 v151, v14, v15 offset1:1
	ds_write2_b32 v152, v20, v21 offset1:1
	ds_write2_b32 v153, v22, v23 offset1:1
	ds_write2_b32 v154, v28, v29 offset1:1
	ds_write2_b32 v155, v30, v31 offset1:1
	ds_write2_b32 v156, v36, v37 offset1:1
	ds_write2_b32 v157, v38, v39 offset1:1
	ds_write2_b32 v158, v44, v45 offset1:1
	ds_write2_b32 v159, v46, v47 offset1:1
	ds_write2_b32 v160, v48, v49 offset1:1
	ds_write2_b32 v161, v50, v51 offset1:1
	ds_write2_b32 v162, v60, v61 offset1:1
	ds_write2_b32 v163, v62, v63 offset1:1
	ds_write2_b32 v164, v64, v65 offset1:1
	ds_write2_b32 v165, v66, v67 offset1:1
	ds_write2_b32 v166, v76, v77 offset1:1
	ds_write2_b32 v167, v78, v79 offset1:1
	ds_write2_b32 v168, v84, v85 offset1:1
	ds_write2_b32 v169, v86, v87 offset1:1
	ds_write2_b32 v170, v92, v93 offset1:1
	ds_write2_b32 v171, v94, v95 offset1:1
	ds_write2_b32 v172, v100, v101 offset1:1
	ds_write2_b32 v173, v102, v103 offset1:1
	ds_write2_b32 v174, v108, v109 offset1:1
	ds_write2_b32 v175, v110, v111 offset1:1
	s_waitcnt lgkmcnt(0)
	ds_read2_b32 v[176:177], v137 offset1:8
	ds_read2_b32 v[178:179], v137 offset0:65 offset1:73
	ds_read2_b32 v[180:181], v137 offset0:130 offset1:138
	ds_read2_b32 v[184:185], v137 offset0:195 offset1:203
	v_mov_b32_e32 v182, v193
	s_waitcnt lgkmcnt(3)
	v_mul_f32_e32 v148, 0x42800000, v176
	s_waitcnt lgkmcnt(2)
	v_mul_f32_e32 v149, 0x42800000, v178
	v_mul_f32_e32 v176, 0x42800000, v177
	v_med3_f32 v148, v148, s93, v224
	v_med3_f32 v149, v149, s93, v224
	ds_read2_b32 v[186:187], v139 offset0:4 offset1:12
	ds_read2_b32 v[188:189], v139 offset0:69 offset1:77
	v_med3_f32 v177, v176, s93, v224
	v_mul_f32_e32 v176, 0x42800000, v179
	v_cvt_pk_fp8_f32 v182, v148, v149
	v_med3_f32 v178, v176, s93, v224
	v_mov_b32_e32 v176, v193
	v_cvt_pk_fp8_f32 v176, v177, v178
	s_waitcnt lgkmcnt(3)
	v_mul_f32_e32 v148, 0x42800000, v180
	s_waitcnt lgkmcnt(2)
	v_mul_f32_e32 v149, 0x42800000, v184
	v_med3_f32 v148, v148, s93, v224
	v_med3_f32 v149, v149, s93, v224
	ds_read2_b32 v[190:191], v139 offset0:134 offset1:142
	ds_read2_b32 v[194:195], v139 offset0:199 offset1:207
	v_mul_f32_e32 v177, 0x42800000, v181
	v_mul_f32_e32 v178, 0x42800000, v185
	v_cvt_pk_fp8_f32 v182, v148, v149 op_sel:[0,0,1]
	s_waitcnt lgkmcnt(3)
	v_mul_f32_e32 v148, 0x42800000, v186
	s_waitcnt lgkmcnt(2)
	v_mul_f32_e32 v149, 0x42800000, v188
	v_med3_f32 v177, v177, s93, v224
	v_med3_f32 v178, v178, s93, v224
	v_med3_f32 v148, v148, s93, v224
	v_med3_f32 v149, v149, s93, v224
	v_mov_b32_e32 v183, v193
	v_cvt_pk_fp8_f32 v176, v177, v178 op_sel:[0,0,1]
	v_mul_f32_e32 v177, 0x42800000, v187
	v_cvt_pk_fp8_f32 v183, v148, v149
	v_med3_f32 v178, v177, s93, v224
	v_mul_f32_e32 v177, 0x42800000, v189
	v_med3_f32 v179, v177, s93, v224
	v_mov_b32_e32 v177, v193
	s_waitcnt lgkmcnt(1)
	v_mul_f32_e32 v148, 0x42800000, v190
	s_waitcnt lgkmcnt(0)
	v_mul_f32_e32 v149, 0x42800000, v194
	v_cvt_pk_fp8_f32 v177, v178, v179
	v_med3_f32 v148, v148, s93, v224
	v_med3_f32 v149, v149, s93, v224
	v_cvt_pk_fp8_f32 v183, v148, v149 op_sel:[0,0,1]
	v_mul_f32_e32 v178, 0x42800000, v191
	v_mul_f32_e32 v179, 0x42800000, v195
	v_mov_b64_e32 v[148:149], s[6:7]
	v_med3_f32 v178, v178, s93, v224
	v_med3_f32 v179, v179, s93, v224
	v_mad_i64_i32 v[196:197], s[0:1], s24, v130, v[148:149]
	v_cvt_pk_fp8_f32 v177, v178, v179 op_sel:[0,0,1]
	ds_read2_b32 v[178:179], v137 offset0:16 offset1:24
	v_lshl_add_u64 v[196:197], v[196:197], 0, v[132:133]
	global_store_dwordx2 v[196:197], v[182:183], off
	ds_read2_b32 v[182:183], v137 offset0:81 offset1:89
	v_mad_i64_i32 v[180:181], s[0:1], s24, v134, v[148:149]
	v_lshl_add_u64 v[180:181], v[180:181], 0, v[132:133]
	global_store_dwordx2 v[180:181], v[176:177], off
	s_waitcnt lgkmcnt(1)
	v_mul_f32_e32 v176, 0x42800000, v178
	v_med3_f32 v178, v176, s93, v224
	ds_read2_b32 v[176:177], v137 offset0:146 offset1:154
	ds_read2_b32 v[184:185], v137 offset0:211 offset1:219
	s_waitcnt lgkmcnt(2)
	v_mul_f32_e32 v180, 0x42800000, v182
	v_med3_f32 v181, v180, s93, v224
	v_mov_b32_e32 v180, v193
	ds_read2_b32 v[186:187], v139 offset0:20 offset1:28
	ds_read2_b32 v[188:189], v139 offset0:85 offset1:93
	v_cvt_pk_fp8_f32 v180, v178, v181
	s_waitcnt lgkmcnt(3)
	v_mul_f32_e32 v176, 0x42800000, v176
	s_waitcnt lgkmcnt(2)
	v_mul_f32_e32 v178, 0x42800000, v184
	v_med3_f32 v176, v176, s93, v224
	v_med3_f32 v178, v178, s93, v224
	ds_read2_b32 v[190:191], v139 offset0:150 offset1:158
	ds_read2_b32 v[194:195], v139 offset0:215 offset1:223
	v_cvt_pk_fp8_f32 v180, v176, v178 op_sel:[0,0,1]
	s_waitcnt lgkmcnt(3)
	v_mul_f32_e32 v176, 0x42800000, v186
	s_waitcnt lgkmcnt(2)
	v_mul_f32_e32 v178, 0x42800000, v188
	v_med3_f32 v176, v176, s93, v224
	v_med3_f32 v178, v178, s93, v224
	v_mov_b32_e32 v181, v193
	v_cvt_pk_fp8_f32 v181, v176, v178
	s_waitcnt lgkmcnt(1)
	v_mul_f32_e32 v176, 0x42800000, v190
	s_waitcnt lgkmcnt(0)
; #define LAS __attribute__((address_space(3)))
; __device__ __forceinline__ float clamp8(float x) { return __builtin_amdgcn_fmed3f(x, -448.f, 448.f); }
; #define LDS_WAIT() asm volatile("s_waitcnt lgkmcnt(0)" ::: "memory")
;     __device__ __forceinline__ unsigned char* ws() const { return *(unsigned char* const __attribute__((address_space(4)))*)(p + 232); }
; __device__ __forceinline__ void cvt_finish(const CvtDesc& d, const float (&t)[64], LAS float* scr, int lane) {
;     LAS float* sw = scr + (lane >> 4) * 65 + 4 * (lane & 15);
; #pragma unroll
;     for (int i = 0; i < 16; ++i) { sw[(4 * i) * 65] = t[4 * i]; sw[(4 * i) * 65 + 1] = t[4 * i + 1]; sw[(4 * i) * 65 + 2] = t[4 * i + 2]; sw[(4 * i) * 65 + 3] = t[4 * i + 3]; }
;     LDS_WAIT();
;     const int c = lane & 7;
;     if (d.f8) {
; #pragma unroll
;         for (int j = 0; j < 8; ++j) { const int n = (lane >> 3) + 8 * j; const LAS float* s = scr + (8 * c) * 65 + n;
;             int a = __builtin_amdgcn_cvt_pk_fp8_f32(clamp8(s[0 * 65] * W8_SCALE), clamp8(s[1 * 65] * W8_SCALE), 0, false); a = __builtin_amdgcn_cvt_pk_fp8_f32(clamp8(s[2 * 65] * W8_SCALE), clamp8(s[3 * 65] * W8_SCALE), a, true);
;             int b = __builtin_amdgcn_cvt_pk_fp8_f32(clamp8(s[4 * 65] * W8_SCALE), clamp8(s[5 * 65] * W8_SCALE), 0, false); b = __builtin_amdgcn_cvt_pk_fp8_f32(clamp8(s[6 * 65] * W8_SCALE), clamp8(s[7 * 65] * W8_SCALE), b, true);
;             __builtin_nontemporal_store((u32x2){(unsigned)a, (unsigned)b}, (u32x2*)(d.dst + (size_t)n * d.dKB + 8 * c)); }
;     ...
;             if (v1) cvt_finish(db, tb, scr, lane);
;             if (v3) { db = conv_expert_desc(a, ws, q0 + 24); cvt_load(db, tb, lane); }
;             if (v2) cvt_finish(da, ta, scr, lane);
;             if (v3) cvt_finish(db, tb, scr, lane);
	v_mul_f32_e32 v178, 0x42800000, v194
	v_med3_f32 v176, v176, s93, v224
	v_med3_f32 v178, v178, s93, v224
	v_cvt_pk_fp8_f32 v181, v176, v178 op_sel:[0,0,1]
	v_mul_f32_e32 v176, 0x42800000, v179
	v_med3_f32 v178, v176, s93, v224
	v_mul_f32_e32 v176, 0x42800000, v183
	v_med3_f32 v179, v176, s93, v224
	v_mov_b32_e32 v176, v193
	v_cvt_pk_fp8_f32 v176, v178, v179
	v_mul_f32_e32 v177, 0x42800000, v177
	v_mul_f32_e32 v178, 0x42800000, v185
	v_med3_f32 v177, v177, s93, v224
	v_med3_f32 v178, v178, s93, v224
	v_cvt_pk_fp8_f32 v176, v177, v178 op_sel:[0,0,1]
	v_mul_f32_e32 v177, 0x42800000, v187
	v_med3_f32 v178, v177, s93, v224
	v_mul_f32_e32 v177, 0x42800000, v189
	v_med3_f32 v179, v177, s93, v224
	v_mov_b32_e32 v177, v193
	v_cvt_pk_fp8_f32 v177, v178, v179
	v_mul_f32_e32 v178, 0x42800000, v191
	v_mul_f32_e32 v179, 0x42800000, v195
	v_med3_f32 v178, v178, s93, v224
	v_med3_f32 v179, v179, s93, v224
	v_cvt_pk_fp8_f32 v177, v178, v179 op_sel:[0,0,1]
	ds_read2_b32 v[178:179], v137 offset0:32 offset1:40
	v_mad_i64_i32 v[196:197], s[0:1], s24, v136, v[148:149]
	v_lshl_add_u64 v[196:197], v[196:197], 0, v[132:133]
	ds_read2_b32 v[182:183], v137 offset0:97 offset1:105
	global_store_dwordx2 v[196:197], v[180:181], off
	v_mad_i64_i32 v[180:181], s[0:1], s24, v138, v[148:149]
	v_lshl_add_u64 v[180:181], v[180:181], 0, v[132:133]
	global_store_dwordx2 v[180:181], v[176:177], off
	s_waitcnt lgkmcnt(1)
	v_mul_f32_e32 v176, 0x42800000, v178
	v_med3_f32 v178, v176, s93, v224
	ds_read2_b32 v[176:177], v137 offset0:162 offset1:170
	ds_read2_b32 v[184:185], v137 offset0:227 offset1:235
	s_waitcnt lgkmcnt(2)
	v_mul_f32_e32 v180, 0x42800000, v182
	v_med3_f32 v181, v180, s93, v224
	v_mov_b32_e32 v180, v193
	ds_read2_b32 v[186:187], v139 offset0:36 offset1:44
	ds_read2_b32 v[188:189], v139 offset0:101 offset1:109
	v_cvt_pk_fp8_f32 v180, v178, v181
	s_waitcnt lgkmcnt(3)
	v_mul_f32_e32 v176, 0x42800000, v176
	s_waitcnt lgkmcnt(2)
	v_mul_f32_e32 v178, 0x42800000, v184
	v_med3_f32 v176, v176, s93, v224
	v_med3_f32 v178, v178, s93, v224
	ds_read2_b32 v[190:191], v139 offset0:166 offset1:174
	ds_read2_b32 v[194:195], v139 offset0:231 offset1:239
	v_cvt_pk_fp8_f32 v180, v176, v178 op_sel:[0,0,1]
	s_waitcnt lgkmcnt(3)
	v_mul_f32_e32 v176, 0x42800000, v186
	s_waitcnt lgkmcnt(2)
	v_mul_f32_e32 v178, 0x42800000, v188
	v_med3_f32 v176, v176, s93, v224
	v_med3_f32 v178, v178, s93, v224
	v_mov_b32_e32 v181, v193
	v_cvt_pk_fp8_f32 v181, v176, v178
	s_waitcnt lgkmcnt(1)
	v_mul_f32_e32 v176, 0x42800000, v190
	s_waitcnt lgkmcnt(0)
	v_mul_f32_e32 v178, 0x42800000, v194
	v_med3_f32 v176, v176, s93, v224
	v_med3_f32 v178, v178, s93, v224
	v_cvt_pk_fp8_f32 v181, v176, v178 op_sel:[0,0,1]
	v_mul_f32_e32 v176, 0x42800000, v179
	v_med3_f32 v178, v176, s93, v224
	v_mul_f32_e32 v176, 0x42800000, v183
	v_med3_f32 v179, v176, s93, v224
	v_mov_b32_e32 v176, v193
	v_cvt_pk_fp8_f32 v176, v178, v179
	v_mul_f32_e32 v177, 0x42800000, v177
	v_mul_f32_e32 v178, 0x42800000, v185
	v_med3_f32 v177, v177, s93, v224
	v_med3_f32 v178, v178, s93, v224
	v_cvt_pk_fp8_f32 v176, v177, v178 op_sel:[0,0,1]
	v_mul_f32_e32 v177, 0x42800000, v187
	v_med3_f32 v178, v177, s93, v224
	v_mul_f32_e32 v177, 0x42800000, v189
	v_med3_f32 v179, v177, s93, v224
	v_mov_b32_e32 v177, v193
	v_cvt_pk_fp8_f32 v177, v178, v179
	v_mul_f32_e32 v178, 0x42800000, v191
	v_mul_f32_e32 v179, 0x42800000, v195
	v_med3_f32 v178, v178, s93, v224
	v_med3_f32 v179, v179, s93, v224
	v_cvt_pk_fp8_f32 v177, v178, v179 op_sel:[0,0,1]
	ds_read2_b32 v[178:179], v137 offset0:48 offset1:56
	v_mad_i64_i32 v[196:197], s[0:1], s24, v140, v[148:149]
	v_lshl_add_u64 v[196:197], v[196:197], 0, v[132:133]
	ds_read2_b32 v[182:183], v137 offset0:113 offset1:121
	global_store_dwordx2 v[196:197], v[180:181], off
	v_mad_i64_i32 v[180:181], s[0:1], s24, v142, v[148:149]
	v_lshl_add_u64 v[180:181], v[180:181], 0, v[132:133]
	global_store_dwordx2 v[180:181], v[176:177], off
	s_waitcnt lgkmcnt(1)
	v_mul_f32_e32 v176, 0x42800000, v178
	v_med3_f32 v178, v176, s93, v224
	ds_read2_b32 v[176:177], v137 offset0:178 offset1:186
	ds_read2_b32 v[184:185], v137 offset0:243 offset1:251
	s_waitcnt lgkmcnt(2)
	v_mul_f32_e32 v180, 0x42800000, v182
	v_med3_f32 v181, v180, s93, v224
	v_mov_b32_e32 v180, v193
	ds_read2_b32 v[186:187], v139 offset0:52 offset1:60
	ds_read2_b32 v[188:189], v139 offset0:117 offset1:125
	v_cvt_pk_fp8_f32 v180, v178, v181
	s_waitcnt lgkmcnt(3)
	v_mul_f32_e32 v176, 0x42800000, v176
	s_waitcnt lgkmcnt(2)
	v_mul_f32_e32 v178, 0x42800000, v184
	v_med3_f32 v176, v176, s93, v224
	v_med3_f32 v178, v178, s93, v224
	ds_read2_b32 v[190:191], v139 offset0:182 offset1:190
	ds_read2_b32 v[194:195], v139 offset0:247 offset1:255
	v_cvt_pk_fp8_f32 v180, v176, v178 op_sel:[0,0,1]
	s_waitcnt lgkmcnt(3)
	v_mul_f32_e32 v176, 0x42800000, v186
	s_waitcnt lgkmcnt(2)
	v_mul_f32_e32 v178, 0x42800000, v188
	v_med3_f32 v176, v176, s93, v224
	v_med3_f32 v178, v178, s93, v224
	v_mov_b32_e32 v181, v193
	v_cvt_pk_fp8_f32 v181, v176, v178
	s_waitcnt lgkmcnt(1)
	v_mul_f32_e32 v176, 0x42800000, v190
	s_waitcnt lgkmcnt(0)
	v_mul_f32_e32 v178, 0x42800000, v194
	v_med3_f32 v176, v176, s93, v224
	v_med3_f32 v178, v178, s93, v224
	v_cvt_pk_fp8_f32 v181, v176, v178 op_sel:[0,0,1]
	v_mul_f32_e32 v176, 0x42800000, v179
	v_med3_f32 v178, v176, s93, v224
	v_mul_f32_e32 v176, 0x42800000, v183
	v_med3_f32 v179, v176, s93, v224
	v_mov_b32_e32 v176, v193
	v_cvt_pk_fp8_f32 v176, v178, v179
	v_mul_f32_e32 v177, 0x42800000, v177
	v_mul_f32_e32 v178, 0x42800000, v185
	v_med3_f32 v177, v177, s93, v224
	v_med3_f32 v178, v178, s93, v224
	v_cvt_pk_fp8_f32 v176, v177, v178 op_sel:[0,0,1]
	v_mul_f32_e32 v177, 0x42800000, v187
	v_med3_f32 v178, v177, s93, v224
	v_mul_f32_e32 v177, 0x42800000, v189
	v_med3_f32 v179, v177, s93, v224
	v_mov_b32_e32 v177, v193
	v_cvt_pk_fp8_f32 v177, v178, v179
	v_mul_f32_e32 v178, 0x42800000, v191
	v_mul_f32_e32 v179, 0x42800000, v195
	v_med3_f32 v178, v178, s93, v224
	v_med3_f32 v179, v179, s93, v224
	v_cvt_pk_fp8_f32 v177, v178, v179 op_sel:[0,0,1]
	v_mad_i64_i32 v[196:197], s[0:1], s24, v144, v[148:149]
	v_mad_i64_i32 v[148:149], s[0:1], s24, v146, v[148:149]
	v_lshl_add_u64 v[196:197], v[196:197], 0, v[132:133]
	v_lshl_add_u64 v[148:149], v[148:149], 0, v[132:133]
	global_store_dwordx2 v[196:197], v[180:181], off
	global_store_dwordx2 v[148:149], v[176:177], off
	s_waitcnt lgkmcnt(0)
	s_cmp_lt_i32 s29, 0x185e8
	s_cselect_b64 s[10:11], -1, 0
	s_cmp_gt_i32 s29, 0x185e7
	s_cbranch_scc0 .LBB0_1305

; #define LAS __attribute__((address_space(3)))
; __device__ __forceinline__ float clamp8(float x) { return __builtin_amdgcn_fmed3f(x, -448.f, 448.f); }
; #define LDS_WAIT() asm volatile("s_waitcnt lgkmcnt(0)" ::: "memory")
; __device__ __forceinline__ void cvt_finish(const CvtDesc& d, const float (&t)[64], LAS float* scr, int lane) {
;     LAS float* sw = scr + (lane >> 4) * 65 + 4 * (lane & 15);
; #pragma unroll
;     for (int i = 0; i < 16; ++i) { sw[(4 * i) * 65] = t[4 * i]; sw[(4 * i) * 65 + 1] = t[4 * i + 1]; sw[(4 * i) * 65 + 2] = t[4 * i + 2]; sw[(4 * i) * 65 + 3] = t[4 * i + 3]; }
;     LDS_WAIT();
;     const int c = lane & 7;
;     if (d.f8) {
; #pragma unroll
;         for (int j = 0; j < 8; ++j) { const int n = (lane >> 3) + 8 * j; const LAS float* s = scr + (8 * c) * 65 + n;
;             int a = __builtin_amdgcn_cvt_pk_fp8_f32(clamp8(s[0 * 65] * W8_SCALE), clamp8(s[1 * 65] * W8_SCALE), 0, false); a = __builtin_amdgcn_cvt_pk_fp8_f32(clamp8(s[2 * 65] * W8_SCALE), clamp8(s[3 * 65] * W8_SCALE), a, true);
;             int b = __builtin_amdgcn_cvt_pk_fp8_f32(clamp8(s[4 * 65] * W8_SCALE), clamp8(s[5 * 65] * W8_SCALE), 0, false); b = __builtin_amdgcn_cvt_pk_fp8_f32(clamp8(s[6 * 65] * W8_SCALE), clamp8(s[7 * 65] * W8_SCALE), b, true);
;             __builtin_nontemporal_store((u32x2){(unsigned)a, (unsigned)b}, (u32x2*)(d.dst + (size_t)n * d.dKB + 8 * c)); }
;     ...
;             if (v2) cvt_finish(da, ta, scr, lane);
;             if (v3) cvt_finish(db, tb, scr, lane);
.LBB0_1287:
	s_waitcnt vmcnt(0)
	ds_write2_b32 v135, v16, v17 offset1:1
	ds_write2_b32 v135, v18, v19 offset0:2 offset1:3
	ds_write2_b32 v141, v24, v25 offset1:1
	ds_write2_b32 v143, v26, v27 offset1:1
	ds_write2_b32 v145, v32, v33 offset1:1
	ds_write2_b32 v147, v34, v35 offset1:1
	ds_write2_b32 v150, v40, v41 offset1:1
	ds_write2_b32 v151, v42, v43 offset1:1
	ds_write2_b32 v152, v52, v53 offset1:1
	ds_write2_b32 v153, v54, v55 offset1:1
	ds_write2_b32 v154, v56, v57 offset1:1
	ds_write2_b32 v155, v58, v59 offset1:1
	ds_write2_b32 v156, v68, v69 offset1:1
	ds_write2_b32 v157, v70, v71 offset1:1
	ds_write2_b32 v158, v72, v73 offset1:1
	ds_write2_b32 v159, v74, v75 offset1:1
	ds_write2_b32 v160, v80, v81 offset1:1
	ds_write2_b32 v161, v82, v83 offset1:1
	ds_write2_b32 v162, v88, v89 offset1:1
	ds_write2_b32 v163, v90, v91 offset1:1
	ds_write2_b32 v164, v96, v97 offset1:1
	ds_write2_b32 v165, v98, v99 offset1:1
	ds_write2_b32 v166, v104, v105 offset1:1
	ds_write2_b32 v167, v106, v107 offset1:1
	ds_write2_b32 v168, v112, v113 offset1:1
	ds_write2_b32 v169, v114, v115 offset1:1
	ds_write2_b32 v170, v116, v117 offset1:1
	ds_write2_b32 v171, v118, v119 offset1:1
	ds_write2_b32 v172, v120, v121 offset1:1
	ds_write2_b32 v173, v122, v123 offset1:1
	ds_write2_b32 v174, v124, v125 offset1:1
	ds_write2_b32 v175, v126, v127 offset1:1
	s_waitcnt lgkmcnt(0)
	ds_read2_b32 v[176:177], v137 offset1:8
	ds_read2_b32 v[178:179], v137 offset0:65 offset1:73
	ds_read2_b32 v[180:181], v137 offset0:130 offset1:138
	ds_read2_b32 v[184:185], v137 offset0:195 offset1:203
	v_mov_b32_e32 v182, v193
	s_waitcnt lgkmcnt(3)
	v_mul_f32_e32 v148, 0x42800000, v176
	s_waitcnt lgkmcnt(2)
	v_mul_f32_e32 v149, 0x42800000, v178
	v_mul_f32_e32 v176, 0x42800000, v177
	v_med3_f32 v148, v148, s93, v224
	v_med3_f32 v149, v149, s93, v224
	ds_read2_b32 v[186:187], v139 offset0:4 offset1:12
	ds_read2_b32 v[188:189], v139 offset0:69 offset1:77
	v_med3_f32 v177, v176, s93, v224
	v_mul_f32_e32 v176, 0x42800000, v179
	v_cvt_pk_fp8_f32 v182, v148, v149
	v_med3_f32 v178, v176, s93, v224
	v_mov_b32_e32 v176, v193
	v_cvt_pk_fp8_f32 v176, v177, v178
	s_waitcnt lgkmcnt(3)
	v_mul_f32_e32 v148, 0x42800000, v180
	s_waitcnt lgkmcnt(2)
	v_mul_f32_e32 v149, 0x42800000, v184
	v_med3_f32 v148, v148, s93, v224
	v_med3_f32 v149, v149, s93, v224
	ds_read2_b32 v[190:191], v139 offset0:134 offset1:142
	ds_read2_b32 v[194:195], v139 offset0:199 offset1:207
	v_mul_f32_e32 v177, 0x42800000, v181
	v_mul_f32_e32 v178, 0x42800000, v185
	v_cvt_pk_fp8_f32 v182, v148, v149 op_sel:[0,0,1]
	s_waitcnt lgkmcnt(3)
	v_mul_f32_e32 v148, 0x42800000, v186
	s_waitcnt lgkmcnt(2)
	v_mul_f32_e32 v149, 0x42800000, v188
	v_med3_f32 v177, v177, s93, v224
	v_med3_f32 v178, v178, s93, v224
	v_med3_f32 v148, v148, s93, v224
	v_med3_f32 v149, v149, s93, v224
	v_mov_b32_e32 v183, v193
	v_cvt_pk_fp8_f32 v176, v177, v178 op_sel:[0,0,1]
	v_mul_f32_e32 v177, 0x42800000, v187
	v_cvt_pk_fp8_f32 v183, v148, v149
	v_med3_f32 v178, v177, s93, v224
	v_mul_f32_e32 v177, 0x42800000, v189
	v_med3_f32 v179, v177, s93, v224
	v_mov_b32_e32 v177, v193
	s_waitcnt lgkmcnt(1)
	v_mul_f32_e32 v148, 0x42800000, v190
	s_waitcnt lgkmcnt(0)
	v_mul_f32_e32 v149, 0x42800000, v194
	v_cvt_pk_fp8_f32 v177, v178, v179
	v_med3_f32 v148, v148, s93, v224
	v_med3_f32 v149, v149, s93, v224
	v_cvt_pk_fp8_f32 v183, v148, v149 op_sel:[0,0,1]
	v_mul_f32_e32 v178, 0x42800000, v191
	v_mul_f32_e32 v179, 0x42800000, v195
	v_mov_b64_e32 v[148:149], s[8:9]
	v_med3_f32 v178, v178, s93, v224
	v_med3_f32 v179, v179, s93, v224
	v_mad_i64_i32 v[196:197], s[0:1], s25, v130, v[148:149]
	v_cvt_pk_fp8_f32 v177, v178, v179 op_sel:[0,0,1]
	ds_read2_b32 v[178:179], v137 offset0:16 offset1:24
	v_lshl_add_u64 v[196:197], v[196:197], 0, v[132:133]
	global_store_dwordx2 v[196:197], v[182:183], off
	ds_read2_b32 v[182:183], v137 offset0:81 offset1:89
	v_mad_i64_i32 v[180:181], s[0:1], s25, v134, v[148:149]
	v_lshl_add_u64 v[180:181], v[180:181], 0, v[132:133]
	global_store_dwordx2 v[180:181], v[176:177], off
	s_waitcnt lgkmcnt(1)
	v_mul_f32_e32 v176, 0x42800000, v178
	v_med3_f32 v178, v176, s93, v224
	ds_read2_b32 v[176:177], v137 offset0:146 offset1:154
	ds_read2_b32 v[184:185], v137 offset0:211 offset1:219
	s_waitcnt lgkmcnt(2)
	v_mul_f32_e32 v180, 0x42800000, v182
	v_med3_f32 v181, v180, s93, v224
	v_mov_b32_e32 v180, v193
	ds_read2_b32 v[186:187], v139 offset0:20 offset1:28
	ds_read2_b32 v[188:189], v139 offset0:85 offset1:93
	v_cvt_pk_fp8_f32 v180, v178, v181
	s_waitcnt lgkmcnt(3)
	v_mul_f32_e32 v176, 0x42800000, v176
	s_waitcnt lgkmcnt(2)
	v_mul_f32_e32 v178, 0x42800000, v184
	v_med3_f32 v176, v176, s93, v224
	v_med3_f32 v178, v178, s93, v224
	ds_read2_b32 v[190:191], v139 offset0:150 offset1:158
	ds_read2_b32 v[194:195], v139 offset0:215 offset1:223
	v_cvt_pk_fp8_f32 v180, v176, v178 op_sel:[0,0,1]
	s_waitcnt lgkmcnt(3)
	v_mul_f32_e32 v176, 0x42800000, v186
	s_waitcnt lgkmcnt(2)
	v_mul_f32_e32 v178, 0x42800000, v188
	v_med3_f32 v176, v176, s93, v224
	v_med3_f32 v178, v178, s93, v224
	v_mov_b32_e32 v181, v193
	v_cvt_pk_fp8_f32 v181, v176, v178
	s_waitcnt lgkmcnt(1)
	v_mul_f32_e32 v176, 0x42800000, v190
	s_waitcnt lgkmcnt(0)
; #define LAS __attribute__((address_space(3)))
; __device__ __forceinline__ float clamp8(float x) { return __builtin_amdgcn_fmed3f(x, -448.f, 448.f); }
; #define LDS_WAIT() asm volatile("s_waitcnt lgkmcnt(0)" ::: "memory")
; __device__ __forceinline__ void cvt_finish(const CvtDesc& d, const float (&t)[64], LAS float* scr, int lane) {
;     LAS float* sw = scr + (lane >> 4) * 65 + 4 * (lane & 15);
; #pragma unroll
;     for (int i = 0; i < 16; ++i) { sw[(4 * i) * 65] = t[4 * i]; sw[(4 * i) * 65 + 1] = t[4 * i + 1]; sw[(4 * i) * 65 + 2] = t[4 * i + 2]; sw[(4 * i) * 65 + 3] = t[4 * i + 3]; }
;     LDS_WAIT();
;     const int c = lane & 7;
;     if (d.f8) {
; #pragma unroll
;         for (int j = 0; j < 8; ++j) { const int n = (lane >> 3) + 8 * j; const LAS float* s = scr + (8 * c) * 65 + n;
;             int a = __builtin_amdgcn_cvt_pk_fp8_f32(clamp8(s[0 * 65] * W8_SCALE), clamp8(s[1 * 65] * W8_SCALE), 0, false); a = __builtin_amdgcn_cvt_pk_fp8_f32(clamp8(s[2 * 65] * W8_SCALE), clamp8(s[3 * 65] * W8_SCALE), a, true);
;             int b = __builtin_amdgcn_cvt_pk_fp8_f32(clamp8(s[4 * 65] * W8_SCALE), clamp8(s[5 * 65] * W8_SCALE), 0, false); b = __builtin_amdgcn_cvt_pk_fp8_f32(clamp8(s[6 * 65] * W8_SCALE), clamp8(s[7 * 65] * W8_SCALE), b, true);
;             __builtin_nontemporal_store((u32x2){(unsigned)a, (unsigned)b}, (u32x2*)(d.dst + (size_t)n * d.dKB + 8 * c)); }
;     ...
;             if (v2) cvt_finish(da, ta, scr, lane);
;             if (v3) cvt_finish(db, tb, scr, lane);
	v_mul_f32_e32 v178, 0x42800000, v194
	v_med3_f32 v176, v176, s93, v224
	v_med3_f32 v178, v178, s93, v224
	v_cvt_pk_fp8_f32 v181, v176, v178 op_sel:[0,0,1]
	v_mul_f32_e32 v176, 0x42800000, v179
	v_med3_f32 v178, v176, s93, v224
	v_mul_f32_e32 v176, 0x42800000, v183
	v_med3_f32 v179, v176, s93, v224
	v_mov_b32_e32 v176, v193
	v_cvt_pk_fp8_f32 v176, v178, v179
	v_mul_f32_e32 v177, 0x42800000, v177
	v_mul_f32_e32 v178, 0x42800000, v185
	v_med3_f32 v177, v177, s93, v224
	v_med3_f32 v178, v178, s93, v224
	v_cvt_pk_fp8_f32 v176, v177, v178 op_sel:[0,0,1]
	v_mul_f32_e32 v177, 0x42800000, v187
	v_med3_f32 v178, v177, s93, v224
	v_mul_f32_e32 v177, 0x42800000, v189
	v_med3_f32 v179, v177, s93, v224
	v_mov_b32_e32 v177, v193
	v_cvt_pk_fp8_f32 v177, v178, v179
	v_mul_f32_e32 v178, 0x42800000, v191
	v_mul_f32_e32 v179, 0x42800000, v195
	v_med3_f32 v178, v178, s93, v224
	v_med3_f32 v179, v179, s93, v224
	v_cvt_pk_fp8_f32 v177, v178, v179 op_sel:[0,0,1]
	ds_read2_b32 v[178:179], v137 offset0:32 offset1:40
	v_mad_i64_i32 v[196:197], s[0:1], s25, v136, v[148:149]
	v_lshl_add_u64 v[196:197], v[196:197], 0, v[132:133]
	ds_read2_b32 v[182:183], v137 offset0:97 offset1:105
	global_store_dwordx2 v[196:197], v[180:181], off
	v_mad_i64_i32 v[180:181], s[0:1], s25, v138, v[148:149]
	v_lshl_add_u64 v[180:181], v[180:181], 0, v[132:133]
	global_store_dwordx2 v[180:181], v[176:177], off
	s_waitcnt lgkmcnt(1)
	v_mul_f32_e32 v176, 0x42800000, v178
	v_med3_f32 v178, v176, s93, v224
	ds_read2_b32 v[176:177], v137 offset0:162 offset1:170
	ds_read2_b32 v[184:185], v137 offset0:227 offset1:235
	s_waitcnt lgkmcnt(2)
	v_mul_f32_e32 v180, 0x42800000, v182
	v_med3_f32 v181, v180, s93, v224
	v_mov_b32_e32 v180, v193
	ds_read2_b32 v[186:187], v139 offset0:36 offset1:44
	ds_read2_b32 v[188:189], v139 offset0:101 offset1:109
	v_cvt_pk_fp8_f32 v180, v178, v181
	s_waitcnt lgkmcnt(3)
	v_mul_f32_e32 v176, 0x42800000, v176
	s_waitcnt lgkmcnt(2)
	v_mul_f32_e32 v178, 0x42800000, v184
	v_med3_f32 v176, v176, s93, v224
	v_med3_f32 v178, v178, s93, v224
	ds_read2_b32 v[190:191], v139 offset0:166 offset1:174
	ds_read2_b32 v[194:195], v139 offset0:231 offset1:239
	v_cvt_pk_fp8_f32 v180, v176, v178 op_sel:[0,0,1]
	s_waitcnt lgkmcnt(3)
	v_mul_f32_e32 v176, 0x42800000, v186
	s_waitcnt lgkmcnt(2)
	v_mul_f32_e32 v178, 0x42800000, v188
	v_med3_f32 v176, v176, s93, v224
	v_med3_f32 v178, v178, s93, v224
	v_mov_b32_e32 v181, v193
	v_cvt_pk_fp8_f32 v181, v176, v178
	s_waitcnt lgkmcnt(1)
	v_mul_f32_e32 v176, 0x42800000, v190
	s_waitcnt lgkmcnt(0)
	v_mul_f32_e32 v178, 0x42800000, v194
	v_med3_f32 v176, v176, s93, v224
	v_med3_f32 v178, v178, s93, v224
	v_cvt_pk_fp8_f32 v181, v176, v178 op_sel:[0,0,1]
	v_mul_f32_e32 v176, 0x42800000, v179
	v_med3_f32 v178, v176, s93, v224
	v_mul_f32_e32 v176, 0x42800000, v183
	v_med3_f32 v179, v176, s93, v224
	v_mov_b32_e32 v176, v193
	v_cvt_pk_fp8_f32 v176, v178, v179
	v_mul_f32_e32 v177, 0x42800000, v177
	v_mul_f32_e32 v178, 0x42800000, v185
	v_med3_f32 v177, v177, s93, v224
	v_med3_f32 v178, v178, s93, v224
	v_cvt_pk_fp8_f32 v176, v177, v178 op_sel:[0,0,1]
	v_mul_f32_e32 v177, 0x42800000, v187
	v_med3_f32 v178, v177, s93, v224
	v_mul_f32_e32 v177, 0x42800000, v189
	v_med3_f32 v179, v177, s93, v224
	v_mov_b32_e32 v177, v193
	v_cvt_pk_fp8_f32 v177, v178, v179
	v_mul_f32_e32 v178, 0x42800000, v191
	v_mul_f32_e32 v179, 0x42800000, v195
	v_med3_f32 v178, v178, s93, v224
	v_med3_f32 v179, v179, s93, v224
	v_cvt_pk_fp8_f32 v177, v178, v179 op_sel:[0,0,1]
	ds_read2_b32 v[178:179], v137 offset0:48 offset1:56
	v_mad_i64_i32 v[196:197], s[0:1], s25, v140, v[148:149]
	v_lshl_add_u64 v[196:197], v[196:197], 0, v[132:133]
	ds_read2_b32 v[182:183], v137 offset0:113 offset1:121
	global_store_dwordx2 v[196:197], v[180:181], off
	v_mad_i64_i32 v[180:181], s[0:1], s25, v142, v[148:149]
	v_lshl_add_u64 v[180:181], v[180:181], 0, v[132:133]
	global_store_dwordx2 v[180:181], v[176:177], off
	s_waitcnt lgkmcnt(1)
	v_mul_f32_e32 v176, 0x42800000, v178
	v_med3_f32 v178, v176, s93, v224
	ds_read2_b32 v[176:177], v137 offset0:178 offset1:186
	ds_read2_b32 v[184:185], v137 offset0:243 offset1:251
	s_waitcnt lgkmcnt(2)
	v_mul_f32_e32 v180, 0x42800000, v182
	v_med3_f32 v181, v180, s93, v224
	v_mov_b32_e32 v180, v193
	ds_read2_b32 v[186:187], v139 offset0:52 offset1:60
	ds_read2_b32 v[188:189], v139 offset0:117 offset1:125
	v_cvt_pk_fp8_f32 v180, v178, v181
	s_waitcnt lgkmcnt(3)
	v_mul_f32_e32 v176, 0x42800000, v176
	s_waitcnt lgkmcnt(2)
	v_mul_f32_e32 v178, 0x42800000, v184
	v_med3_f32 v176, v176, s93, v224
	v_med3_f32 v178, v178, s93, v224
	ds_read2_b32 v[190:191], v139 offset0:182 offset1:190
	ds_read2_b32 v[194:195], v139 offset0:247 offset1:255
	v_cvt_pk_fp8_f32 v180, v176, v178 op_sel:[0,0,1]
	s_waitcnt lgkmcnt(3)
	v_mul_f32_e32 v176, 0x42800000, v186
	s_waitcnt lgkmcnt(2)
	v_mul_f32_e32 v178, 0x42800000, v188
	v_med3_f32 v176, v176, s93, v224
	v_med3_f32 v178, v178, s93, v224
	v_mov_b32_e32 v181, v193
	v_cvt_pk_fp8_f32 v181, v176, v178
	s_waitcnt lgkmcnt(1)
	v_mul_f32_e32 v176, 0x42800000, v190
	s_waitcnt lgkmcnt(0)
	v_mul_f32_e32 v178, 0x42800000, v194
	v_med3_f32 v176, v176, s93, v224
	v_med3_f32 v178, v178, s93, v224
	v_cvt_pk_fp8_f32 v181, v176, v178 op_sel:[0,0,1]
	v_mul_f32_e32 v176, 0x42800000, v179
	v_med3_f32 v178, v176, s93, v224
	v_mul_f32_e32 v176, 0x42800000, v183
	v_med3_f32 v179, v176, s93, v224
	v_mov_b32_e32 v176, v193
	v_cvt_pk_fp8_f32 v176, v178, v179
	v_mul_f32_e32 v177, 0x42800000, v177
	v_mul_f32_e32 v178, 0x42800000, v185
	v_med3_f32 v177, v177, s93, v224
	v_med3_f32 v178, v178, s93, v224
	v_cvt_pk_fp8_f32 v176, v177, v178 op_sel:[0,0,1]
	v_mul_f32_e32 v177, 0x42800000, v187
	v_med3_f32 v178, v177, s93, v224
	v_mul_f32_e32 v177, 0x42800000, v189
	v_med3_f32 v179, v177, s93, v224
	v_mov_b32_e32 v177, v193
	v_cvt_pk_fp8_f32 v177, v178, v179
	v_mul_f32_e32 v178, 0x42800000, v191
	v_mul_f32_e32 v179, 0x42800000, v195
	v_med3_f32 v178, v178, s93, v224
	v_med3_f32 v179, v179, s93, v224
	v_cvt_pk_fp8_f32 v177, v178, v179 op_sel:[0,0,1]
	v_mad_i64_i32 v[196:197], s[0:1], s25, v144, v[148:149]
	v_mad_i64_i32 v[148:149], s[0:1], s25, v146, v[148:149]
	v_lshl_add_u64 v[196:197], v[196:197], 0, v[132:133]
	v_lshl_add_u64 v[148:149], v[148:149], 0, v[132:133]
	global_store_dwordx2 v[196:197], v[180:181], off
	global_store_dwordx2 v[148:149], v[176:177], off
	s_waitcnt lgkmcnt(0)
	s_andn2_b64 vcc, exec, s[10:11]
	s_cbranch_vccz .LBB0_1321
	s_branch .LBB0_1322

; #define LAS __attribute__((address_space(3)))
; __device__ __forceinline__ float clamp8(float x) { return __builtin_amdgcn_fmed3f(x, -448.f, 448.f); }
; #define LDS_WAIT() asm volatile("s_waitcnt lgkmcnt(0)" ::: "memory")
; __device__ __forceinline__ void cvt_finish(const CvtDesc& d, const float (&t)[64], LAS float* scr, int lane) {
;     LAS float* sw = scr + (lane >> 4) * 65 + 4 * (lane & 15);
; #pragma unroll
;     for (int i = 0; i < 16; ++i) { sw[(4 * i) * 65] = t[4 * i]; sw[(4 * i) * 65 + 1] = t[4 * i + 1]; sw[(4 * i) * 65 + 2] = t[4 * i + 2]; sw[(4 * i) * 65 + 3] = t[4 * i + 3]; }
;     LDS_WAIT();
;     const int c = lane & 7;
;     if (d.f8) {
; #pragma unroll
;         for (int j = 0; j < 8; ++j) { const int n = (lane >> 3) + 8 * j; const LAS float* s = scr + (8 * c) * 65 + n;
;             int a = __builtin_amdgcn_cvt_pk_fp8_f32(clamp8(s[0 * 65] * W8_SCALE), clamp8(s[1 * 65] * W8_SCALE), 0, false); a = __builtin_amdgcn_cvt_pk_fp8_f32(clamp8(s[2 * 65] * W8_SCALE), clamp8(s[3 * 65] * W8_SCALE), a, true);
;             int b = __builtin_amdgcn_cvt_pk_fp8_f32(clamp8(s[4 * 65] * W8_SCALE), clamp8(s[5 * 65] * W8_SCALE), 0, false); b = __builtin_amdgcn_cvt_pk_fp8_f32(clamp8(s[6 * 65] * W8_SCALE), clamp8(s[7 * 65] * W8_SCALE), b, true);
;             __builtin_nontemporal_store((u32x2){(unsigned)a, (unsigned)b}, (u32x2*)(d.dst + (size_t)n * d.dKB + 8 * c)); }
;     ...
;             if (v3) cvt_finish(db, tb, scr, lane);
.LBB0_1321:
	s_waitcnt vmcnt(0)
	ds_write2_b32 v135, v0, v1 offset1:1
	ds_write2_b32 v135, v2, v3 offset0:2 offset1:3
	ds_write2_b32 v141, v4, v5 offset1:1
	ds_write2_b32 v143, v6, v7 offset1:1
	ds_write2_b32 v145, v8, v9 offset1:1
	ds_write2_b32 v147, v10, v11 offset1:1
	ds_write2_b32 v150, v12, v13 offset1:1
	ds_write2_b32 v151, v14, v15 offset1:1
	ds_write2_b32 v152, v20, v21 offset1:1
	ds_write2_b32 v153, v22, v23 offset1:1
	ds_write2_b32 v154, v28, v29 offset1:1
	ds_write2_b32 v155, v30, v31 offset1:1
	ds_write2_b32 v156, v36, v37 offset1:1
	ds_write2_b32 v157, v38, v39 offset1:1
	ds_write2_b32 v158, v44, v45 offset1:1
	ds_write2_b32 v159, v46, v47 offset1:1
	ds_write2_b32 v160, v48, v49 offset1:1
	ds_write2_b32 v161, v50, v51 offset1:1
	ds_write2_b32 v162, v60, v61 offset1:1
	ds_write2_b32 v163, v62, v63 offset1:1
	ds_write2_b32 v164, v64, v65 offset1:1
	ds_write2_b32 v165, v66, v67 offset1:1
	ds_write2_b32 v166, v76, v77 offset1:1
	ds_write2_b32 v167, v78, v79 offset1:1
	ds_write2_b32 v168, v84, v85 offset1:1
	ds_write2_b32 v169, v86, v87 offset1:1
	ds_write2_b32 v170, v92, v93 offset1:1
	ds_write2_b32 v171, v94, v95 offset1:1
	ds_write2_b32 v172, v100, v101 offset1:1
	ds_write2_b32 v173, v102, v103 offset1:1
	ds_write2_b32 v174, v108, v109 offset1:1
	ds_write2_b32 v175, v110, v111 offset1:1
	s_waitcnt lgkmcnt(0)
	ds_read2_b32 v[150:151], v137 offset1:8
	ds_read2_b32 v[152:153], v137 offset0:65 offset1:73
	ds_read2_b32 v[154:155], v137 offset0:130 offset1:138
	ds_read2_b32 v[158:159], v137 offset0:195 offset1:203
	v_mov_b32_e32 v156, v193
	s_waitcnt lgkmcnt(3)
	v_mul_f32_e32 v141, 0x42800000, v150
	s_waitcnt lgkmcnt(2)
	v_mul_f32_e32 v143, 0x42800000, v152
	v_med3_f32 v141, v141, s93, v224
	v_med3_f32 v143, v143, s93, v224
	ds_read2_b32 v[160:161], v139 offset0:4 offset1:12
	ds_read2_b32 v[162:163], v139 offset0:69 offset1:77
	v_cvt_pk_fp8_f32 v156, v141, v143
	s_waitcnt lgkmcnt(3)
	v_mul_f32_e32 v141, 0x42800000, v154
	s_waitcnt lgkmcnt(2)
	v_mul_f32_e32 v143, 0x42800000, v158
	v_med3_f32 v141, v141, s93, v224
	v_med3_f32 v143, v143, s93, v224
	ds_read2_b32 v[164:165], v139 offset0:134 offset1:142
	ds_read2_b32 v[166:167], v139 offset0:199 offset1:207
	v_cvt_pk_fp8_f32 v156, v141, v143 op_sel:[0,0,1]
	s_waitcnt lgkmcnt(3)
	v_mul_f32_e32 v141, 0x42800000, v160
	s_waitcnt lgkmcnt(2)
	v_mul_f32_e32 v143, 0x42800000, v162
	v_med3_f32 v141, v141, s93, v224
	v_med3_f32 v143, v143, s93, v224
	v_mov_b32_e32 v157, v193
	v_cvt_pk_fp8_f32 v157, v141, v143
	s_waitcnt lgkmcnt(1)
	v_mul_f32_e32 v141, 0x42800000, v164
	s_waitcnt lgkmcnt(0)
	v_mul_f32_e32 v143, 0x42800000, v166
	v_med3_f32 v141, v141, s93, v224
	v_med3_f32 v143, v143, s93, v224
	v_cvt_pk_fp8_f32 v157, v141, v143 op_sel:[0,0,1]
	v_mul_f32_e32 v141, 0x42800000, v151
	v_mul_f32_e32 v143, 0x42800000, v153
	v_med3_f32 v141, v141, s93, v224
	v_med3_f32 v143, v143, s93, v224
	v_mov_b32_e32 v150, v193
	v_cvt_pk_fp8_f32 v150, v141, v143
	v_mul_f32_e32 v141, 0x42800000, v155
	v_mul_f32_e32 v143, 0x42800000, v159
	v_med3_f32 v141, v141, s93, v224
	v_med3_f32 v143, v143, s93, v224
	v_cvt_pk_fp8_f32 v150, v141, v143 op_sel:[0,0,1]
	v_mul_f32_e32 v141, 0x42800000, v161
	v_mul_f32_e32 v143, 0x42800000, v163
	v_med3_f32 v141, v141, s93, v224
	v_med3_f32 v143, v143, s93, v224
	v_mov_b32_e32 v151, v193
	v_cvt_pk_fp8_f32 v151, v141, v143
	v_mov_b64_e32 v[148:149], s[6:7]
	v_mad_i64_i32 v[168:169], s[0:1], s24, v130, v[148:149]
	v_mul_f32_e32 v141, 0x42800000, v165
	v_mul_f32_e32 v143, 0x42800000, v167
	v_lshl_add_u64 v[168:169], v[168:169], 0, v[132:133]
	v_med3_f32 v141, v141, s93, v224
	v_med3_f32 v143, v143, s93, v224
	global_store_dwordx2 v[168:169], v[156:157], off
	v_cvt_pk_fp8_f32 v151, v141, v143 op_sel:[0,0,1]
	ds_read2_b32 v[152:153], v137 offset0:16 offset1:24
	ds_read2_b32 v[156:157], v137 offset0:81 offset1:89
	v_mad_i64_i32 v[154:155], s[0:1], s24, v134, v[148:149]
	v_lshl_add_u64 v[154:155], v[154:155], 0, v[132:133]
	global_store_dwordx2 v[154:155], v[150:151], off
	ds_read2_b32 v[150:151], v137 offset0:146 offset1:154
	ds_read2_b32 v[158:159], v137 offset0:211 offset1:219
	s_waitcnt lgkmcnt(3)
	v_mul_f32_e32 v141, 0x42800000, v152
	s_waitcnt lgkmcnt(2)
	v_mul_f32_e32 v143, 0x42800000, v156
	v_med3_f32 v141, v141, s93, v224
	v_med3_f32 v143, v143, s93, v224
	v_mov_b32_e32 v154, v193
	ds_read2_b32 v[160:161], v139 offset0:20 offset1:28
	ds_read2_b32 v[162:163], v139 offset0:85 offset1:93
	v_cvt_pk_fp8_f32 v154, v141, v143
	s_waitcnt lgkmcnt(3)
	v_mul_f32_e32 v141, 0x42800000, v150
	s_waitcnt lgkmcnt(2)
	v_mul_f32_e32 v143, 0x42800000, v158
	v_med3_f32 v141, v141, s93, v224
	v_med3_f32 v143, v143, s93, v224
	ds_read2_b32 v[164:165], v139 offset0:150 offset1:158
	ds_read2_b32 v[166:167], v139 offset0:215 offset1:223
	v_cvt_pk_fp8_f32 v154, v141, v143 op_sel:[0,0,1]
	s_waitcnt lgkmcnt(3)
	v_mul_f32_e32 v141, 0x42800000, v160
	s_waitcnt lgkmcnt(2)
	v_mul_f32_e32 v143, 0x42800000, v162
	v_med3_f32 v141, v141, s93, v224
	v_med3_f32 v143, v143, s93, v224
	v_mov_b32_e32 v155, v193
	v_cvt_pk_fp8_f32 v155, v141, v143
	s_waitcnt lgkmcnt(1)
	v_mul_f32_e32 v141, 0x42800000, v164
	s_waitcnt lgkmcnt(0)
; #define LAS __attribute__((address_space(3)))
; __device__ __forceinline__ float clamp8(float x) { return __builtin_amdgcn_fmed3f(x, -448.f, 448.f); }
; #define LDS_WAIT() asm volatile("s_waitcnt lgkmcnt(0)" ::: "memory")
; __device__ __forceinline__ void cvt_finish(const CvtDesc& d, const float (&t)[64], LAS float* scr, int lane) {
;     LAS float* sw = scr + (lane >> 4) * 65 + 4 * (lane & 15);
; #pragma unroll
;     for (int i = 0; i < 16; ++i) { sw[(4 * i) * 65] = t[4 * i]; sw[(4 * i) * 65 + 1] = t[4 * i + 1]; sw[(4 * i) * 65 + 2] = t[4 * i + 2]; sw[(4 * i) * 65 + 3] = t[4 * i + 3]; }
;     LDS_WAIT();
;     const int c = lane & 7;
;     if (d.f8) {
; #pragma unroll
;         for (int j = 0; j < 8; ++j) { const int n = (lane >> 3) + 8 * j; const LAS float* s = scr + (8 * c) * 65 + n;
;             int a = __builtin_amdgcn_cvt_pk_fp8_f32(clamp8(s[0 * 65] * W8_SCALE), clamp8(s[1 * 65] * W8_SCALE), 0, false); a = __builtin_amdgcn_cvt_pk_fp8_f32(clamp8(s[2 * 65] * W8_SCALE), clamp8(s[3 * 65] * W8_SCALE), a, true);
;             int b = __builtin_amdgcn_cvt_pk_fp8_f32(clamp8(s[4 * 65] * W8_SCALE), clamp8(s[5 * 65] * W8_SCALE), 0, false); b = __builtin_amdgcn_cvt_pk_fp8_f32(clamp8(s[6 * 65] * W8_SCALE), clamp8(s[7 * 65] * W8_SCALE), b, true);
;             __builtin_nontemporal_store((u32x2){(unsigned)a, (unsigned)b}, (u32x2*)(d.dst + (size_t)n * d.dKB + 8 * c)); }
	v_mul_f32_e32 v143, 0x42800000, v166
	v_med3_f32 v141, v141, s93, v224
	v_med3_f32 v143, v143, s93, v224
	v_cvt_pk_fp8_f32 v155, v141, v143 op_sel:[0,0,1]
	v_mul_f32_e32 v141, 0x42800000, v153
	v_mul_f32_e32 v143, 0x42800000, v157
	v_med3_f32 v141, v141, s93, v224
	v_med3_f32 v143, v143, s93, v224
	v_mov_b32_e32 v150, v193
	v_cvt_pk_fp8_f32 v150, v141, v143
	v_mul_f32_e32 v141, 0x42800000, v151
	v_mul_f32_e32 v143, 0x42800000, v159
	v_med3_f32 v141, v141, s93, v224
	v_med3_f32 v143, v143, s93, v224
	v_cvt_pk_fp8_f32 v150, v141, v143 op_sel:[0,0,1]
	v_mul_f32_e32 v141, 0x42800000, v161
	v_mul_f32_e32 v143, 0x42800000, v163
	v_med3_f32 v141, v141, s93, v224
	v_med3_f32 v143, v143, s93, v224
	v_mov_b32_e32 v151, v193
	v_cvt_pk_fp8_f32 v151, v141, v143
	v_mul_f32_e32 v141, 0x42800000, v165
	v_mul_f32_e32 v143, 0x42800000, v167
	v_med3_f32 v141, v141, s93, v224
	v_med3_f32 v143, v143, s93, v224
	v_mad_i64_i32 v[168:169], s[0:1], s24, v136, v[148:149]
	v_cvt_pk_fp8_f32 v151, v141, v143 op_sel:[0,0,1]
	ds_read2_b32 v[152:153], v137 offset0:32 offset1:40
	ds_read2_b32 v[156:157], v137 offset0:97 offset1:105
	v_lshl_add_u64 v[168:169], v[168:169], 0, v[132:133]
	global_store_dwordx2 v[168:169], v[154:155], off
	v_mad_i64_i32 v[154:155], s[0:1], s24, v138, v[148:149]
	v_lshl_add_u64 v[154:155], v[154:155], 0, v[132:133]
	global_store_dwordx2 v[154:155], v[150:151], off
	ds_read2_b32 v[150:151], v137 offset0:162 offset1:170
	ds_read2_b32 v[158:159], v137 offset0:227 offset1:235
	s_waitcnt lgkmcnt(3)
	v_mul_f32_e32 v141, 0x42800000, v152
	s_waitcnt lgkmcnt(2)
	v_mul_f32_e32 v143, 0x42800000, v156
	v_med3_f32 v141, v141, s93, v224
	v_med3_f32 v143, v143, s93, v224
	v_mov_b32_e32 v154, v193
	ds_read2_b32 v[160:161], v139 offset0:36 offset1:44
	ds_read2_b32 v[162:163], v139 offset0:101 offset1:109
	v_cvt_pk_fp8_f32 v154, v141, v143
	s_waitcnt lgkmcnt(3)
	v_mul_f32_e32 v141, 0x42800000, v150
	s_waitcnt lgkmcnt(2)
	v_mul_f32_e32 v143, 0x42800000, v158
	v_med3_f32 v141, v141, s93, v224
	v_med3_f32 v143, v143, s93, v224
	ds_read2_b32 v[164:165], v139 offset0:166 offset1:174
	ds_read2_b32 v[166:167], v139 offset0:231 offset1:239
	v_cvt_pk_fp8_f32 v154, v141, v143 op_sel:[0,0,1]
	s_waitcnt lgkmcnt(3)
	v_mul_f32_e32 v141, 0x42800000, v160
	s_waitcnt lgkmcnt(2)
	v_mul_f32_e32 v143, 0x42800000, v162
	v_med3_f32 v141, v141, s93, v224
	v_med3_f32 v143, v143, s93, v224
	v_mov_b32_e32 v155, v193
	v_cvt_pk_fp8_f32 v155, v141, v143
	s_waitcnt lgkmcnt(1)
	v_mul_f32_e32 v141, 0x42800000, v164
	s_waitcnt lgkmcnt(0)
	v_mul_f32_e32 v143, 0x42800000, v166
	v_med3_f32 v141, v141, s93, v224
	v_med3_f32 v143, v143, s93, v224
	v_cvt_pk_fp8_f32 v155, v141, v143 op_sel:[0,0,1]
	v_mul_f32_e32 v141, 0x42800000, v153
	v_mul_f32_e32 v143, 0x42800000, v157
	v_med3_f32 v141, v141, s93, v224
	v_med3_f32 v143, v143, s93, v224
	v_mov_b32_e32 v150, v193
	v_cvt_pk_fp8_f32 v150, v141, v143
	v_mul_f32_e32 v141, 0x42800000, v151
	v_mul_f32_e32 v143, 0x42800000, v159
	v_med3_f32 v141, v141, s93, v224
	v_med3_f32 v143, v143, s93, v224
	v_cvt_pk_fp8_f32 v150, v141, v143 op_sel:[0,0,1]
	v_mul_f32_e32 v141, 0x42800000, v161
	v_mul_f32_e32 v143, 0x42800000, v163
	v_med3_f32 v141, v141, s93, v224
	v_med3_f32 v143, v143, s93, v224
	v_mov_b32_e32 v151, v193
	v_cvt_pk_fp8_f32 v151, v141, v143
	v_mul_f32_e32 v141, 0x42800000, v165
	v_mul_f32_e32 v143, 0x42800000, v167
	v_med3_f32 v141, v141, s93, v224
	v_med3_f32 v143, v143, s93, v224
	v_mad_i64_i32 v[168:169], s[0:1], s24, v140, v[148:149]
	v_cvt_pk_fp8_f32 v151, v141, v143 op_sel:[0,0,1]
	ds_read2_b32 v[152:153], v137 offset0:48 offset1:56
	ds_read2_b32 v[156:157], v137 offset0:113 offset1:121
	v_lshl_add_u64 v[168:169], v[168:169], 0, v[132:133]
	global_store_dwordx2 v[168:169], v[154:155], off
	v_mad_i64_i32 v[154:155], s[0:1], s24, v142, v[148:149]
	v_lshl_add_u64 v[154:155], v[154:155], 0, v[132:133]
	global_store_dwordx2 v[154:155], v[150:151], off
	ds_read2_b32 v[150:151], v137 offset0:178 offset1:186
	ds_read2_b32 v[158:159], v137 offset0:243 offset1:251
	s_waitcnt lgkmcnt(3)
	v_mul_f32_e32 v141, 0x42800000, v152
	s_waitcnt lgkmcnt(2)
	v_mul_f32_e32 v143, 0x42800000, v156
	v_med3_f32 v141, v141, s93, v224
	v_med3_f32 v143, v143, s93, v224
	v_mov_b32_e32 v154, v193
	ds_read2_b32 v[160:161], v139 offset0:52 offset1:60
	ds_read2_b32 v[162:163], v139 offset0:117 offset1:125
	v_cvt_pk_fp8_f32 v154, v141, v143
	s_waitcnt lgkmcnt(3)
	v_mul_f32_e32 v141, 0x42800000, v150
	s_waitcnt lgkmcnt(2)
	v_mul_f32_e32 v143, 0x42800000, v158
	v_med3_f32 v141, v141, s93, v224
	v_med3_f32 v143, v143, s93, v224
	ds_read2_b32 v[164:165], v139 offset0:182 offset1:190
	ds_read2_b32 v[166:167], v139 offset0:247 offset1:255
	v_cvt_pk_fp8_f32 v154, v141, v143 op_sel:[0,0,1]
	s_waitcnt lgkmcnt(3)
	v_mul_f32_e32 v141, 0x42800000, v160
	s_waitcnt lgkmcnt(2)
	v_mul_f32_e32 v143, 0x42800000, v162
	v_med3_f32 v141, v141, s93, v224
	v_med3_f32 v143, v143, s93, v224
	v_mov_b32_e32 v155, v193
	v_cvt_pk_fp8_f32 v155, v141, v143
	s_waitcnt lgkmcnt(1)
	v_mul_f32_e32 v139, 0x42800000, v164
	s_waitcnt lgkmcnt(0)
	v_mul_f32_e32 v141, 0x42800000, v166
	v_med3_f32 v139, v139, s93, v224
	v_med3_f32 v141, v141, s93, v224
	v_cvt_pk_fp8_f32 v155, v139, v141 op_sel:[0,0,1]
	v_mul_f32_e32 v139, 0x42800000, v153
	v_mul_f32_e32 v141, 0x42800000, v157
	v_med3_f32 v139, v139, s93, v224
	v_med3_f32 v141, v141, s93, v224
	v_mov_b32_e32 v150, v193
	v_cvt_pk_fp8_f32 v150, v139, v141
	v_mul_f32_e32 v139, 0x42800000, v151
	v_mul_f32_e32 v141, 0x42800000, v159
	v_med3_f32 v139, v139, s93, v224
	v_med3_f32 v141, v141, s93, v224
	v_cvt_pk_fp8_f32 v150, v139, v141 op_sel:[0,0,1]
	v_mul_f32_e32 v139, 0x42800000, v161
	v_mul_f32_e32 v141, 0x42800000, v163
	v_med3_f32 v139, v139, s93, v224
	v_med3_f32 v141, v141, s93, v224
	v_mov_b32_e32 v151, v193
	v_cvt_pk_fp8_f32 v151, v139, v141
	v_mul_f32_e32 v139, 0x42800000, v165
	v_mul_f32_e32 v141, 0x42800000, v167
	v_med3_f32 v139, v139, s93, v224
	v_med3_f32 v141, v141, s93, v224
	v_cvt_pk_fp8_f32 v151, v139, v141 op_sel:[0,0,1]
	v_mad_i64_i32 v[168:169], s[0:1], s24, v144, v[148:149]
	v_mad_i64_i32 v[148:149], s[0:1], s24, v146, v[148:149]
	v_lshl_add_u64 v[168:169], v[168:169], 0, v[132:133]
	v_lshl_add_u64 v[148:149], v[148:149], 0, v[132:133]
	global_store_dwordx2 v[168:169], v[154:155], off
	global_store_dwordx2 v[148:149], v[150:151], off
	s_waitcnt lgkmcnt(0)

; #define LAS __attribute__((address_space(3)))
; #define LDS_WAIT() asm volatile("s_waitcnt lgkmcnt(0)" ::: "memory")
; __device__ __forceinline__ void cvt_load(const CvtDesc& d, float (&t)[64], int lane) {
;     const float* p = d.src + (size_t)(lane >> 4) * d.N + 4 * (lane & 15);
; #pragma unroll
;     for (int i = 0; i < 16; ++i) { const f32x4 v = __builtin_nontemporal_load((const f32x4*)(p + (size_t)(4 * i) * d.N));
;         t[4 * i] = v.x; t[4 * i + 1] = v.y; t[4 * i + 2] = v.z; t[4 * i + 3] = v.w; }
; }
; __device__ __forceinline__ void cvt_finish(const CvtDesc& d, const float (&t)[64], LAS float* scr, int lane) {
;     LAS float* sw = scr + (lane >> 4) * 65 + 4 * (lane & 15);
; #pragma unroll
;     for (int i = 0; i < 16; ++i) { sw[(4 * i) * 65] = t[4 * i]; sw[(4 * i) * 65 + 1] = t[4 * i + 1]; sw[(4 * i) * 65 + 2] = t[4 * i + 2]; sw[(4 * i) * 65 + 3] = t[4 * i + 3]; }
;     LDS_WAIT();
;     const int c = lane & 7;
;     if (d.f8) {
; #pragma unroll
;         for (int j = 0; j < 8; ++j) { const int n = (lane >> 3) + 8 * j; const LAS float* s = scr + (8 * c) * 65 + n;
.LBB0_1339:
	v_mul_u32_u24_e32 v2, s0, v9
	v_lshlrev_b32_e32 v192, 2, v2
	v_lshl_add_u64 v[0:1], v[0:1], 0, v[192:193]
	v_mov_b32_e32 v7, v193
	v_lshl_add_u64 v[0:1], v[0:1], 0, v[6:7]
	s_lshl_b32 s68, s0, 4
	global_load_dwordx4 v[20:23], v[0:1], off nt
	v_lshl_add_u64 v[0:1], v[0:1], 0, s[68:69]
	global_load_dwordx4 v[24:27], v[0:1], off nt
	v_lshl_add_u64 v[0:1], v[0:1], 0, s[68:69]
	global_load_dwordx4 v[28:31], v[0:1], off nt
	v_lshl_add_u64 v[0:1], v[0:1], 0, s[68:69]
	global_load_dwordx4 v[32:35], v[0:1], off nt
	v_lshl_add_u64 v[0:1], v[0:1], 0, s[68:69]
	global_load_dwordx4 v[36:39], v[0:1], off nt
	v_lshl_add_u64 v[0:1], v[0:1], 0, s[68:69]
	global_load_dwordx4 v[40:43], v[0:1], off nt
	v_lshl_add_u64 v[0:1], v[0:1], 0, s[68:69]
	global_load_dwordx4 v[44:47], v[0:1], off nt
	v_lshl_add_u64 v[0:1], v[0:1], 0, s[68:69]
	global_load_dwordx4 v[48:51], v[0:1], off nt
	v_lshl_add_u64 v[0:1], v[0:1], 0, s[68:69]
	global_load_dwordx4 v[52:55], v[0:1], off nt
	v_lshl_add_u64 v[0:1], v[0:1], 0, s[68:69]
	global_load_dwordx4 v[56:59], v[0:1], off nt
	v_lshl_add_u64 v[0:1], v[0:1], 0, s[68:69]
	global_load_dwordx4 v[60:63], v[0:1], off nt
	v_lshl_add_u64 v[0:1], v[0:1], 0, s[68:69]
	global_load_dwordx4 v[64:67], v[0:1], off nt
	v_lshl_add_u64 v[0:1], v[0:1], 0, s[68:69]
	global_load_dwordx4 v[68:71], v[0:1], off nt
	v_lshl_add_u64 v[0:1], v[0:1], 0, s[68:69]
	global_load_dwordx4 v[72:75], v[0:1], off nt
	v_lshl_add_u64 v[0:1], v[0:1], 0, s[68:69]
	global_load_dwordx4 v[76:79], v[0:1], off nt
	v_lshl_add_u64 v[0:1], v[0:1], 0, s[68:69]
	global_load_dwordx4 v[0:3], v[0:1], off nt
	v_add_u32_e32 v7, 0x410, v10
	s_waitcnt vmcnt(0)
	ds_write2_b32 v10, v20, v21 offset1:1
	ds_write2_b32 v10, v22, v23 offset0:2 offset1:3
	v_mov_b32_e32 v22, v193
	ds_write2_b32 v7, v24, v25 offset1:1
	v_add_u32_e32 v7, 0x418, v10
	ds_write2_b32 v7, v26, v27 offset1:1
	v_add_u32_e32 v7, 0x820, v10
	ds_write2_b32 v7, v28, v29 offset1:1
	v_add_u32_e32 v7, 0x828, v10
	ds_write2_b32 v7, v30, v31 offset1:1
	v_add_u32_e32 v7, 0xc30, v10
	ds_write2_b32 v7, v32, v33 offset1:1
	v_add_u32_e32 v7, 0xc38, v10
	ds_write2_b32 v7, v34, v35 offset1:1
	v_add_u32_e32 v7, 0x1040, v10
	ds_write2_b32 v7, v36, v37 offset1:1
	v_add_u32_e32 v7, 0x1048, v10
	ds_write2_b32 v7, v38, v39 offset1:1
	v_add_u32_e32 v7, 0x1450, v10
	ds_write2_b32 v7, v40, v41 offset1:1
	v_add_u32_e32 v7, 0x1458, v10
	ds_write2_b32 v7, v42, v43 offset1:1
	v_add_u32_e32 v7, 0x1860, v10
	ds_write2_b32 v7, v44, v45 offset1:1
	v_add_u32_e32 v7, 0x1868, v10
	ds_write2_b32 v7, v46, v47 offset1:1
	v_add_u32_e32 v7, 0x1c70, v10
	ds_write2_b32 v7, v48, v49 offset1:1
	v_add_u32_e32 v7, 0x1c78, v10
	ds_write2_b32 v7, v50, v51 offset1:1
	v_add_u32_e32 v7, 0x2080, v10
	ds_write2_b32 v7, v52, v53 offset1:1
	v_add_u32_e32 v7, 0x2088, v10
	ds_write2_b32 v7, v54, v55 offset1:1
	v_add_u32_e32 v7, 0x2490, v10
	ds_write2_b32 v7, v56, v57 offset1:1
	v_add_u32_e32 v7, 0x2498, v10
	ds_write2_b32 v7, v58, v59 offset1:1
	v_add_u32_e32 v7, 0x28a0, v10
	ds_write2_b32 v7, v60, v61 offset1:1
	v_add_u32_e32 v7, 0x28a8, v10
	ds_write2_b32 v7, v62, v63 offset1:1
	v_add_u32_e32 v7, 0x2cb0, v10
	ds_write2_b32 v7, v64, v65 offset1:1
	v_add_u32_e32 v7, 0x2cb8, v10
	ds_write2_b32 v7, v66, v67 offset1:1
	v_add_u32_e32 v7, 0x30c0, v10
	ds_write2_b32 v7, v68, v69 offset1:1
	v_add_u32_e32 v7, 0x30c8, v10
	ds_write2_b32 v7, v70, v71 offset1:1
	v_add_u32_e32 v7, 0x34d0, v10
	ds_write2_b32 v7, v72, v73 offset1:1
	v_add_u32_e32 v7, 0x34d8, v10
	ds_write2_b32 v7, v74, v75 offset1:1
	v_add_u32_e32 v7, 0x38e0, v10
	ds_write2_b32 v7, v76, v77 offset1:1
	v_add_u32_e32 v7, 0x38e8, v10
	ds_write2_b32 v7, v78, v79 offset1:1
	v_add_u32_e32 v7, 0x3cf0, v10
	ds_write2_b32 v7, v0, v1 offset1:1
	v_add_u32_e32 v0, 0x3cf8, v10
	ds_write2_b32 v0, v2, v3 offset1:1
	s_waitcnt lgkmcnt(0)
	ds_read2_b32 v[2:3], v12 offset1:8
	ds_read2_b32 v[20:21], v12 offset0:65 offset1:73
	ds_read2_b32 v[24:25], v12 offset0:130 offset1:138
	ds_read2_b32 v[26:27], v12 offset0:195 offset1:203
	v_mov_b32_e32 v23, v193
	s_waitcnt lgkmcnt(3)
	v_mul_f32_e32 v0, 0x42800000, v2
	s_waitcnt lgkmcnt(2)
	v_mul_f32_e32 v1, 0x42800000, v20
	v_add_u32_e32 v2, 0x400, v12
	v_med3_f32 v0, v0, s93, v224
	v_med3_f32 v1, v1, s93, v224
	ds_read2_b32 v[28:29], v2 offset0:4 offset1:12
	ds_read2_b32 v[30:31], v2 offset0:69 offset1:77
	v_cvt_pk_fp8_f32 v22, v0, v1
	v_mul_f32_e32 v3, 0x42800000, v3
	v_mul_f32_e32 v7, 0x42800000, v21
	v_med3_f32 v3, v3, s93, v224
	v_med3_f32 v7, v7, s93, v224
	v_mov_b32_e32 v20, v193
	s_waitcnt lgkmcnt(3)
	v_mul_f32_e32 v0, 0x42800000, v24
	s_waitcnt lgkmcnt(2)
	v_mul_f32_e32 v1, 0x42800000, v26
	v_cvt_pk_fp8_f32 v20, v3, v7
	v_med3_f32 v0, v0, s93, v224
	v_med3_f32 v1, v1, s93, v224
	ds_read2_b32 v[32:33], v2 offset0:134 offset1:142
	ds_read2_b32 v[34:35], v2 offset0:199 offset1:207
	v_cvt_pk_fp8_f32 v22, v0, v1 op_sel:[0,0,1]
	s_waitcnt lgkmcnt(3)
	v_mul_f32_e32 v0, 0x42800000, v28
	s_waitcnt lgkmcnt(2)
	v_mul_f32_e32 v1, 0x42800000, v30
	v_mul_f32_e32 v3, 0x42800000, v25
	v_mul_f32_e32 v7, 0x42800000, v27
	v_med3_f32 v0, v0, s93, v224
	v_med3_f32 v1, v1, s93, v224
	v_med3_f32 v3, v3, s93, v224
	v_med3_f32 v7, v7, s93, v224
	v_cvt_pk_fp8_f32 v23, v0, v1
	v_cvt_pk_fp8_f32 v20, v3, v7 op_sel:[0,0,1]
	v_mul_f32_e32 v3, 0x42800000, v29
	v_mul_f32_e32 v7, 0x42800000, v31
	v_med3_f32 v3, v3, s93, v224
	v_med3_f32 v7, v7, s93, v224
	v_mov_b32_e32 v21, v193
	s_waitcnt lgkmcnt(1)
	v_mul_f32_e32 v0, 0x42800000, v32
	s_waitcnt lgkmcnt(0)
; #define LAS __attribute__((address_space(3)))
; __device__ __forceinline__ float clamp8(float x) { return __builtin_amdgcn_fmed3f(x, -448.f, 448.f); }
; __device__ __forceinline__ void cvt_finish(const CvtDesc& d, const float (&t)[64], LAS float* scr, int lane) {
;     ...
;     if (d.f8) {
; #pragma unroll
;         for (int j = 0; j < 8; ++j) { const int n = (lane >> 3) + 8 * j; const LAS float* s = scr + (8 * c) * 65 + n;
;             int a = __builtin_amdgcn_cvt_pk_fp8_f32(clamp8(s[0 * 65] * W8_SCALE), clamp8(s[1 * 65] * W8_SCALE), 0, false); a = __builtin_amdgcn_cvt_pk_fp8_f32(clamp8(s[2 * 65] * W8_SCALE), clamp8(s[3 * 65] * W8_SCALE), a, true);
;             int b = __builtin_amdgcn_cvt_pk_fp8_f32(clamp8(s[4 * 65] * W8_SCALE), clamp8(s[5 * 65] * W8_SCALE), 0, false); b = __builtin_amdgcn_cvt_pk_fp8_f32(clamp8(s[6 * 65] * W8_SCALE), clamp8(s[7 * 65] * W8_SCALE), b, true);
;             __builtin_nontemporal_store((u32x2){(unsigned)a, (unsigned)b}, (u32x2*)(d.dst + (size_t)n * d.dKB + 8 * c)); }
	v_mul_f32_e32 v1, 0x42800000, v34
	v_cvt_pk_fp8_f32 v21, v3, v7
	v_med3_f32 v0, v0, s93, v224
	v_med3_f32 v1, v1, s93, v224
	v_cvt_pk_fp8_f32 v23, v0, v1 op_sel:[0,0,1]
	v_mul_f32_e32 v3, 0x42800000, v33
	v_mul_f32_e32 v7, 0x42800000, v35
	v_mov_b64_e32 v[0:1], s[16:17]
	v_med3_f32 v3, v3, s93, v224
	v_med3_f32 v7, v7, s93, v224
	v_mad_u64_u32 v[36:37], s[0:1], s14, v11, v[0:1]
	v_cvt_pk_fp8_f32 v21, v3, v7 op_sel:[0,0,1]
	v_lshl_add_u64 v[36:37], v[36:37], 0, v[4:5]
	global_store_dwordx2 v[36:37], v[22:23], off
	v_mad_u64_u32 v[22:23], s[0:1], s14, v13, v[0:1]
	v_lshl_add_u64 v[22:23], v[22:23], 0, v[4:5]
	global_store_dwordx2 v[22:23], v[20:21], off
	ds_read2_b32 v[20:21], v12 offset0:16 offset1:24
	ds_read2_b32 v[22:23], v12 offset0:81 offset1:89
	ds_read2_b32 v[26:27], v12 offset0:146 offset1:154
	ds_read2_b32 v[28:29], v12 offset0:211 offset1:219
	v_mov_b32_e32 v24, v193
	s_waitcnt lgkmcnt(3)
	v_mul_f32_e32 v3, 0x42800000, v20
	s_waitcnt lgkmcnt(2)
	v_mul_f32_e32 v7, 0x42800000, v22
	v_med3_f32 v3, v3, s93, v224
	v_med3_f32 v7, v7, s93, v224
	ds_read2_b32 v[30:31], v2 offset0:20 offset1:28
	ds_read2_b32 v[32:33], v2 offset0:85 offset1:93
	v_cvt_pk_fp8_f32 v24, v3, v7
	s_waitcnt lgkmcnt(3)
	v_mul_f32_e32 v3, 0x42800000, v26
	s_waitcnt lgkmcnt(2)
	v_mul_f32_e32 v7, 0x42800000, v28
	v_med3_f32 v3, v3, s93, v224
	v_med3_f32 v7, v7, s93, v224
	ds_read2_b32 v[34:35], v2 offset0:150 offset1:158
	ds_read2_b32 v[36:37], v2 offset0:215 offset1:223
	v_cvt_pk_fp8_f32 v24, v3, v7 op_sel:[0,0,1]
	s_waitcnt lgkmcnt(3)
	v_mul_f32_e32 v3, 0x42800000, v30
	s_waitcnt lgkmcnt(2)
	v_mul_f32_e32 v7, 0x42800000, v32
	v_med3_f32 v3, v3, s93, v224
	v_med3_f32 v7, v7, s93, v224
	v_mov_b32_e32 v25, v193
	v_cvt_pk_fp8_f32 v25, v3, v7
	s_waitcnt lgkmcnt(1)
	v_mul_f32_e32 v3, 0x42800000, v34
	s_waitcnt lgkmcnt(0)
	v_mul_f32_e32 v7, 0x42800000, v36
	v_med3_f32 v3, v3, s93, v224
	v_med3_f32 v7, v7, s93, v224
	v_cvt_pk_fp8_f32 v25, v3, v7 op_sel:[0,0,1]
	v_mul_f32_e32 v3, 0x42800000, v21
	v_mul_f32_e32 v7, 0x42800000, v23
	v_med3_f32 v3, v3, s93, v224
	v_med3_f32 v7, v7, s93, v224
	v_mov_b32_e32 v20, v193
	v_cvt_pk_fp8_f32 v20, v3, v7
	v_mul_f32_e32 v3, 0x42800000, v27
	v_mul_f32_e32 v7, 0x42800000, v29
	v_med3_f32 v3, v3, s93, v224
	v_med3_f32 v7, v7, s93, v224
	v_cvt_pk_fp8_f32 v20, v3, v7 op_sel:[0,0,1]
	v_mul_f32_e32 v3, 0x42800000, v31
	v_mul_f32_e32 v7, 0x42800000, v33
	v_med3_f32 v3, v3, s93, v224
	v_med3_f32 v7, v7, s93, v224
	v_mov_b32_e32 v21, v193
	v_cvt_pk_fp8_f32 v21, v3, v7
	v_mul_f32_e32 v3, 0x42800000, v35
	v_mul_f32_e32 v7, 0x42800000, v37
	v_med3_f32 v3, v3, s93, v224
	v_med3_f32 v7, v7, s93, v224
	v_cvt_pk_fp8_f32 v21, v3, v7 op_sel:[0,0,1]
	v_mad_u64_u32 v[38:39], s[0:1], s14, v14, v[0:1]
	v_mad_u64_u32 v[22:23], s[0:1], s14, v15, v[0:1]
	v_lshl_add_u64 v[38:39], v[38:39], 0, v[4:5]
	v_lshl_add_u64 v[22:23], v[22:23], 0, v[4:5]
	global_store_dwordx2 v[38:39], v[24:25], off
	global_store_dwordx2 v[22:23], v[20:21], off
	ds_read2_b32 v[20:21], v12 offset0:32 offset1:40
	ds_read2_b32 v[22:23], v12 offset0:97 offset1:105
	ds_read2_b32 v[26:27], v12 offset0:162 offset1:170
	ds_read2_b32 v[28:29], v12 offset0:227 offset1:235
	v_mov_b32_e32 v24, v193
	s_waitcnt lgkmcnt(3)
	v_mul_f32_e32 v3, 0x42800000, v20
	s_waitcnt lgkmcnt(2)
	v_mul_f32_e32 v7, 0x42800000, v22
	v_med3_f32 v3, v3, s93, v224
	v_med3_f32 v7, v7, s93, v224
	ds_read2_b32 v[30:31], v2 offset0:36 offset1:44
	ds_read2_b32 v[32:33], v2 offset0:101 offset1:109
	v_cvt_pk_fp8_f32 v24, v3, v7
	s_waitcnt lgkmcnt(3)
	v_mul_f32_e32 v3, 0x42800000, v26
	s_waitcnt lgkmcnt(2)
	v_mul_f32_e32 v7, 0x42800000, v28
	v_med3_f32 v3, v3, s93, v224
	v_med3_f32 v7, v7, s93, v224
	ds_read2_b32 v[34:35], v2 offset0:166 offset1:174
	ds_read2_b32 v[36:37], v2 offset0:231 offset1:239
	v_cvt_pk_fp8_f32 v24, v3, v7 op_sel:[0,0,1]
	s_waitcnt lgkmcnt(3)
; #define LAS __attribute__((address_space(3)))
; __device__ __forceinline__ float clamp8(float x) { return __builtin_amdgcn_fmed3f(x, -448.f, 448.f); }
; __device__ __forceinline__ void cvt_finish(const CvtDesc& d, const float (&t)[64], LAS float* scr, int lane) {
;     ...
;     if (d.f8) {
; #pragma unroll
;         for (int j = 0; j < 8; ++j) { const int n = (lane >> 3) + 8 * j; const LAS float* s = scr + (8 * c) * 65 + n;
;             int a = __builtin_amdgcn_cvt_pk_fp8_f32(clamp8(s[0 * 65] * W8_SCALE), clamp8(s[1 * 65] * W8_SCALE), 0, false); a = __builtin_amdgcn_cvt_pk_fp8_f32(clamp8(s[2 * 65] * W8_SCALE), clamp8(s[3 * 65] * W8_SCALE), a, true);
;             int b = __builtin_amdgcn_cvt_pk_fp8_f32(clamp8(s[4 * 65] * W8_SCALE), clamp8(s[5 * 65] * W8_SCALE), 0, false); b = __builtin_amdgcn_cvt_pk_fp8_f32(clamp8(s[6 * 65] * W8_SCALE), clamp8(s[7 * 65] * W8_SCALE), b, true);
;             __builtin_nontemporal_store((u32x2){(unsigned)a, (unsigned)b}, (u32x2*)(d.dst + (size_t)n * d.dKB + 8 * c)); }
	v_mul_f32_e32 v3, 0x42800000, v30
	s_waitcnt lgkmcnt(2)
	v_mul_f32_e32 v7, 0x42800000, v32
	v_med3_f32 v3, v3, s93, v224
	v_med3_f32 v7, v7, s93, v224
	v_mov_b32_e32 v25, v193
	v_cvt_pk_fp8_f32 v25, v3, v7
	s_waitcnt lgkmcnt(1)
	v_mul_f32_e32 v3, 0x42800000, v34
	s_waitcnt lgkmcnt(0)
	v_mul_f32_e32 v7, 0x42800000, v36
	v_med3_f32 v3, v3, s93, v224
	v_med3_f32 v7, v7, s93, v224
	v_cvt_pk_fp8_f32 v25, v3, v7 op_sel:[0,0,1]
	v_mul_f32_e32 v3, 0x42800000, v21
	v_mul_f32_e32 v7, 0x42800000, v23
	v_med3_f32 v3, v3, s93, v224
	v_med3_f32 v7, v7, s93, v224
	v_mov_b32_e32 v20, v193
	v_cvt_pk_fp8_f32 v20, v3, v7
	v_mul_f32_e32 v3, 0x42800000, v27
	v_mul_f32_e32 v7, 0x42800000, v29
	v_med3_f32 v3, v3, s93, v224
	v_med3_f32 v7, v7, s93, v224
	v_cvt_pk_fp8_f32 v20, v3, v7 op_sel:[0,0,1]
	v_mul_f32_e32 v3, 0x42800000, v31
	v_mul_f32_e32 v7, 0x42800000, v33
	v_med3_f32 v3, v3, s93, v224
	v_med3_f32 v7, v7, s93, v224
	v_mov_b32_e32 v21, v193
	v_cvt_pk_fp8_f32 v21, v3, v7
	v_mul_f32_e32 v3, 0x42800000, v35
	v_mul_f32_e32 v7, 0x42800000, v37
	v_med3_f32 v3, v3, s93, v224
	v_med3_f32 v7, v7, s93, v224
	v_cvt_pk_fp8_f32 v21, v3, v7 op_sel:[0,0,1]
	v_mad_u64_u32 v[38:39], s[0:1], s14, v16, v[0:1]
	v_mad_u64_u32 v[22:23], s[0:1], s14, v17, v[0:1]
	v_lshl_add_u64 v[38:39], v[38:39], 0, v[4:5]
	v_lshl_add_u64 v[22:23], v[22:23], 0, v[4:5]
	global_store_dwordx2 v[38:39], v[24:25], off
	global_store_dwordx2 v[22:23], v[20:21], off
	ds_read2_b32 v[20:21], v12 offset0:48 offset1:56
	ds_read2_b32 v[22:23], v12 offset0:113 offset1:121
	ds_read2_b32 v[26:27], v12 offset0:178 offset1:186
	ds_read2_b32 v[28:29], v12 offset0:243 offset1:251
	v_mov_b32_e32 v24, v193
	s_waitcnt lgkmcnt(3)
	v_mul_f32_e32 v3, 0x42800000, v20
	s_waitcnt lgkmcnt(2)
	v_mul_f32_e32 v7, 0x42800000, v22
	v_med3_f32 v3, v3, s93, v224
	v_med3_f32 v7, v7, s93, v224
	ds_read2_b32 v[30:31], v2 offset0:52 offset1:60
	ds_read2_b32 v[32:33], v2 offset0:117 offset1:125
	v_cvt_pk_fp8_f32 v24, v3, v7
	ds_read2_b32 v[34:35], v2 offset0:182 offset1:190
	s_waitcnt lgkmcnt(4)
	v_mul_f32_e32 v3, 0x42800000, v26
	s_waitcnt lgkmcnt(3)
	v_mul_f32_e32 v7, 0x42800000, v28
	v_med3_f32 v3, v3, s93, v224
	v_med3_f32 v7, v7, s93, v224
	v_cvt_pk_fp8_f32 v24, v3, v7 op_sel:[0,0,1]
	s_waitcnt lgkmcnt(2)
	v_mul_f32_e32 v3, 0x42800000, v30
	s_waitcnt lgkmcnt(1)
	v_mul_f32_e32 v7, 0x42800000, v32
	v_med3_f32 v3, v3, s93, v224
	v_med3_f32 v7, v7, s93, v224
	v_mov_b32_e32 v25, v193
	v_cvt_pk_fp8_f32 v25, v3, v7
	s_waitcnt lgkmcnt(0)
	v_mul_f32_e32 v3, 0x42800000, v34
	v_med3_f32 v7, v3, s93, v224
	ds_read2_b32 v[2:3], v2 offset0:247 offset1:255
	v_mov_b32_e32 v20, v193
	v_mad_u64_u32 v[36:37], s[0:1], s14, v18, v[0:1]
	v_mad_u64_u32 v[0:1], s[0:1], s14, v19, v[0:1]
	s_waitcnt lgkmcnt(0)
	v_mul_f32_e32 v2, 0x42800000, v2
	v_med3_f32 v2, v2, s93, v224
	v_cvt_pk_fp8_f32 v25, v7, v2 op_sel:[0,0,1]
	v_mul_f32_e32 v2, 0x42800000, v21
	v_mul_f32_e32 v7, 0x42800000, v23
	v_med3_f32 v2, v2, s93, v224
	v_med3_f32 v7, v7, s93, v224
	v_cvt_pk_fp8_f32 v20, v2, v7
	v_mul_f32_e32 v2, 0x42800000, v27
	v_mul_f32_e32 v7, 0x42800000, v29
	v_med3_f32 v2, v2, s93, v224
	v_med3_f32 v7, v7, s93, v224
	v_cvt_pk_fp8_f32 v20, v2, v7 op_sel:[0,0,1]
	v_mul_f32_e32 v2, 0x42800000, v31
	v_mul_f32_e32 v7, 0x42800000, v33
	v_med3_f32 v2, v2, s93, v224
	v_med3_f32 v7, v7, s93, v224
	v_mov_b32_e32 v21, v193
	v_cvt_pk_fp8_f32 v21, v2, v7
	v_mul_f32_e32 v2, 0x42800000, v35
	v_mul_f32_e32 v3, 0x42800000, v3
	v_med3_f32 v2, v2, s93, v224
	v_med3_f32 v3, v3, s93, v224
	v_cvt_pk_fp8_f32 v21, v2, v3 op_sel:[0,0,1]
	v_lshl_add_u64 v[36:37], v[36:37], 0, v[4:5]
	v_lshl_add_u64 v[0:1], v[0:1], 0, v[4:5]
	global_store_dwordx2 v[36:37], v[24:25], off
	global_store_dwordx2 v[0:1], v[20:21], off
	s_waitcnt lgkmcnt(0)
